# all s_setprio removed from GEMM K-loops (VMEM-issue-bound loops: loader wave no longer deprioritised)
# speedup vs baseline: 1.0096x; 1.0017x over previous
.LBB0_261:
	ds_read_b128 v[144:147], v141
	ds_read_b128 v[148:151], v141 offset:1024
	ds_read_b128 v[152:155], v141 offset:2048
	ds_read_b128 v[156:159], v141 offset:3072
	ds_read_b128 v[160:163], v142
	ds_read_b128 v[164:167], v142 offset:1024
	ds_read_b128 v[168:171], v142 offset:2048
	ds_read_b128 v[172:175], v142 offset:3072
	s_add_i32 s0, s67, s10
	s_add_u32 s0, s4, s0
	s_addc_u32 s1, s5, 0
	s_add_i32 m0, s22, 0xc000
	s_add_i32 s30, s22, 0xe000
	s_add_i32 s31, s10, 0xfff80080
	s_cmp_eq_u32 s18, 28
	s_cselect_b32 s19, s45, s67
	s_cselect_b32 s68, s44, s66
	v_lshl_add_u64 v[208:209], s[0:1], 0, v[128:129]
	ds_read_b128 v[176:179], v143
	ds_read_b128 v[180:183], v143 offset:1024
	ds_read_b128 v[184:187], v143 offset:2048
	ds_read_b128 v[188:191], v143 offset:3072
	ds_read_b128 v[192:195], v143 offset:4096
	ds_read_b128 v[196:199], v143 offset:5120
	ds_read_b128 v[200:203], v143 offset:6144
	ds_read_b128 v[204:207], v143 offset:7168
	global_load_lds_dwordx4 v[208:209], off
	v_lshl_add_u64 v[208:209], s[0:1], 0, v[130:131]
	s_mov_b32 m0, s30
	s_nop 0
	global_load_lds_dwordx4 v[208:209], off
	s_waitcnt vmcnt(8)
	s_waitcnt lgkmcnt(0)
	s_barrier
	s_waitcnt lgkmcnt(0)
	v_mfma_f32_16x16x32_bf16 v[124:127], v[144:147], v[176:179], v[124:127]
	v_mfma_f32_16x16x32_bf16 v[120:123], v[152:155], v[176:179], v[120:123]
	v_mfma_f32_16x16x32_bf16 v[116:119], v[144:147], v[184:187], v[116:119]
	v_mfma_f32_16x16x32_bf16 v[112:115], v[152:155], v[184:187], v[112:115]
	v_mfma_f32_16x16x32_bf16 v[108:111], v[144:147], v[192:195], v[108:111]
	v_mfma_f32_16x16x32_bf16 v[100:103], v[152:155], v[192:195], v[100:103]
	v_mfma_f32_16x16x32_bf16 v[92:95], v[144:147], v[200:203], v[92:95]
	v_mfma_f32_16x16x32_bf16 v[84:87], v[152:155], v[200:203], v[84:87]
	v_mfma_f32_16x16x32_bf16 v[124:127], v[148:151], v[180:183], v[124:127]
	v_mfma_f32_16x16x32_bf16 v[120:123], v[156:159], v[180:183], v[120:123]
	v_mfma_f32_16x16x32_bf16 v[116:119], v[148:151], v[188:191], v[116:119]
	v_mfma_f32_16x16x32_bf16 v[112:115], v[156:159], v[188:191], v[112:115]
	v_mfma_f32_16x16x32_bf16 v[108:111], v[148:151], v[196:199], v[108:111]
	v_mfma_f32_16x16x32_bf16 v[100:103], v[156:159], v[196:199], v[100:103]
	v_mfma_f32_16x16x32_bf16 v[92:95], v[148:151], v[204:207], v[92:95]
	v_mfma_f32_16x16x32_bf16 v[84:87], v[156:159], v[204:207], v[84:87]
	v_mfma_f32_16x16x32_bf16 v[104:107], v[160:163], v[176:179], v[104:107]
	v_mfma_f32_16x16x32_bf16 v[96:99], v[168:171], v[176:179], v[96:99]
	v_mfma_f32_16x16x32_bf16 v[88:91], v[160:163], v[184:187], v[88:91]
	v_mfma_f32_16x16x32_bf16 v[80:83], v[168:171], v[184:187], v[80:83]
	v_mfma_f32_16x16x32_bf16 v[76:79], v[160:163], v[192:195], v[76:79]
	v_mfma_f32_16x16x32_bf16 v[72:75], v[168:171], v[192:195], v[72:75]
	v_mfma_f32_16x16x32_bf16 v[68:71], v[160:163], v[200:203], v[68:71]
	v_mfma_f32_16x16x32_bf16 v[64:67], v[168:171], v[200:203], v[64:67]
	v_mfma_f32_16x16x32_bf16 v[104:107], v[164:167], v[180:183], v[104:107]
	v_mfma_f32_16x16x32_bf16 v[96:99], v[172:175], v[180:183], v[96:99]
	v_mfma_f32_16x16x32_bf16 v[88:91], v[164:167], v[188:191], v[88:91]
	v_mfma_f32_16x16x32_bf16 v[80:83], v[172:175], v[188:191], v[80:83]
	v_mfma_f32_16x16x32_bf16 v[76:79], v[164:167], v[196:199], v[76:79]
	v_mfma_f32_16x16x32_bf16 v[72:75], v[172:175], v[196:199], v[72:75]
	v_mfma_f32_16x16x32_bf16 v[68:71], v[164:167], v[204:207], v[68:71]
	v_mfma_f32_16x16x32_bf16 v[64:67], v[172:175], v[204:207], v[64:67]
	s_barrier
	s_cselect_b32 s30, 0, s31
	s_add_i32 s0, s30, s68
	s_ashr_i32 s1, s0, 31
	s_add_u32 s0, s6, s0
	s_addc_u32 s1, s7, s1
	s_add_i32 s31, s38, s27
	v_lshl_add_u64 v[208:209], s[0:1], 0, v[128:129]
	s_mov_b32 m0, s31
	ds_read_b128 v[176:179], v143 offset:16384
	ds_read_b128 v[180:183], v143 offset:17408
	ds_read_b128 v[184:187], v143 offset:18432
	ds_read_b128 v[188:191], v143 offset:19456
	ds_read_b128 v[192:195], v143 offset:20480
	ds_read_b128 v[196:199], v143 offset:21504
	ds_read_b128 v[200:203], v143 offset:22528
	ds_read_b128 v[204:207], v143 offset:23552
	global_load_lds_dwordx4 v[208:209], off
	s_add_i32 m0, s31, 0x2000
	s_add_i32 s31, s68, 0x80000
	v_lshl_add_u64 v[208:209], s[0:1], 0, v[130:131]
	s_add_i32 s0, s31, s30
	s_ashr_i32 s1, s0, 31
	s_add_u32 s0, s6, s0
	s_addc_u32 s1, s7, s1
	s_add_i32 s69, s39, s27
	global_load_lds_dwordx4 v[208:209], off
	v_lshl_add_u64 v[208:209], s[0:1], 0, v[128:129]
	s_mov_b32 m0, s69
	s_nop 0
	global_load_lds_dwordx4 v[208:209], off
	s_add_i32 m0, s69, 0x2000
	s_add_i32 s69, s30, s19
	v_lshl_add_u64 v[208:209], s[0:1], 0, v[130:131]
	s_add_u32 s0, s4, s69
	s_addc_u32 s1, s5, 0
	global_load_lds_dwordx4 v[208:209], off
	v_lshl_add_u64 v[208:209], s[0:1], 0, v[128:129]
	s_mov_b32 m0, s22
	s_nop 0
	global_load_lds_dwordx4 v[208:209], off
	v_lshl_add_u64 v[208:209], s[0:1], 0, v[130:131]
	s_mov_b32 m0, s23
	s_nop 0
	global_load_lds_dwordx4 v[208:209], off
	s_waitcnt vmcnt(8)
	s_waitcnt lgkmcnt(0)
	s_barrier
	s_waitcnt lgkmcnt(0)
	v_mfma_f32_16x16x32_bf16 v[60:63], v[144:147], v[176:179], v[60:63]
	v_mfma_f32_16x16x32_bf16 v[56:59], v[152:155], v[176:179], v[56:59]
	v_mfma_f32_16x16x32_bf16 v[52:55], v[144:147], v[184:187], v[52:55]
	v_mfma_f32_16x16x32_bf16 v[48:51], v[152:155], v[184:187], v[48:51]
	v_mfma_f32_16x16x32_bf16 v[44:47], v[144:147], v[192:195], v[44:47]
	v_mfma_f32_16x16x32_bf16 v[36:39], v[152:155], v[192:195], v[36:39]
	v_mfma_f32_16x16x32_bf16 v[28:31], v[144:147], v[200:203], v[28:31]
	v_mfma_f32_16x16x32_bf16 v[20:23], v[152:155], v[200:203], v[20:23]
	v_mfma_f32_16x16x32_bf16 v[60:63], v[148:151], v[180:183], v[60:63]
	v_mfma_f32_16x16x32_bf16 v[56:59], v[156:159], v[180:183], v[56:59]
	v_mfma_f32_16x16x32_bf16 v[52:55], v[148:151], v[188:191], v[52:55]
	v_mfma_f32_16x16x32_bf16 v[48:51], v[156:159], v[188:191], v[48:51]
	v_mfma_f32_16x16x32_bf16 v[44:47], v[148:151], v[196:199], v[44:47]
	v_mfma_f32_16x16x32_bf16 v[36:39], v[156:159], v[196:199], v[36:39]
	v_mfma_f32_16x16x32_bf16 v[28:31], v[148:151], v[204:207], v[28:31]
	v_mfma_f32_16x16x32_bf16 v[20:23], v[156:159], v[204:207], v[20:23]
	v_mfma_f32_16x16x32_bf16 v[40:43], v[160:163], v[176:179], v[40:43]
	v_mfma_f32_16x16x32_bf16 v[32:35], v[168:171], v[176:179], v[32:35]
	v_mfma_f32_16x16x32_bf16 v[24:27], v[160:163], v[184:187], v[24:27]
	v_mfma_f32_16x16x32_bf16 v[16:19], v[168:171], v[184:187], v[16:19]
	v_mfma_f32_16x16x32_bf16 v[12:15], v[160:163], v[192:195], v[12:15]
	v_mfma_f32_16x16x32_bf16 v[8:11], v[168:171], v[192:195], v[8:11]
	v_mfma_f32_16x16x32_bf16 v[4:7], v[160:163], v[200:203], v[4:7]
	v_mfma_f32_16x16x32_bf16 v[0:3], v[168:171], v[200:203], v[0:3]
	v_mfma_f32_16x16x32_bf16 v[40:43], v[164:167], v[180:183], v[40:43]
	v_mfma_f32_16x16x32_bf16 v[32:35], v[172:175], v[180:183], v[32:35]
	v_mfma_f32_16x16x32_bf16 v[24:27], v[164:167], v[188:191], v[24:27]
	v_mfma_f32_16x16x32_bf16 v[16:19], v[172:175], v[188:191], v[16:19]
	v_mfma_f32_16x16x32_bf16 v[12:15], v[164:167], v[196:199], v[12:15]
	v_mfma_f32_16x16x32_bf16 v[8:11], v[172:175], v[196:199], v[8:11]
	v_mfma_f32_16x16x32_bf16 v[4:7], v[164:167], v[204:207], v[4:7]
	v_mfma_f32_16x16x32_bf16 v[0:3], v[172:175], v[204:207], v[0:3]
	s_barrier
	s_add_i32 s70, 0, 0x18000
	s_add_i32 s71, 0, 0x1c000
	v_add_u32_e32 v156, s70, v140
	v_add_u32_e32 v172, s71, v140
	ds_read_b128 v[144:147], v156
	ds_read_b128 v[148:151], v156 offset:1024
	ds_read_b128 v[152:155], v156 offset:2048
	ds_read_b128 v[156:159], v156 offset:3072
	ds_read_b128 v[160:163], v172
	ds_read_b128 v[164:167], v172 offset:1024
	ds_read_b128 v[168:171], v172 offset:2048
	ds_read_b128 v[172:175], v172 offset:3072
	s_add_i32 s69, s69, 0x80000
	s_add_u32 s0, s4, s69
	s_addc_u32 s1, s5, 0
	s_mov_b32 m0, s24
	v_lshl_add_u64 v[208:209], s[0:1], 0, v[128:129]
	ds_read_b128 v[176:179], v143 offset:32768
	ds_read_b128 v[180:183], v143 offset:33792
	ds_read_b128 v[184:187], v143 offset:34816
	ds_read_b128 v[188:191], v143 offset:35840
	ds_read_b128 v[192:195], v143 offset:36864
	ds_read_b128 v[196:199], v143 offset:37888
	ds_read_b128 v[200:203], v143 offset:38912
	ds_read_b128 v[204:207], v143 offset:39936
	global_load_lds_dwordx4 v[208:209], off
	v_lshl_add_u64 v[208:209], s[0:1], 0, v[130:131]
	s_mov_b32 m0, s25
	s_nop 0
	global_load_lds_dwordx4 v[208:209], off
	s_waitcnt vmcnt(8)
	s_waitcnt lgkmcnt(0)
	s_barrier
	s_waitcnt lgkmcnt(0)
	v_mfma_f32_16x16x32_bf16 v[124:127], v[144:147], v[176:179], v[124:127]
	v_mfma_f32_16x16x32_bf16 v[120:123], v[152:155], v[176:179], v[120:123]
	v_mfma_f32_16x16x32_bf16 v[116:119], v[144:147], v[184:187], v[116:119]
	v_mfma_f32_16x16x32_bf16 v[112:115], v[152:155], v[184:187], v[112:115]
	v_mfma_f32_16x16x32_bf16 v[108:111], v[144:147], v[192:195], v[108:111]
	v_mfma_f32_16x16x32_bf16 v[100:103], v[152:155], v[192:195], v[100:103]
	v_mfma_f32_16x16x32_bf16 v[92:95], v[144:147], v[200:203], v[92:95]
	v_mfma_f32_16x16x32_bf16 v[84:87], v[152:155], v[200:203], v[84:87]
	v_mfma_f32_16x16x32_bf16 v[124:127], v[148:151], v[180:183], v[124:127]
	v_mfma_f32_16x16x32_bf16 v[120:123], v[156:159], v[180:183], v[120:123]
	v_mfma_f32_16x16x32_bf16 v[116:119], v[148:151], v[188:191], v[116:119]
	v_mfma_f32_16x16x32_bf16 v[112:115], v[156:159], v[188:191], v[112:115]
	v_mfma_f32_16x16x32_bf16 v[108:111], v[148:151], v[196:199], v[108:111]
	v_mfma_f32_16x16x32_bf16 v[100:103], v[156:159], v[196:199], v[100:103]
	v_mfma_f32_16x16x32_bf16 v[92:95], v[148:151], v[204:207], v[92:95]
	v_mfma_f32_16x16x32_bf16 v[84:87], v[156:159], v[204:207], v[84:87]
	v_mfma_f32_16x16x32_bf16 v[104:107], v[160:163], v[176:179], v[104:107]
	v_mfma_f32_16x16x32_bf16 v[96:99], v[168:171], v[176:179], v[96:99]
	v_mfma_f32_16x16x32_bf16 v[88:91], v[160:163], v[184:187], v[88:91]
	v_mfma_f32_16x16x32_bf16 v[80:83], v[168:171], v[184:187], v[80:83]
	v_mfma_f32_16x16x32_bf16 v[76:79], v[160:163], v[192:195], v[76:79]
	v_mfma_f32_16x16x32_bf16 v[72:75], v[168:171], v[192:195], v[72:75]
	v_mfma_f32_16x16x32_bf16 v[68:71], v[160:163], v[200:203], v[68:71]
	v_mfma_f32_16x16x32_bf16 v[64:67], v[168:171], v[200:203], v[64:67]
	v_mfma_f32_16x16x32_bf16 v[104:107], v[164:167], v[180:183], v[104:107]
	v_mfma_f32_16x16x32_bf16 v[96:99], v[172:175], v[180:183], v[96:99]
	v_mfma_f32_16x16x32_bf16 v[88:91], v[164:167], v[188:191], v[88:91]
	v_mfma_f32_16x16x32_bf16 v[80:83], v[172:175], v[188:191], v[80:83]
	v_mfma_f32_16x16x32_bf16 v[76:79], v[164:167], v[196:199], v[76:79]
	v_mfma_f32_16x16x32_bf16 v[72:75], v[172:175], v[196:199], v[72:75]
	v_mfma_f32_16x16x32_bf16 v[68:71], v[164:167], v[204:207], v[68:71]
	v_mfma_f32_16x16x32_bf16 v[64:67], v[172:175], v[204:207], v[64:67]
	s_barrier
; template <class Epi, class Sched, class Hook = NoHook>
; __device__ __forceinline__ void gemm_phase_w(LAS unsigned char* lds, const Sched& S, const Epi& E, int wave_id, const Hook& HK = Hook()) {
;     ...
;         if constexpr (!SEG2) {
;             for (int tt = 0; tt < nt; tt += 2) {
;                 if constexpr (GATHER) { if (tt == nt - 2) {
;                     if (has_next) { gnxt_00 = S.grow_l(nxt, lds, nbuf, R0) + (unsigned)(C0 * 2); gnxt_01 = S.grow_l(nxt, lds, nbuf, R1) + (unsigned)(C1 * 2); gnxt_10 = S.grow_l(nxt, lds, nbuf, 128 + R0) + (unsigned)(C0 * 2); gnxt_11 = S.grow_l(nxt, lds, nbuf, 128 + R1) + (unsigned)(C1 * 2); }
;                     else { gnxt_00 = gcur_00; gnxt_01 = gcur_01; gnxt_10 = gcur_10; gnxt_11 = gcur_11; } } }
;                 PG_TRIP(tt, false, false, false);
;             }
	s_bitset1_b32 s30, 7
	s_add_i32 s0, s30, s68
	s_ashr_i32 s1, s0, 31
	s_add_u32 s0, s6, s0
	s_addc_u32 s1, s7, s1
	s_add_i32 s68, s70, s27
	v_lshl_add_u64 v[208:209], s[0:1], 0, v[128:129]
	s_mov_b32 m0, s68
	ds_read_b128 v[176:179], v143 offset:49152
	ds_read_b128 v[180:183], v143 offset:50176
	ds_read_b128 v[184:187], v143 offset:51200
	ds_read_b128 v[188:191], v143 offset:52224
	ds_read_b128 v[192:195], v143 offset:53248
	ds_read_b128 v[196:199], v143 offset:54272
	ds_read_b128 v[200:203], v143 offset:55296
	ds_read_b128 v[204:207], v143 offset:56320
	global_load_lds_dwordx4 v[208:209], off
	v_lshl_add_u64 v[208:209], s[0:1], 0, v[130:131]
	s_add_i32 s0, s30, s31
	s_add_i32 m0, s68, 0x2000
	s_ashr_i32 s1, s0, 31
	s_add_u32 s0, s6, s0
	s_addc_u32 s1, s7, s1
	s_add_i32 s31, s71, s27
	global_load_lds_dwordx4 v[208:209], off
	v_lshl_add_u64 v[208:209], s[0:1], 0, v[128:129]
	s_mov_b32 m0, s31
	s_add_i32 s30, s30, s19
	global_load_lds_dwordx4 v[208:209], off
	s_add_i32 m0, s31, 0x2000
	v_lshl_add_u64 v[208:209], s[0:1], 0, v[130:131]
	s_add_u32 s0, s4, s30
	s_addc_u32 s1, s5, 0
	global_load_lds_dwordx4 v[208:209], off
	v_lshl_add_u64 v[208:209], s[0:1], 0, v[128:129]
	s_mov_b32 m0, s36
	s_nop 0
	global_load_lds_dwordx4 v[208:209], off
	v_lshl_add_u64 v[208:209], s[0:1], 0, v[130:131]
	s_mov_b32 m0, s37
	s_nop 0
	global_load_lds_dwordx4 v[208:209], off
	s_waitcnt vmcnt(8)
	s_waitcnt lgkmcnt(0)
	s_barrier
	s_waitcnt lgkmcnt(0)
	v_mfma_f32_16x16x32_bf16 v[60:63], v[144:147], v[176:179], v[60:63]
	v_mfma_f32_16x16x32_bf16 v[56:59], v[152:155], v[176:179], v[56:59]
	v_mfma_f32_16x16x32_bf16 v[52:55], v[144:147], v[184:187], v[52:55]
	v_mfma_f32_16x16x32_bf16 v[48:51], v[152:155], v[184:187], v[48:51]
	v_mfma_f32_16x16x32_bf16 v[44:47], v[144:147], v[192:195], v[44:47]
	v_mfma_f32_16x16x32_bf16 v[36:39], v[152:155], v[192:195], v[36:39]
	v_mfma_f32_16x16x32_bf16 v[28:31], v[144:147], v[200:203], v[28:31]
	v_mfma_f32_16x16x32_bf16 v[20:23], v[152:155], v[200:203], v[20:23]
	v_mfma_f32_16x16x32_bf16 v[60:63], v[148:151], v[180:183], v[60:63]
	v_mfma_f32_16x16x32_bf16 v[56:59], v[156:159], v[180:183], v[56:59]
	v_mfma_f32_16x16x32_bf16 v[52:55], v[148:151], v[188:191], v[52:55]
	v_mfma_f32_16x16x32_bf16 v[48:51], v[156:159], v[188:191], v[48:51]
	v_mfma_f32_16x16x32_bf16 v[44:47], v[148:151], v[196:199], v[44:47]
	v_mfma_f32_16x16x32_bf16 v[36:39], v[156:159], v[196:199], v[36:39]
	v_mfma_f32_16x16x32_bf16 v[28:31], v[148:151], v[204:207], v[28:31]
	v_mfma_f32_16x16x32_bf16 v[20:23], v[156:159], v[204:207], v[20:23]
	v_mfma_f32_16x16x32_bf16 v[40:43], v[160:163], v[176:179], v[40:43]
	v_mfma_f32_16x16x32_bf16 v[32:35], v[168:171], v[176:179], v[32:35]
	v_mfma_f32_16x16x32_bf16 v[24:27], v[160:163], v[184:187], v[24:27]
	v_mfma_f32_16x16x32_bf16 v[16:19], v[168:171], v[184:187], v[16:19]
	v_mfma_f32_16x16x32_bf16 v[12:15], v[160:163], v[192:195], v[12:15]
	v_mfma_f32_16x16x32_bf16 v[8:11], v[168:171], v[192:195], v[8:11]
	v_mfma_f32_16x16x32_bf16 v[4:7], v[160:163], v[200:203], v[4:7]
	v_mfma_f32_16x16x32_bf16 v[0:3], v[168:171], v[200:203], v[0:3]
	v_mfma_f32_16x16x32_bf16 v[40:43], v[164:167], v[180:183], v[40:43]
	v_mfma_f32_16x16x32_bf16 v[32:35], v[172:175], v[180:183], v[32:35]
	v_mfma_f32_16x16x32_bf16 v[24:27], v[164:167], v[188:191], v[24:27]
	v_mfma_f32_16x16x32_bf16 v[16:19], v[172:175], v[188:191], v[16:19]
	v_mfma_f32_16x16x32_bf16 v[12:15], v[164:167], v[196:199], v[12:15]
	v_mfma_f32_16x16x32_bf16 v[8:11], v[172:175], v[196:199], v[8:11]
	v_mfma_f32_16x16x32_bf16 v[4:7], v[164:167], v[204:207], v[4:7]
	v_mfma_f32_16x16x32_bf16 v[0:3], v[172:175], v[204:207], v[0:3]
	s_barrier
	s_addk_i32 s10, 0x100
	s_add_i32 s18, s18, 2
	s_cmp_gt_u32 s18, 29
	s_cbranch_scc0 .LBB0_261
	s_and_b64 vcc, exec, s[14:15]
	s_cbranch_vccz .LBB0_264
	s_barrier

.LBB0_386:
	ds_read_b128 v[142:145], v139
	ds_read_b128 v[146:149], v139 offset:1024
	ds_read_b128 v[150:153], v139 offset:2048
	ds_read_b128 v[154:157], v139 offset:3072
	ds_read_b128 v[158:161], v140
	ds_read_b128 v[162:165], v140 offset:1024
	ds_read_b128 v[166:169], v140 offset:2048
	ds_read_b128 v[170:173], v140 offset:3072
	s_add_i32 s0, s45, s10
	s_add_u32 s0, s4, s0
	s_addc_u32 s1, s5, 0
	s_add_i32 m0, s23, 0xc000
	s_add_i32 s61, s23, 0xe000
	s_add_i32 s66, s10, 0xfff80080
	s_cmp_eq_u32 s18, 28
	s_cselect_b32 s19, s41, s45
	s_cselect_b32 s60, s40, s44
	v_lshl_add_u64 v[206:207], s[0:1], 0, v[128:129]
	ds_read_b128 v[174:177], v141
	ds_read_b128 v[178:181], v141 offset:1024
	ds_read_b128 v[182:185], v141 offset:2048
	ds_read_b128 v[186:189], v141 offset:3072
	ds_read_b128 v[190:193], v141 offset:4096
	ds_read_b128 v[194:197], v141 offset:5120
	ds_read_b128 v[198:201], v141 offset:6144
	ds_read_b128 v[202:205], v141 offset:7168
	global_load_lds_dwordx4 v[206:207], off
	v_lshl_add_u64 v[206:207], s[0:1], 0, v[130:131]
	s_mov_b32 m0, s61
	s_nop 0
	global_load_lds_dwordx4 v[206:207], off
	s_waitcnt vmcnt(8)
	s_waitcnt lgkmcnt(0)
	s_barrier
	s_waitcnt lgkmcnt(0)
	v_mfma_f32_16x16x32_bf16 v[124:127], v[142:145], v[174:177], v[124:127]
	v_mfma_f32_16x16x32_bf16 v[120:123], v[150:153], v[174:177], v[120:123]
	v_mfma_f32_16x16x32_bf16 v[116:119], v[142:145], v[182:185], v[116:119]
	v_mfma_f32_16x16x32_bf16 v[112:115], v[150:153], v[182:185], v[112:115]
	v_mfma_f32_16x16x32_bf16 v[108:111], v[142:145], v[190:193], v[108:111]
	v_mfma_f32_16x16x32_bf16 v[100:103], v[150:153], v[190:193], v[100:103]
	v_mfma_f32_16x16x32_bf16 v[92:95], v[142:145], v[198:201], v[92:95]
	v_mfma_f32_16x16x32_bf16 v[84:87], v[150:153], v[198:201], v[84:87]
	v_mfma_f32_16x16x32_bf16 v[124:127], v[146:149], v[178:181], v[124:127]
	v_mfma_f32_16x16x32_bf16 v[120:123], v[154:157], v[178:181], v[120:123]
	v_mfma_f32_16x16x32_bf16 v[116:119], v[146:149], v[186:189], v[116:119]
	v_mfma_f32_16x16x32_bf16 v[112:115], v[154:157], v[186:189], v[112:115]
	v_mfma_f32_16x16x32_bf16 v[108:111], v[146:149], v[194:197], v[108:111]
	v_mfma_f32_16x16x32_bf16 v[100:103], v[154:157], v[194:197], v[100:103]
	v_mfma_f32_16x16x32_bf16 v[92:95], v[146:149], v[202:205], v[92:95]
	v_mfma_f32_16x16x32_bf16 v[84:87], v[154:157], v[202:205], v[84:87]
	v_mfma_f32_16x16x32_bf16 v[104:107], v[158:161], v[174:177], v[104:107]
	v_mfma_f32_16x16x32_bf16 v[96:99], v[166:169], v[174:177], v[96:99]
	v_mfma_f32_16x16x32_bf16 v[88:91], v[158:161], v[182:185], v[88:91]
	v_mfma_f32_16x16x32_bf16 v[80:83], v[166:169], v[182:185], v[80:83]
	v_mfma_f32_16x16x32_bf16 v[76:79], v[158:161], v[190:193], v[76:79]
	v_mfma_f32_16x16x32_bf16 v[72:75], v[166:169], v[190:193], v[72:75]
	v_mfma_f32_16x16x32_bf16 v[68:71], v[158:161], v[198:201], v[68:71]
	v_mfma_f32_16x16x32_bf16 v[64:67], v[166:169], v[198:201], v[64:67]
	v_mfma_f32_16x16x32_bf16 v[104:107], v[162:165], v[178:181], v[104:107]
	v_mfma_f32_16x16x32_bf16 v[96:99], v[170:173], v[178:181], v[96:99]
	v_mfma_f32_16x16x32_bf16 v[88:91], v[162:165], v[186:189], v[88:91]
	v_mfma_f32_16x16x32_bf16 v[80:83], v[170:173], v[186:189], v[80:83]
	v_mfma_f32_16x16x32_bf16 v[76:79], v[162:165], v[194:197], v[76:79]
	v_mfma_f32_16x16x32_bf16 v[72:75], v[170:173], v[194:197], v[72:75]
	v_mfma_f32_16x16x32_bf16 v[68:71], v[162:165], v[202:205], v[68:71]
	v_mfma_f32_16x16x32_bf16 v[64:67], v[170:173], v[202:205], v[64:67]
	s_barrier
	s_cselect_b32 s61, 0, s66
	s_add_i32 s0, s61, s60
	s_ashr_i32 s1, s0, 31
	s_add_u32 s0, s6, s0
	s_addc_u32 s1, s7, s1
	s_add_i32 s66, s30, s27
	v_lshl_add_u64 v[206:207], s[0:1], 0, v[128:129]
	s_mov_b32 m0, s66
	ds_read_b128 v[174:177], v141 offset:16384
	ds_read_b128 v[178:181], v141 offset:17408
	ds_read_b128 v[182:185], v141 offset:18432
	ds_read_b128 v[186:189], v141 offset:19456
	ds_read_b128 v[190:193], v141 offset:20480
	ds_read_b128 v[194:197], v141 offset:21504
	ds_read_b128 v[198:201], v141 offset:22528
	ds_read_b128 v[202:205], v141 offset:23552
	global_load_lds_dwordx4 v[206:207], off
	s_add_i32 m0, s66, 0x2000
	s_add_i32 s66, s60, 0x80000
	v_lshl_add_u64 v[206:207], s[0:1], 0, v[130:131]
	s_add_i32 s0, s66, s61
	s_ashr_i32 s1, s0, 31
	s_add_u32 s0, s6, s0
	s_addc_u32 s1, s7, s1
	s_add_i32 s67, s31, s27
	global_load_lds_dwordx4 v[206:207], off
	v_lshl_add_u64 v[206:207], s[0:1], 0, v[128:129]
	s_mov_b32 m0, s67
	s_nop 0
	global_load_lds_dwordx4 v[206:207], off
	s_add_i32 m0, s67, 0x2000
	s_add_i32 s67, s61, s19
	v_lshl_add_u64 v[206:207], s[0:1], 0, v[130:131]
	s_add_u32 s0, s4, s67
	s_addc_u32 s1, s5, 0
	global_load_lds_dwordx4 v[206:207], off
	v_lshl_add_u64 v[206:207], s[0:1], 0, v[128:129]
	s_mov_b32 m0, s23
	s_nop 0
	global_load_lds_dwordx4 v[206:207], off
	v_lshl_add_u64 v[206:207], s[0:1], 0, v[130:131]
	s_mov_b32 m0, s24
	s_nop 0
	global_load_lds_dwordx4 v[206:207], off
	s_waitcnt vmcnt(8)
	s_waitcnt lgkmcnt(0)
	s_barrier
	s_waitcnt lgkmcnt(0)
	v_mfma_f32_16x16x32_bf16 v[60:63], v[142:145], v[174:177], v[60:63]
	v_mfma_f32_16x16x32_bf16 v[56:59], v[150:153], v[174:177], v[56:59]
	v_mfma_f32_16x16x32_bf16 v[52:55], v[142:145], v[182:185], v[52:55]
	v_mfma_f32_16x16x32_bf16 v[48:51], v[150:153], v[182:185], v[48:51]
	v_mfma_f32_16x16x32_bf16 v[44:47], v[142:145], v[190:193], v[44:47]
	v_mfma_f32_16x16x32_bf16 v[36:39], v[150:153], v[190:193], v[36:39]
	v_mfma_f32_16x16x32_bf16 v[28:31], v[142:145], v[198:201], v[28:31]
	v_mfma_f32_16x16x32_bf16 v[20:23], v[150:153], v[198:201], v[20:23]
	v_mfma_f32_16x16x32_bf16 v[60:63], v[146:149], v[178:181], v[60:63]
	v_mfma_f32_16x16x32_bf16 v[56:59], v[154:157], v[178:181], v[56:59]
	v_mfma_f32_16x16x32_bf16 v[52:55], v[146:149], v[186:189], v[52:55]
	v_mfma_f32_16x16x32_bf16 v[48:51], v[154:157], v[186:189], v[48:51]
	v_mfma_f32_16x16x32_bf16 v[44:47], v[146:149], v[194:197], v[44:47]
	v_mfma_f32_16x16x32_bf16 v[36:39], v[154:157], v[194:197], v[36:39]
	v_mfma_f32_16x16x32_bf16 v[28:31], v[146:149], v[202:205], v[28:31]
	v_mfma_f32_16x16x32_bf16 v[20:23], v[154:157], v[202:205], v[20:23]
	v_mfma_f32_16x16x32_bf16 v[40:43], v[158:161], v[174:177], v[40:43]
	v_mfma_f32_16x16x32_bf16 v[32:35], v[166:169], v[174:177], v[32:35]
	v_mfma_f32_16x16x32_bf16 v[24:27], v[158:161], v[182:185], v[24:27]
	v_mfma_f32_16x16x32_bf16 v[16:19], v[166:169], v[182:185], v[16:19]
	v_mfma_f32_16x16x32_bf16 v[12:15], v[158:161], v[190:193], v[12:15]
	v_mfma_f32_16x16x32_bf16 v[8:11], v[166:169], v[190:193], v[8:11]
	v_mfma_f32_16x16x32_bf16 v[4:7], v[158:161], v[198:201], v[4:7]
	v_mfma_f32_16x16x32_bf16 v[0:3], v[166:169], v[198:201], v[0:3]
	v_mfma_f32_16x16x32_bf16 v[40:43], v[162:165], v[178:181], v[40:43]
	v_mfma_f32_16x16x32_bf16 v[32:35], v[170:173], v[178:181], v[32:35]
	v_mfma_f32_16x16x32_bf16 v[24:27], v[162:165], v[186:189], v[24:27]
	v_mfma_f32_16x16x32_bf16 v[16:19], v[170:173], v[186:189], v[16:19]
	v_mfma_f32_16x16x32_bf16 v[12:15], v[162:165], v[194:197], v[12:15]
	v_mfma_f32_16x16x32_bf16 v[8:11], v[170:173], v[194:197], v[8:11]
	v_mfma_f32_16x16x32_bf16 v[4:7], v[162:165], v[202:205], v[4:7]
	v_mfma_f32_16x16x32_bf16 v[0:3], v[170:173], v[202:205], v[0:3]
	s_barrier
	s_add_i32 s68, 0, 0x18000
	s_add_i32 s69, 0, 0x1c000
	v_add_u32_e32 v154, s68, v138
	v_add_u32_e32 v170, s69, v138
	ds_read_b128 v[142:145], v154
	ds_read_b128 v[146:149], v154 offset:1024
	ds_read_b128 v[150:153], v154 offset:2048
	ds_read_b128 v[154:157], v154 offset:3072
	ds_read_b128 v[158:161], v170
	ds_read_b128 v[162:165], v170 offset:1024
	ds_read_b128 v[166:169], v170 offset:2048
	ds_read_b128 v[170:173], v170 offset:3072
	s_add_i32 s67, s67, 0x80000
	s_add_u32 s0, s4, s67
	s_addc_u32 s1, s5, 0
	s_mov_b32 m0, s25
	v_lshl_add_u64 v[206:207], s[0:1], 0, v[128:129]
	ds_read_b128 v[174:177], v141 offset:32768
	ds_read_b128 v[178:181], v141 offset:33792
	ds_read_b128 v[182:185], v141 offset:34816
	ds_read_b128 v[186:189], v141 offset:35840
	ds_read_b128 v[190:193], v141 offset:36864
	ds_read_b128 v[194:197], v141 offset:37888
	ds_read_b128 v[198:201], v141 offset:38912
	ds_read_b128 v[202:205], v141 offset:39936
	global_load_lds_dwordx4 v[206:207], off
	v_lshl_add_u64 v[206:207], s[0:1], 0, v[130:131]
	s_mov_b32 m0, s33
	s_nop 0
	global_load_lds_dwordx4 v[206:207], off
	s_waitcnt vmcnt(8)
	s_waitcnt lgkmcnt(0)
	s_barrier
	s_waitcnt lgkmcnt(0)
	v_mfma_f32_16x16x32_bf16 v[124:127], v[142:145], v[174:177], v[124:127]
	v_mfma_f32_16x16x32_bf16 v[120:123], v[150:153], v[174:177], v[120:123]
	v_mfma_f32_16x16x32_bf16 v[116:119], v[142:145], v[182:185], v[116:119]
	v_mfma_f32_16x16x32_bf16 v[112:115], v[150:153], v[182:185], v[112:115]
	v_mfma_f32_16x16x32_bf16 v[108:111], v[142:145], v[190:193], v[108:111]
	v_mfma_f32_16x16x32_bf16 v[100:103], v[150:153], v[190:193], v[100:103]
	v_mfma_f32_16x16x32_bf16 v[92:95], v[142:145], v[198:201], v[92:95]
	v_mfma_f32_16x16x32_bf16 v[84:87], v[150:153], v[198:201], v[84:87]
	v_mfma_f32_16x16x32_bf16 v[124:127], v[146:149], v[178:181], v[124:127]
	v_mfma_f32_16x16x32_bf16 v[120:123], v[154:157], v[178:181], v[120:123]
	v_mfma_f32_16x16x32_bf16 v[116:119], v[146:149], v[186:189], v[116:119]
	v_mfma_f32_16x16x32_bf16 v[112:115], v[154:157], v[186:189], v[112:115]
	v_mfma_f32_16x16x32_bf16 v[108:111], v[146:149], v[194:197], v[108:111]
	v_mfma_f32_16x16x32_bf16 v[100:103], v[154:157], v[194:197], v[100:103]
	v_mfma_f32_16x16x32_bf16 v[92:95], v[146:149], v[202:205], v[92:95]
	v_mfma_f32_16x16x32_bf16 v[84:87], v[154:157], v[202:205], v[84:87]
	v_mfma_f32_16x16x32_bf16 v[104:107], v[158:161], v[174:177], v[104:107]
	v_mfma_f32_16x16x32_bf16 v[96:99], v[166:169], v[174:177], v[96:99]
	v_mfma_f32_16x16x32_bf16 v[88:91], v[158:161], v[182:185], v[88:91]
	v_mfma_f32_16x16x32_bf16 v[80:83], v[166:169], v[182:185], v[80:83]
	v_mfma_f32_16x16x32_bf16 v[76:79], v[158:161], v[190:193], v[76:79]
	v_mfma_f32_16x16x32_bf16 v[72:75], v[166:169], v[190:193], v[72:75]
	v_mfma_f32_16x16x32_bf16 v[68:71], v[158:161], v[198:201], v[68:71]
	v_mfma_f32_16x16x32_bf16 v[64:67], v[166:169], v[198:201], v[64:67]
	v_mfma_f32_16x16x32_bf16 v[104:107], v[162:165], v[178:181], v[104:107]
	v_mfma_f32_16x16x32_bf16 v[96:99], v[170:173], v[178:181], v[96:99]
	v_mfma_f32_16x16x32_bf16 v[88:91], v[162:165], v[186:189], v[88:91]
	v_mfma_f32_16x16x32_bf16 v[80:83], v[170:173], v[186:189], v[80:83]
	v_mfma_f32_16x16x32_bf16 v[76:79], v[162:165], v[194:197], v[76:79]
	v_mfma_f32_16x16x32_bf16 v[72:75], v[170:173], v[194:197], v[72:75]
	v_mfma_f32_16x16x32_bf16 v[68:71], v[162:165], v[202:205], v[68:71]
	v_mfma_f32_16x16x32_bf16 v[64:67], v[170:173], v[202:205], v[64:67]
	s_barrier
; template <class Epi, class Sched, class Hook = NoHook>
; __device__ __forceinline__ void gemm_phase_w(LAS unsigned char* lds, const Sched& S, const Epi& E, int wave_id, const Hook& HK = Hook()) {
;     ...
;         if constexpr (!SEG2) {
;             for (int tt = 0; tt < nt; tt += 2) {
;                 if constexpr (GATHER) { if (tt == nt - 2) {
;                     if (has_next) { gnxt_00 = S.grow_l(nxt, lds, nbuf, R0) + (unsigned)(C0 * 2); gnxt_01 = S.grow_l(nxt, lds, nbuf, R1) + (unsigned)(C1 * 2); gnxt_10 = S.grow_l(nxt, lds, nbuf, 128 + R0) + (unsigned)(C0 * 2); gnxt_11 = S.grow_l(nxt, lds, nbuf, 128 + R1) + (unsigned)(C1 * 2); }
;                     else { gnxt_00 = gcur_00; gnxt_01 = gcur_01; gnxt_10 = gcur_10; gnxt_11 = gcur_11; } } }
;                 PG_TRIP(tt, false, false, false);
;             }
	s_bitset1_b32 s61, 7
	s_add_i32 s0, s61, s60
	s_ashr_i32 s1, s0, 31
	s_add_u32 s0, s6, s0
	s_addc_u32 s1, s7, s1
	s_add_i32 s60, s68, s27
	v_lshl_add_u64 v[206:207], s[0:1], 0, v[128:129]
	s_mov_b32 m0, s60
	ds_read_b128 v[174:177], v141 offset:49152
	ds_read_b128 v[178:181], v141 offset:50176
	ds_read_b128 v[182:185], v141 offset:51200
	ds_read_b128 v[186:189], v141 offset:52224
	ds_read_b128 v[190:193], v141 offset:53248
	ds_read_b128 v[194:197], v141 offset:54272
	ds_read_b128 v[198:201], v141 offset:55296
	ds_read_b128 v[202:205], v141 offset:56320
	global_load_lds_dwordx4 v[206:207], off
	v_lshl_add_u64 v[206:207], s[0:1], 0, v[130:131]
	s_add_i32 s0, s61, s66
	s_add_i32 m0, s60, 0x2000
	s_ashr_i32 s1, s0, 31
	s_add_u32 s0, s6, s0
	s_addc_u32 s1, s7, s1
	s_add_i32 s60, s69, s27
	global_load_lds_dwordx4 v[206:207], off
	v_lshl_add_u64 v[206:207], s[0:1], 0, v[128:129]
	s_mov_b32 m0, s60
	s_add_i32 s61, s61, s19
	global_load_lds_dwordx4 v[206:207], off
	s_add_i32 m0, s60, 0x2000
	v_lshl_add_u64 v[206:207], s[0:1], 0, v[130:131]
	s_add_u32 s0, s4, s61
	s_addc_u32 s1, s5, 0
	global_load_lds_dwordx4 v[206:207], off
	v_lshl_add_u64 v[206:207], s[0:1], 0, v[128:129]
	s_mov_b32 m0, s34
	s_nop 0
	global_load_lds_dwordx4 v[206:207], off
	v_lshl_add_u64 v[206:207], s[0:1], 0, v[130:131]
	s_mov_b32 m0, s35
	s_nop 0
	global_load_lds_dwordx4 v[206:207], off
	s_waitcnt vmcnt(8)
	s_waitcnt lgkmcnt(0)
	s_barrier
	s_waitcnt lgkmcnt(0)
	v_mfma_f32_16x16x32_bf16 v[60:63], v[142:145], v[174:177], v[60:63]
	v_mfma_f32_16x16x32_bf16 v[56:59], v[150:153], v[174:177], v[56:59]
	v_mfma_f32_16x16x32_bf16 v[52:55], v[142:145], v[182:185], v[52:55]
	v_mfma_f32_16x16x32_bf16 v[48:51], v[150:153], v[182:185], v[48:51]
	v_mfma_f32_16x16x32_bf16 v[44:47], v[142:145], v[190:193], v[44:47]
	v_mfma_f32_16x16x32_bf16 v[36:39], v[150:153], v[190:193], v[36:39]
	v_mfma_f32_16x16x32_bf16 v[28:31], v[142:145], v[198:201], v[28:31]
	v_mfma_f32_16x16x32_bf16 v[20:23], v[150:153], v[198:201], v[20:23]
	v_mfma_f32_16x16x32_bf16 v[60:63], v[146:149], v[178:181], v[60:63]
	v_mfma_f32_16x16x32_bf16 v[56:59], v[154:157], v[178:181], v[56:59]
	v_mfma_f32_16x16x32_bf16 v[52:55], v[146:149], v[186:189], v[52:55]
	v_mfma_f32_16x16x32_bf16 v[48:51], v[154:157], v[186:189], v[48:51]
	v_mfma_f32_16x16x32_bf16 v[44:47], v[146:149], v[194:197], v[44:47]
	v_mfma_f32_16x16x32_bf16 v[36:39], v[154:157], v[194:197], v[36:39]
	v_mfma_f32_16x16x32_bf16 v[28:31], v[146:149], v[202:205], v[28:31]
	v_mfma_f32_16x16x32_bf16 v[20:23], v[154:157], v[202:205], v[20:23]
	v_mfma_f32_16x16x32_bf16 v[40:43], v[158:161], v[174:177], v[40:43]
	v_mfma_f32_16x16x32_bf16 v[32:35], v[166:169], v[174:177], v[32:35]
	v_mfma_f32_16x16x32_bf16 v[24:27], v[158:161], v[182:185], v[24:27]
	v_mfma_f32_16x16x32_bf16 v[16:19], v[166:169], v[182:185], v[16:19]
	v_mfma_f32_16x16x32_bf16 v[12:15], v[158:161], v[190:193], v[12:15]
	v_mfma_f32_16x16x32_bf16 v[8:11], v[166:169], v[190:193], v[8:11]
	v_mfma_f32_16x16x32_bf16 v[4:7], v[158:161], v[198:201], v[4:7]
	v_mfma_f32_16x16x32_bf16 v[0:3], v[166:169], v[198:201], v[0:3]
	v_mfma_f32_16x16x32_bf16 v[40:43], v[162:165], v[178:181], v[40:43]
	v_mfma_f32_16x16x32_bf16 v[32:35], v[170:173], v[178:181], v[32:35]
	v_mfma_f32_16x16x32_bf16 v[24:27], v[162:165], v[186:189], v[24:27]
	v_mfma_f32_16x16x32_bf16 v[16:19], v[170:173], v[186:189], v[16:19]
	v_mfma_f32_16x16x32_bf16 v[12:15], v[162:165], v[194:197], v[12:15]
	v_mfma_f32_16x16x32_bf16 v[8:11], v[170:173], v[194:197], v[8:11]
	v_mfma_f32_16x16x32_bf16 v[4:7], v[162:165], v[202:205], v[4:7]
	v_mfma_f32_16x16x32_bf16 v[0:3], v[170:173], v[202:205], v[0:3]
	s_barrier
	s_addk_i32 s10, 0x100
	s_add_i32 s18, s18, 2
	s_cmp_gt_u32 s18, 29
	s_cbranch_scc0 .LBB0_386
	s_and_b64 vcc, exec, s[14:15]
	s_cbranch_vccz .LBB0_389
	s_barrier

.LBB0_654:
	ds_read_b128 v[116:119], v157
	ds_read_b128 v[120:123], v157 offset:1024
	ds_read_b128 v[128:131], v157 offset:2048
	ds_read_b128 v[132:135], v157 offset:3072
	ds_read_b128 v[150:153], v158
	ds_read_b128 v[160:163], v158 offset:1024
	ds_read_b128 v[164:167], v158 offset:2048
	ds_read_b128 v[168:171], v158 offset:3072
	s_add_i32 s40, s39, s18
	s_add_u32 s42, s4, s40
	s_addc_u32 s43, s5, 0
	s_add_i32 m0, s23, 0xc000
	s_add_i32 s44, s23, 0xe000
	s_add_i32 s45, s18, 0xfff80080
	s_cmp_eq_u32 s19, 28
	s_cselect_b32 s40, s35, s39
	s_cselect_b32 s41, s34, s38
	v_lshl_add_u64 v[204:205], s[42:43], 0, v[144:145]
	ds_read_b128 v[172:175], v159
	ds_read_b128 v[176:179], v159 offset:1024
	ds_read_b128 v[180:183], v159 offset:2048
	ds_read_b128 v[184:187], v159 offset:3072
	ds_read_b128 v[188:191], v159 offset:4096
	ds_read_b128 v[192:195], v159 offset:5120
	ds_read_b128 v[196:199], v159 offset:6144
	ds_read_b128 v[200:203], v159 offset:7168
	global_load_lds_dwordx4 v[204:205], off
	v_lshl_add_u64 v[204:205], s[42:43], 0, v[146:147]
	s_mov_b32 m0, s44
	s_nop 0
	global_load_lds_dwordx4 v[204:205], off
	s_waitcnt vmcnt(8)
	s_waitcnt lgkmcnt(0)
	s_barrier
	s_waitcnt lgkmcnt(0)
	v_mfma_f32_16x16x32_bf16 v[140:143], v[116:119], v[172:175], v[140:143]
	v_mfma_f32_16x16x32_bf16 v[136:139], v[128:131], v[172:175], v[136:139]
	v_mfma_f32_16x16x32_bf16 v[112:115], v[116:119], v[180:183], v[112:115]
	v_mfma_f32_16x16x32_bf16 v[104:107], v[128:131], v[180:183], v[104:107]
	v_mfma_f32_16x16x32_bf16 v[96:99], v[116:119], v[188:191], v[96:99]
	v_mfma_f32_16x16x32_bf16 v[88:91], v[128:131], v[188:191], v[88:91]
	v_mfma_f32_16x16x32_bf16 v[80:83], v[116:119], v[196:199], v[80:83]
	v_mfma_f32_16x16x32_bf16 v[72:75], v[128:131], v[196:199], v[72:75]
	v_mfma_f32_16x16x32_bf16 v[140:143], v[120:123], v[176:179], v[140:143]
	v_mfma_f32_16x16x32_bf16 v[136:139], v[132:135], v[176:179], v[136:139]
	v_mfma_f32_16x16x32_bf16 v[112:115], v[120:123], v[184:187], v[112:115]
	v_mfma_f32_16x16x32_bf16 v[104:107], v[132:135], v[184:187], v[104:107]
	v_mfma_f32_16x16x32_bf16 v[96:99], v[120:123], v[192:195], v[96:99]
	v_mfma_f32_16x16x32_bf16 v[88:91], v[132:135], v[192:195], v[88:91]
	v_mfma_f32_16x16x32_bf16 v[80:83], v[120:123], v[200:203], v[80:83]
	v_mfma_f32_16x16x32_bf16 v[72:75], v[132:135], v[200:203], v[72:75]
	v_mfma_f32_16x16x32_bf16 v[124:127], v[150:153], v[172:175], v[124:127]
	v_mfma_f32_16x16x32_bf16 v[108:111], v[164:167], v[172:175], v[108:111]
	v_mfma_f32_16x16x32_bf16 v[100:103], v[150:153], v[180:183], v[100:103]
	v_mfma_f32_16x16x32_bf16 v[92:95], v[164:167], v[180:183], v[92:95]
	v_mfma_f32_16x16x32_bf16 v[84:87], v[150:153], v[188:191], v[84:87]
	v_mfma_f32_16x16x32_bf16 v[76:79], v[164:167], v[188:191], v[76:79]
	v_mfma_f32_16x16x32_bf16 v[68:71], v[150:153], v[196:199], v[68:71]
	v_mfma_f32_16x16x32_bf16 v[64:67], v[164:167], v[196:199], v[64:67]
	v_mfma_f32_16x16x32_bf16 v[124:127], v[160:163], v[176:179], v[124:127]
	v_mfma_f32_16x16x32_bf16 v[108:111], v[168:171], v[176:179], v[108:111]
	v_mfma_f32_16x16x32_bf16 v[100:103], v[160:163], v[184:187], v[100:103]
	v_mfma_f32_16x16x32_bf16 v[92:95], v[168:171], v[184:187], v[92:95]
	v_mfma_f32_16x16x32_bf16 v[84:87], v[160:163], v[192:195], v[84:87]
	v_mfma_f32_16x16x32_bf16 v[76:79], v[168:171], v[192:195], v[76:79]
	v_mfma_f32_16x16x32_bf16 v[68:71], v[160:163], v[200:203], v[68:71]
	v_mfma_f32_16x16x32_bf16 v[64:67], v[168:171], v[200:203], v[64:67]
	s_barrier
	s_cselect_b32 s44, 0, s45
	s_add_i32 s42, s44, s41
	s_ashr_i32 s43, s42, 31
	s_add_u32 s42, s20, s42
	s_addc_u32 s43, s21, s43
	s_add_i32 s45, s29, s22
	v_lshl_add_u64 v[204:205], s[42:43], 0, v[144:145]
	s_mov_b32 m0, s45
	ds_read_b128 v[172:175], v159 offset:16384
	ds_read_b128 v[176:179], v159 offset:17408
	ds_read_b128 v[180:183], v159 offset:18432
	ds_read_b128 v[184:187], v159 offset:19456
	ds_read_b128 v[188:191], v159 offset:20480
	ds_read_b128 v[192:195], v159 offset:21504
	ds_read_b128 v[196:199], v159 offset:22528
	ds_read_b128 v[200:203], v159 offset:23552
	global_load_lds_dwordx4 v[204:205], off
	s_add_i32 m0, s45, 0x2000
	s_add_i32 s45, s41, 0x80000
	v_lshl_add_u64 v[204:205], s[42:43], 0, v[146:147]
	s_add_i32 s42, s45, s44
	s_ashr_i32 s43, s42, 31
	s_add_u32 s42, s20, s42
	s_addc_u32 s43, s21, s43
	s_add_i32 s58, s30, s22
	global_load_lds_dwordx4 v[204:205], off
	v_lshl_add_u64 v[204:205], s[42:43], 0, v[144:145]
	s_mov_b32 m0, s58
	s_nop 0
	global_load_lds_dwordx4 v[204:205], off
	s_add_i32 m0, s58, 0x2000
	s_add_i32 s58, s44, s40
	v_lshl_add_u64 v[204:205], s[42:43], 0, v[146:147]
	s_add_u32 s42, s4, s58
	s_addc_u32 s43, s5, 0
	global_load_lds_dwordx4 v[204:205], off
	v_lshl_add_u64 v[204:205], s[42:43], 0, v[144:145]
	s_mov_b32 m0, s23
	s_nop 0
	global_load_lds_dwordx4 v[204:205], off
	v_lshl_add_u64 v[204:205], s[42:43], 0, v[146:147]
	s_mov_b32 m0, s24
	s_nop 0
	global_load_lds_dwordx4 v[204:205], off
	s_waitcnt vmcnt(8)
	s_waitcnt lgkmcnt(0)
	s_barrier
	s_waitcnt lgkmcnt(0)
	v_mfma_f32_16x16x32_bf16 v[60:63], v[116:119], v[172:175], v[60:63]
	v_mfma_f32_16x16x32_bf16 v[56:59], v[128:131], v[172:175], v[56:59]
	v_mfma_f32_16x16x32_bf16 v[48:51], v[116:119], v[180:183], v[48:51]
	v_mfma_f32_16x16x32_bf16 v[40:43], v[128:131], v[180:183], v[40:43]
	v_mfma_f32_16x16x32_bf16 v[32:35], v[116:119], v[188:191], v[32:35]
	v_mfma_f32_16x16x32_bf16 v[24:27], v[128:131], v[188:191], v[24:27]
	v_mfma_f32_16x16x32_bf16 v[16:19], v[116:119], v[196:199], v[16:19]
	v_mfma_f32_16x16x32_bf16 v[8:11], v[128:131], v[196:199], v[8:11]
	v_mfma_f32_16x16x32_bf16 v[60:63], v[120:123], v[176:179], v[60:63]
	v_mfma_f32_16x16x32_bf16 v[56:59], v[132:135], v[176:179], v[56:59]
	v_mfma_f32_16x16x32_bf16 v[48:51], v[120:123], v[184:187], v[48:51]
	v_mfma_f32_16x16x32_bf16 v[40:43], v[132:135], v[184:187], v[40:43]
	v_mfma_f32_16x16x32_bf16 v[32:35], v[120:123], v[192:195], v[32:35]
	v_mfma_f32_16x16x32_bf16 v[24:27], v[132:135], v[192:195], v[24:27]
	v_mfma_f32_16x16x32_bf16 v[16:19], v[120:123], v[200:203], v[16:19]
	v_mfma_f32_16x16x32_bf16 v[8:11], v[132:135], v[200:203], v[8:11]
	v_mfma_f32_16x16x32_bf16 v[52:55], v[150:153], v[172:175], v[52:55]
	v_mfma_f32_16x16x32_bf16 v[44:47], v[164:167], v[172:175], v[44:47]
	v_mfma_f32_16x16x32_bf16 v[36:39], v[150:153], v[180:183], v[36:39]
	v_mfma_f32_16x16x32_bf16 v[28:31], v[164:167], v[180:183], v[28:31]
	v_mfma_f32_16x16x32_bf16 v[20:23], v[150:153], v[188:191], v[20:23]
	v_mfma_f32_16x16x32_bf16 v[12:15], v[164:167], v[188:191], v[12:15]
	v_mfma_f32_16x16x32_bf16 v[4:7], v[150:153], v[196:199], v[4:7]
	v_mfma_f32_16x16x32_bf16 v[0:3], v[164:167], v[196:199], v[0:3]
	v_mfma_f32_16x16x32_bf16 v[52:55], v[160:163], v[176:179], v[52:55]
	v_mfma_f32_16x16x32_bf16 v[44:47], v[168:171], v[176:179], v[44:47]
	v_mfma_f32_16x16x32_bf16 v[36:39], v[160:163], v[184:187], v[36:39]
	v_mfma_f32_16x16x32_bf16 v[28:31], v[168:171], v[184:187], v[28:31]
	v_mfma_f32_16x16x32_bf16 v[20:23], v[160:163], v[192:195], v[20:23]
	v_mfma_f32_16x16x32_bf16 v[12:15], v[168:171], v[192:195], v[12:15]
	v_mfma_f32_16x16x32_bf16 v[4:7], v[160:163], v[200:203], v[4:7]
	v_mfma_f32_16x16x32_bf16 v[0:3], v[168:171], v[200:203], v[0:3]
	s_barrier
	s_add_i32 s59, 0, 0x18000
	s_add_i32 s60, 0, 0x1c000
	v_add_u32_e32 v132, s59, v155
	v_add_u32_e32 v168, s60, v155
	ds_read_b128 v[116:119], v132
	ds_read_b128 v[120:123], v132 offset:1024
	ds_read_b128 v[128:131], v132 offset:2048
	ds_read_b128 v[132:135], v132 offset:3072
	ds_read_b128 v[150:153], v168
	ds_read_b128 v[160:163], v168 offset:1024
	ds_read_b128 v[164:167], v168 offset:2048
	ds_read_b128 v[168:171], v168 offset:3072
	s_add_i32 s58, s58, 0x80000
	s_add_u32 s42, s4, s58
	s_addc_u32 s43, s5, 0
	s_mov_b32 m0, s25
	v_lshl_add_u64 v[204:205], s[42:43], 0, v[144:145]
	ds_read_b128 v[172:175], v159 offset:32768
	ds_read_b128 v[176:179], v159 offset:33792
	ds_read_b128 v[180:183], v159 offset:34816
	ds_read_b128 v[184:187], v159 offset:35840
	ds_read_b128 v[188:191], v159 offset:36864
	ds_read_b128 v[192:195], v159 offset:37888
	ds_read_b128 v[196:199], v159 offset:38912
	ds_read_b128 v[200:203], v159 offset:39936
	global_load_lds_dwordx4 v[204:205], off
	v_lshl_add_u64 v[204:205], s[42:43], 0, v[146:147]
	s_mov_b32 m0, s26
	s_nop 0
	global_load_lds_dwordx4 v[204:205], off
	s_waitcnt vmcnt(8)
	s_waitcnt lgkmcnt(0)
	s_barrier
	s_waitcnt lgkmcnt(0)
	v_mfma_f32_16x16x32_bf16 v[140:143], v[116:119], v[172:175], v[140:143]
	v_mfma_f32_16x16x32_bf16 v[136:139], v[128:131], v[172:175], v[136:139]
	v_mfma_f32_16x16x32_bf16 v[112:115], v[116:119], v[180:183], v[112:115]
	v_mfma_f32_16x16x32_bf16 v[104:107], v[128:131], v[180:183], v[104:107]
	v_mfma_f32_16x16x32_bf16 v[96:99], v[116:119], v[188:191], v[96:99]
	v_mfma_f32_16x16x32_bf16 v[88:91], v[128:131], v[188:191], v[88:91]
	v_mfma_f32_16x16x32_bf16 v[80:83], v[116:119], v[196:199], v[80:83]
	v_mfma_f32_16x16x32_bf16 v[72:75], v[128:131], v[196:199], v[72:75]
	v_mfma_f32_16x16x32_bf16 v[140:143], v[120:123], v[176:179], v[140:143]
	v_mfma_f32_16x16x32_bf16 v[136:139], v[132:135], v[176:179], v[136:139]
	v_mfma_f32_16x16x32_bf16 v[112:115], v[120:123], v[184:187], v[112:115]
	v_mfma_f32_16x16x32_bf16 v[104:107], v[132:135], v[184:187], v[104:107]
	v_mfma_f32_16x16x32_bf16 v[96:99], v[120:123], v[192:195], v[96:99]
	v_mfma_f32_16x16x32_bf16 v[88:91], v[132:135], v[192:195], v[88:91]
	v_mfma_f32_16x16x32_bf16 v[80:83], v[120:123], v[200:203], v[80:83]
	v_mfma_f32_16x16x32_bf16 v[72:75], v[132:135], v[200:203], v[72:75]
	v_mfma_f32_16x16x32_bf16 v[124:127], v[150:153], v[172:175], v[124:127]
	v_mfma_f32_16x16x32_bf16 v[108:111], v[164:167], v[172:175], v[108:111]
	v_mfma_f32_16x16x32_bf16 v[100:103], v[150:153], v[180:183], v[100:103]
	v_mfma_f32_16x16x32_bf16 v[92:95], v[164:167], v[180:183], v[92:95]
	v_mfma_f32_16x16x32_bf16 v[84:87], v[150:153], v[188:191], v[84:87]
	v_mfma_f32_16x16x32_bf16 v[76:79], v[164:167], v[188:191], v[76:79]
	v_mfma_f32_16x16x32_bf16 v[68:71], v[150:153], v[196:199], v[68:71]
	v_mfma_f32_16x16x32_bf16 v[64:67], v[164:167], v[196:199], v[64:67]
	v_mfma_f32_16x16x32_bf16 v[124:127], v[160:163], v[176:179], v[124:127]
	v_mfma_f32_16x16x32_bf16 v[108:111], v[168:171], v[176:179], v[108:111]
	v_mfma_f32_16x16x32_bf16 v[100:103], v[160:163], v[184:187], v[100:103]
	v_mfma_f32_16x16x32_bf16 v[92:95], v[168:171], v[184:187], v[92:95]
	v_mfma_f32_16x16x32_bf16 v[84:87], v[160:163], v[192:195], v[84:87]
	v_mfma_f32_16x16x32_bf16 v[76:79], v[168:171], v[192:195], v[76:79]
	v_mfma_f32_16x16x32_bf16 v[68:71], v[160:163], v[200:203], v[68:71]
	v_mfma_f32_16x16x32_bf16 v[64:67], v[168:171], v[200:203], v[64:67]
	s_barrier
; template <class Epi, class Sched, class Hook = NoHook>
; __device__ __forceinline__ void gemm_phase_w(LAS unsigned char* lds, const Sched& S, const Epi& E, int wave_id, const Hook& HK = Hook()) {
;     ...
;         if constexpr (!SEG2) {
;             for (int tt = 0; tt < nt; tt += 2) {
;                 if constexpr (GATHER) { if (tt == nt - 2) {
;                     if (has_next) { gnxt_00 = S.grow_l(nxt, lds, nbuf, R0) + (unsigned)(C0 * 2); gnxt_01 = S.grow_l(nxt, lds, nbuf, R1) + (unsigned)(C1 * 2); gnxt_10 = S.grow_l(nxt, lds, nbuf, 128 + R0) + (unsigned)(C0 * 2); gnxt_11 = S.grow_l(nxt, lds, nbuf, 128 + R1) + (unsigned)(C1 * 2); }
;                     else { gnxt_00 = gcur_00; gnxt_01 = gcur_01; gnxt_10 = gcur_10; gnxt_11 = gcur_11; } } }
;                 PG_TRIP(tt, false, false, false);
;             }
	s_bitset1_b32 s44, 7
	s_add_i32 s41, s44, s41
	s_ashr_i32 s43, s41, 31
	s_add_u32 s42, s20, s41
	s_addc_u32 s43, s21, s43
	s_add_i32 s41, s59, s22
	v_lshl_add_u64 v[204:205], s[42:43], 0, v[144:145]
	s_mov_b32 m0, s41
	ds_read_b128 v[172:175], v159 offset:49152
	ds_read_b128 v[176:179], v159 offset:50176
	ds_read_b128 v[180:183], v159 offset:51200
	ds_read_b128 v[184:187], v159 offset:52224
	ds_read_b128 v[188:191], v159 offset:53248
	ds_read_b128 v[192:195], v159 offset:54272
	ds_read_b128 v[196:199], v159 offset:55296
	ds_read_b128 v[200:203], v159 offset:56320
	global_load_lds_dwordx4 v[204:205], off
	s_add_i32 m0, s41, 0x2000
	s_add_i32 s41, s44, s45
	v_lshl_add_u64 v[204:205], s[42:43], 0, v[146:147]
	s_ashr_i32 s43, s41, 31
	s_add_u32 s42, s20, s41
	s_addc_u32 s43, s21, s43
	s_add_i32 s41, s60, s22
	global_load_lds_dwordx4 v[204:205], off
	v_lshl_add_u64 v[204:205], s[42:43], 0, v[144:145]
	s_mov_b32 m0, s41
	s_add_i32 s44, s44, s40
	global_load_lds_dwordx4 v[204:205], off
	s_add_i32 m0, s41, 0x2000
	s_add_u32 s40, s4, s44
	v_lshl_add_u64 v[204:205], s[42:43], 0, v[146:147]
	s_addc_u32 s41, s5, 0
	global_load_lds_dwordx4 v[204:205], off
	v_lshl_add_u64 v[204:205], s[40:41], 0, v[144:145]
	s_mov_b32 m0, s28
	s_nop 0
	global_load_lds_dwordx4 v[204:205], off
	v_lshl_add_u64 v[204:205], s[40:41], 0, v[146:147]
	s_mov_b32 m0, s6
	s_nop 0
	global_load_lds_dwordx4 v[204:205], off
	s_waitcnt vmcnt(8)
	s_waitcnt lgkmcnt(0)
	s_barrier
	s_waitcnt lgkmcnt(0)
	v_mfma_f32_16x16x32_bf16 v[60:63], v[116:119], v[172:175], v[60:63]
	v_mfma_f32_16x16x32_bf16 v[56:59], v[128:131], v[172:175], v[56:59]
	v_mfma_f32_16x16x32_bf16 v[48:51], v[116:119], v[180:183], v[48:51]
	v_mfma_f32_16x16x32_bf16 v[40:43], v[128:131], v[180:183], v[40:43]
	v_mfma_f32_16x16x32_bf16 v[32:35], v[116:119], v[188:191], v[32:35]
	v_mfma_f32_16x16x32_bf16 v[24:27], v[128:131], v[188:191], v[24:27]
	v_mfma_f32_16x16x32_bf16 v[16:19], v[116:119], v[196:199], v[16:19]
	v_mfma_f32_16x16x32_bf16 v[8:11], v[128:131], v[196:199], v[8:11]
	v_mfma_f32_16x16x32_bf16 v[60:63], v[120:123], v[176:179], v[60:63]
	v_mfma_f32_16x16x32_bf16 v[56:59], v[132:135], v[176:179], v[56:59]
	v_mfma_f32_16x16x32_bf16 v[48:51], v[120:123], v[184:187], v[48:51]
	v_mfma_f32_16x16x32_bf16 v[40:43], v[132:135], v[184:187], v[40:43]
	v_mfma_f32_16x16x32_bf16 v[32:35], v[120:123], v[192:195], v[32:35]
	v_mfma_f32_16x16x32_bf16 v[24:27], v[132:135], v[192:195], v[24:27]
	v_mfma_f32_16x16x32_bf16 v[16:19], v[120:123], v[200:203], v[16:19]
	v_mfma_f32_16x16x32_bf16 v[8:11], v[132:135], v[200:203], v[8:11]
	v_mfma_f32_16x16x32_bf16 v[52:55], v[150:153], v[172:175], v[52:55]
	v_mfma_f32_16x16x32_bf16 v[44:47], v[164:167], v[172:175], v[44:47]
	v_mfma_f32_16x16x32_bf16 v[36:39], v[150:153], v[180:183], v[36:39]
	v_mfma_f32_16x16x32_bf16 v[28:31], v[164:167], v[180:183], v[28:31]
	v_mfma_f32_16x16x32_bf16 v[20:23], v[150:153], v[188:191], v[20:23]
	v_mfma_f32_16x16x32_bf16 v[12:15], v[164:167], v[188:191], v[12:15]
	v_mfma_f32_16x16x32_bf16 v[4:7], v[150:153], v[196:199], v[4:7]
	v_mfma_f32_16x16x32_bf16 v[0:3], v[164:167], v[196:199], v[0:3]
	v_mfma_f32_16x16x32_bf16 v[52:55], v[160:163], v[176:179], v[52:55]
	v_mfma_f32_16x16x32_bf16 v[44:47], v[168:171], v[176:179], v[44:47]
	v_mfma_f32_16x16x32_bf16 v[36:39], v[160:163], v[184:187], v[36:39]
	v_mfma_f32_16x16x32_bf16 v[28:31], v[168:171], v[184:187], v[28:31]
	v_mfma_f32_16x16x32_bf16 v[20:23], v[160:163], v[192:195], v[20:23]
	v_mfma_f32_16x16x32_bf16 v[12:15], v[168:171], v[192:195], v[12:15]
	v_mfma_f32_16x16x32_bf16 v[4:7], v[160:163], v[200:203], v[4:7]
	v_mfma_f32_16x16x32_bf16 v[0:3], v[168:171], v[200:203], v[0:3]
	s_barrier
	s_addk_i32 s18, 0x100
	s_add_i32 s19, s19, 2
	s_cmp_gt_u32 s19, 29
	s_cbranch_scc0 .LBB0_654
	s_and_b64 vcc, exec, s[14:15]
	s_cbranch_vccz .LBB0_657
	s_barrier

; template <class Epi, class Sched, class Hook = NoHook>
; __device__ __forceinline__ void gemm_phase_w(LAS unsigned char* lds, const Sched& S, const Epi& E, int wave_id, const Hook& HK = Hook()) {
;     ...
;                     if (has_next) { gnxt_00 = S.grow_l(nxt, lds, nbuf, R0) + (unsigned)(C0 * 2); gnxt_01 = S.grow_l(nxt, lds, nbuf, R1) + (unsigned)(C1 * 2); gnxt_10 = S.grow_l(nxt, lds, nbuf, 128 + R0) + (unsigned)(C0 * 2); gnxt_11 = S.grow_l(nxt, lds, nbuf, 128 + R1) + (unsigned)(C1 * 2); }
.LBB0_827:
	v_add_u32_e32 v147, s73, v166
	ds_read_b128 v[186:189], v147
	ds_read_b128 v[190:193], v147 offset:1024
	ds_read_b128 v[194:197], v147 offset:2048
	ds_read_b128 v[198:201], v147 offset:3072
	v_add_u32_e32 v147, s74, v166
	ds_read_b128 v[202:205], v147
	ds_read_b128 v[206:209], v147 offset:1024
	ds_read_b128 v[210:213], v147 offset:2048
	ds_read_b128 v[214:217], v147 offset:3072
	v_lshl_add_u64 v[250:251], s[38:39], 0, v[130:131]
	s_add_i32 m0, s62, 0xc000
	ds_read_b128 v[218:221], v182
	ds_read_b128 v[222:225], v182 offset:1024
	ds_read_b128 v[226:229], v182 offset:2048
	ds_read_b128 v[230:233], v182 offset:3072
	ds_read_b128 v[234:237], v182 offset:4096
	ds_read_b128 v[238:241], v182 offset:5120
	ds_read_b128 v[242:245], v182 offset:6144
	ds_read_b128 v[246:249], v182 offset:7168
	global_load_lds_dwordx4 v[250:251], off
	v_lshl_add_u64 v[250:251], s[38:39], 0, v[132:133]
	s_add_i32 m0, s62, 0xe000
	s_nop 0
	global_load_lds_dwordx4 v[250:251], off
	s_waitcnt vmcnt(8)
	s_waitcnt lgkmcnt(0)
	s_barrier
	s_waitcnt lgkmcnt(0)
	v_mfma_f32_16x16x32_bf16 v[124:127], v[186:189], v[218:221], v[124:127]
	v_mfma_f32_16x16x32_bf16 v[120:123], v[194:197], v[218:221], v[120:123]
	v_mfma_f32_16x16x32_bf16 v[108:111], v[186:189], v[226:229], v[108:111]
	v_mfma_f32_16x16x32_bf16 v[104:107], v[194:197], v[226:229], v[104:107]
	v_mfma_f32_16x16x32_bf16 v[92:95], v[186:189], v[234:237], v[92:95]
	v_mfma_f32_16x16x32_bf16 v[88:91], v[194:197], v[234:237], v[88:91]
	v_mfma_f32_16x16x32_bf16 v[76:79], v[186:189], v[242:245], v[76:79]
	v_mfma_f32_16x16x32_bf16 v[72:75], v[194:197], v[242:245], v[72:75]
	v_mfma_f32_16x16x32_bf16 v[124:127], v[190:193], v[222:225], v[124:127]
	v_mfma_f32_16x16x32_bf16 v[120:123], v[198:201], v[222:225], v[120:123]
	v_mfma_f32_16x16x32_bf16 v[108:111], v[190:193], v[230:233], v[108:111]
	v_mfma_f32_16x16x32_bf16 v[104:107], v[198:201], v[230:233], v[104:107]
	v_mfma_f32_16x16x32_bf16 v[92:95], v[190:193], v[238:241], v[92:95]
	v_mfma_f32_16x16x32_bf16 v[88:91], v[198:201], v[238:241], v[88:91]
	v_mfma_f32_16x16x32_bf16 v[76:79], v[190:193], v[246:249], v[76:79]
	v_mfma_f32_16x16x32_bf16 v[72:75], v[198:201], v[246:249], v[72:75]
	v_mfma_f32_16x16x32_bf16 v[116:119], v[202:205], v[218:221], v[116:119]
	v_mfma_f32_16x16x32_bf16 v[112:115], v[210:213], v[218:221], v[112:115]
	v_mfma_f32_16x16x32_bf16 v[100:103], v[202:205], v[226:229], v[100:103]
	v_mfma_f32_16x16x32_bf16 v[96:99], v[210:213], v[226:229], v[96:99]
	v_mfma_f32_16x16x32_bf16 v[84:87], v[202:205], v[234:237], v[84:87]
	v_mfma_f32_16x16x32_bf16 v[80:83], v[210:213], v[234:237], v[80:83]
	v_mfma_f32_16x16x32_bf16 v[68:71], v[202:205], v[242:245], v[68:71]
	v_mfma_f32_16x16x32_bf16 v[64:67], v[210:213], v[242:245], v[64:67]
	v_mfma_f32_16x16x32_bf16 v[116:119], v[206:209], v[222:225], v[116:119]
	v_mfma_f32_16x16x32_bf16 v[112:115], v[214:217], v[222:225], v[112:115]
	v_mfma_f32_16x16x32_bf16 v[100:103], v[206:209], v[230:233], v[100:103]
	v_mfma_f32_16x16x32_bf16 v[96:99], v[214:217], v[230:233], v[96:99]
	v_mfma_f32_16x16x32_bf16 v[84:87], v[206:209], v[238:241], v[84:87]
	v_mfma_f32_16x16x32_bf16 v[80:83], v[214:217], v[238:241], v[80:83]
	v_mfma_f32_16x16x32_bf16 v[68:71], v[206:209], v[246:249], v[68:71]
	v_mfma_f32_16x16x32_bf16 v[64:67], v[214:217], v[246:249], v[64:67]
	s_barrier
	s_and_b64 s[40:41], s[40:41], exec
	s_cselect_b32 s22, 0, s97
	s_add_i32 s48, vcc_lo, s22
	s_ashr_i32 s41, s48, 31
	s_add_u32 s40, s16, s48
	s_addc_u32 s41, s17, s41
	s_add_i32 s49, s73, s44
	v_lshl_add_u64 v[250:251], s[40:41], 0, v[136:137]
	s_mov_b32 m0, s49
	s_add_i32 s48, s48, 0x80000
	ds_read_b128 v[218:221], v182 offset:16384
	ds_read_b128 v[222:225], v182 offset:17408
	ds_read_b128 v[226:229], v182 offset:18432
	ds_read_b128 v[230:233], v182 offset:19456
	ds_read_b128 v[234:237], v182 offset:20480
	ds_read_b128 v[238:241], v182 offset:21504
	ds_read_b128 v[242:245], v182 offset:22528
	ds_read_b128 v[246:249], v182 offset:23552
	global_load_lds_dwordx4 v[250:251], off
	v_lshl_add_u64 v[250:251], s[40:41], 0, v[138:139]
	s_add_i32 m0, s49, 0x2000
	s_ashr_i32 s41, s48, 31
	s_add_u32 s40, s16, s48
	s_addc_u32 s41, s17, s41
	s_add_i32 s48, s74, s44
	global_load_lds_dwordx4 v[250:251], off
	v_lshl_add_u64 v[250:251], s[40:41], 0, v[136:137]
	s_mov_b32 m0, s48
	v_mov_b32_e32 v147, v141
	global_load_lds_dwordx4 v[250:251], off
	s_add_i32 m0, s48, 0x2000
	v_lshl_add_u64 v[250:251], s[40:41], 0, v[138:139]
	s_add_u32 s40, s14, s22
	global_load_lds_dwordx4 v[250:251], off
	s_addc_u32 s41, s15, 0
	s_mov_b32 m0, s62
	s_nop 0
	global_load_lds_dwordx4 v140, s[40:41]
	s_mov_b32 m0, s63
	s_nop 0
	global_load_lds_dwordx4 v146, s[40:41]
	s_waitcnt vmcnt(8)
	s_waitcnt lgkmcnt(0)
	s_barrier
	s_waitcnt lgkmcnt(0)
	v_mfma_f32_16x16x32_bf16 v[60:63], v[186:189], v[218:221], v[60:63]
	v_mfma_f32_16x16x32_bf16 v[56:59], v[194:197], v[218:221], v[56:59]
	v_mfma_f32_16x16x32_bf16 v[44:47], v[186:189], v[226:229], v[44:47]
	v_mfma_f32_16x16x32_bf16 v[40:43], v[194:197], v[226:229], v[40:43]
	v_mfma_f32_16x16x32_bf16 v[28:31], v[186:189], v[234:237], v[28:31]
	v_mfma_f32_16x16x32_bf16 v[24:27], v[194:197], v[234:237], v[24:27]
	v_mfma_f32_16x16x32_bf16 v[12:15], v[186:189], v[242:245], v[12:15]
	v_mfma_f32_16x16x32_bf16 v[8:11], v[194:197], v[242:245], v[8:11]
	v_mfma_f32_16x16x32_bf16 v[60:63], v[190:193], v[222:225], v[60:63]
	v_mfma_f32_16x16x32_bf16 v[56:59], v[198:201], v[222:225], v[56:59]
	v_mfma_f32_16x16x32_bf16 v[44:47], v[190:193], v[230:233], v[44:47]
	v_mfma_f32_16x16x32_bf16 v[40:43], v[198:201], v[230:233], v[40:43]
	v_mfma_f32_16x16x32_bf16 v[28:31], v[190:193], v[238:241], v[28:31]
	v_mfma_f32_16x16x32_bf16 v[24:27], v[198:201], v[238:241], v[24:27]
	v_mfma_f32_16x16x32_bf16 v[12:15], v[190:193], v[246:249], v[12:15]
	v_mfma_f32_16x16x32_bf16 v[8:11], v[198:201], v[246:249], v[8:11]
	v_mfma_f32_16x16x32_bf16 v[52:55], v[202:205], v[218:221], v[52:55]
	v_mfma_f32_16x16x32_bf16 v[48:51], v[210:213], v[218:221], v[48:51]
	v_mfma_f32_16x16x32_bf16 v[36:39], v[202:205], v[226:229], v[36:39]
	v_mfma_f32_16x16x32_bf16 v[32:35], v[210:213], v[226:229], v[32:35]
	v_mfma_f32_16x16x32_bf16 v[20:23], v[202:205], v[234:237], v[20:23]
	v_mfma_f32_16x16x32_bf16 v[16:19], v[210:213], v[234:237], v[16:19]
	v_mfma_f32_16x16x32_bf16 v[4:7], v[202:205], v[242:245], v[4:7]
	v_mfma_f32_16x16x32_bf16 v[0:3], v[210:213], v[242:245], v[0:3]
	v_mfma_f32_16x16x32_bf16 v[52:55], v[206:209], v[222:225], v[52:55]
	v_mfma_f32_16x16x32_bf16 v[48:51], v[214:217], v[222:225], v[48:51]
	v_mfma_f32_16x16x32_bf16 v[36:39], v[206:209], v[230:233], v[36:39]
	v_mfma_f32_16x16x32_bf16 v[32:35], v[214:217], v[230:233], v[32:35]
	v_mfma_f32_16x16x32_bf16 v[20:23], v[206:209], v[238:241], v[20:23]
	v_mfma_f32_16x16x32_bf16 v[16:19], v[214:217], v[238:241], v[16:19]
	v_mfma_f32_16x16x32_bf16 v[4:7], v[206:209], v[246:249], v[4:7]
	v_mfma_f32_16x16x32_bf16 v[0:3], v[214:217], v[246:249], v[0:3]
	s_barrier
	s_add_i32 s48, 0, 0x18000
	v_add_u32_e32 v185, s48, v166
	s_add_i32 s49, 0, 0x1c000
	ds_read_b128 v[186:189], v185
	ds_read_b128 v[190:193], v185 offset:1024
	ds_read_b128 v[194:197], v185 offset:2048
	ds_read_b128 v[198:201], v185 offset:3072
	v_add_u32_e32 v185, s49, v166
	ds_read_b128 v[202:205], v185
	ds_read_b128 v[206:209], v185 offset:1024
	ds_read_b128 v[210:213], v185 offset:2048
	ds_read_b128 v[214:217], v185 offset:3072
	s_mov_b32 m0, s66
	v_lshl_add_u64 v[148:149], s[40:41], 0, v[148:149]
	ds_read_b128 v[218:221], v182 offset:32768
	ds_read_b128 v[222:225], v182 offset:33792
	ds_read_b128 v[226:229], v182 offset:34816
	ds_read_b128 v[230:233], v182 offset:35840
	ds_read_b128 v[234:237], v182 offset:36864
	ds_read_b128 v[238:241], v182 offset:37888
	ds_read_b128 v[242:245], v182 offset:38912
	ds_read_b128 v[246:249], v182 offset:39936
	global_load_lds_dwordx4 v[148:149], off
	v_lshl_add_u64 v[148:149], s[40:41], 0, v[150:151]
	s_mov_b32 m0, s67
	s_nop 0
	global_load_lds_dwordx4 v[148:149], off
	s_waitcnt vmcnt(8)
	s_waitcnt lgkmcnt(0)
	s_barrier
	s_waitcnt lgkmcnt(0)
	v_mfma_f32_16x16x32_bf16 v[124:127], v[186:189], v[218:221], v[124:127]
	v_mfma_f32_16x16x32_bf16 v[120:123], v[194:197], v[218:221], v[120:123]
	v_mfma_f32_16x16x32_bf16 v[108:111], v[186:189], v[226:229], v[108:111]
	v_mfma_f32_16x16x32_bf16 v[104:107], v[194:197], v[226:229], v[104:107]
	v_mfma_f32_16x16x32_bf16 v[92:95], v[186:189], v[234:237], v[92:95]
	v_mfma_f32_16x16x32_bf16 v[88:91], v[194:197], v[234:237], v[88:91]
	v_mfma_f32_16x16x32_bf16 v[76:79], v[186:189], v[242:245], v[76:79]
	v_mfma_f32_16x16x32_bf16 v[72:75], v[194:197], v[242:245], v[72:75]
	v_mfma_f32_16x16x32_bf16 v[124:127], v[190:193], v[222:225], v[124:127]
	v_mfma_f32_16x16x32_bf16 v[120:123], v[198:201], v[222:225], v[120:123]
	v_mfma_f32_16x16x32_bf16 v[108:111], v[190:193], v[230:233], v[108:111]
	v_mfma_f32_16x16x32_bf16 v[104:107], v[198:201], v[230:233], v[104:107]
	v_mfma_f32_16x16x32_bf16 v[92:95], v[190:193], v[238:241], v[92:95]
	v_mfma_f32_16x16x32_bf16 v[88:91], v[198:201], v[238:241], v[88:91]
	v_mfma_f32_16x16x32_bf16 v[76:79], v[190:193], v[246:249], v[76:79]
	v_mfma_f32_16x16x32_bf16 v[72:75], v[198:201], v[246:249], v[72:75]
	v_mfma_f32_16x16x32_bf16 v[116:119], v[202:205], v[218:221], v[116:119]
	v_mfma_f32_16x16x32_bf16 v[112:115], v[210:213], v[218:221], v[112:115]
	v_mfma_f32_16x16x32_bf16 v[100:103], v[202:205], v[226:229], v[100:103]
	v_mfma_f32_16x16x32_bf16 v[96:99], v[210:213], v[226:229], v[96:99]
	v_mfma_f32_16x16x32_bf16 v[84:87], v[202:205], v[234:237], v[84:87]
	v_mfma_f32_16x16x32_bf16 v[80:83], v[210:213], v[234:237], v[80:83]
	v_mfma_f32_16x16x32_bf16 v[68:71], v[202:205], v[242:245], v[68:71]
	v_mfma_f32_16x16x32_bf16 v[64:67], v[210:213], v[242:245], v[64:67]
	v_mfma_f32_16x16x32_bf16 v[116:119], v[206:209], v[222:225], v[116:119]
	v_mfma_f32_16x16x32_bf16 v[112:115], v[214:217], v[222:225], v[112:115]
	v_mfma_f32_16x16x32_bf16 v[100:103], v[206:209], v[230:233], v[100:103]
	v_mfma_f32_16x16x32_bf16 v[96:99], v[214:217], v[230:233], v[96:99]
	v_mfma_f32_16x16x32_bf16 v[84:87], v[206:209], v[238:241], v[84:87]
	v_mfma_f32_16x16x32_bf16 v[80:83], v[214:217], v[238:241], v[80:83]
	v_mfma_f32_16x16x32_bf16 v[68:71], v[206:209], v[246:249], v[68:71]
	v_mfma_f32_16x16x32_bf16 v[64:67], v[214:217], v[246:249], v[64:67]
	s_barrier
; template <class Epi, class Sched, class Hook = NoHook>
; __device__ __forceinline__ void gemm_phase_w(LAS unsigned char* lds, const Sched& S, const Epi& E, int wave_id, const Hook& HK = Hook()) {
;     ...
;         if constexpr (!SEG2) {
;             for (int tt = 0; tt < nt; tt += 2) {
;                 if constexpr (GATHER) { if (tt == nt - 2) {
;                     if (has_next) { gnxt_00 = S.grow_l(nxt, lds, nbuf, R0) + (unsigned)(C0 * 2); gnxt_01 = S.grow_l(nxt, lds, nbuf, R1) + (unsigned)(C1 * 2); gnxt_10 = S.grow_l(nxt, lds, nbuf, 128 + R0) + (unsigned)(C0 * 2); gnxt_11 = S.grow_l(nxt, lds, nbuf, 128 + R1) + (unsigned)(C1 * 2); }
;                     else { gnxt_00 = gcur_00; gnxt_01 = gcur_01; gnxt_10 = gcur_10; gnxt_11 = gcur_11; } } }
;                 PG_TRIP(tt, false, false, false);
;             }
	s_bitset1_b32 s22, 7
	s_add_i32 vcc_lo, vcc_lo, s22
	s_ashr_i32 s41, vcc_lo, 31
	s_add_u32 s40, s16, vcc_lo
	s_addc_u32 s41, s17, s41
	s_add_i32 s48, s48, s44
	v_lshl_add_u64 v[246:247], s[40:41], 0, v[136:137]
	s_mov_b32 m0, s48
	s_add_i32 vcc_lo, vcc_lo, 0x80000
	ds_read_b128 v[148:151], v182 offset:49152
	ds_read_b128 v[218:221], v182 offset:50176
	ds_read_b128 v[222:225], v182 offset:51200
	ds_read_b128 v[226:229], v182 offset:52224
	ds_read_b128 v[230:233], v182 offset:53248
	ds_read_b128 v[234:237], v182 offset:54272
	ds_read_b128 v[238:241], v182 offset:55296
	ds_read_b128 v[242:245], v182 offset:56320
	global_load_lds_dwordx4 v[246:247], off
	v_lshl_add_u64 v[246:247], s[40:41], 0, v[138:139]
	s_add_i32 m0, s48, 0x2000
	s_ashr_i32 s41, vcc_lo, 31
	s_add_u32 s40, s16, vcc_lo
	s_addc_u32 s41, s17, s41
	s_add_i32 s48, s49, s44
	global_load_lds_dwordx4 v[246:247], off
	v_lshl_add_u64 v[246:247], s[40:41], 0, v[136:137]
	s_mov_b32 m0, s48
	v_lshl_add_u64 v[146:147], s[14:15], 0, v[146:147]
	global_load_lds_dwordx4 v[246:247], off
	v_lshl_add_u64 v[246:247], s[40:41], 0, v[138:139]
	s_add_i32 m0, s48, 0x2000
	v_lshl_add_u64 v[146:147], v[146:147], 0, s[22:23]
	global_load_lds_dwordx4 v[246:247], off
	v_lshl_add_u64 v[246:247], s[14:15], 0, v[140:141]
	v_lshl_add_u64 v[246:247], v[246:247], 0, s[22:23]
	s_mov_b32 m0, s68
	s_nop 0
	global_load_lds_dwordx4 v[246:247], off
	s_mov_b32 m0, s69
	s_nop 0
	global_load_lds_dwordx4 v[146:147], off
	s_waitcnt vmcnt(8)
	s_waitcnt lgkmcnt(0)
	s_barrier
	s_waitcnt lgkmcnt(0)
	v_mfma_f32_16x16x32_bf16 v[60:63], v[186:189], v[148:151], v[60:63]
	v_mfma_f32_16x16x32_bf16 v[56:59], v[194:197], v[148:151], v[56:59]
	v_mfma_f32_16x16x32_bf16 v[44:47], v[186:189], v[222:225], v[44:47]
	v_mfma_f32_16x16x32_bf16 v[40:43], v[194:197], v[222:225], v[40:43]
	v_mfma_f32_16x16x32_bf16 v[28:31], v[186:189], v[230:233], v[28:31]
	v_mfma_f32_16x16x32_bf16 v[24:27], v[194:197], v[230:233], v[24:27]
	v_mfma_f32_16x16x32_bf16 v[12:15], v[186:189], v[238:241], v[12:15]
	v_mfma_f32_16x16x32_bf16 v[8:11], v[194:197], v[238:241], v[8:11]
	v_mfma_f32_16x16x32_bf16 v[60:63], v[190:193], v[218:221], v[60:63]
	v_mfma_f32_16x16x32_bf16 v[56:59], v[198:201], v[218:221], v[56:59]
	v_mfma_f32_16x16x32_bf16 v[44:47], v[190:193], v[226:229], v[44:47]
	v_mfma_f32_16x16x32_bf16 v[40:43], v[198:201], v[226:229], v[40:43]
	v_mfma_f32_16x16x32_bf16 v[28:31], v[190:193], v[234:237], v[28:31]
	v_mfma_f32_16x16x32_bf16 v[24:27], v[198:201], v[234:237], v[24:27]
	v_mfma_f32_16x16x32_bf16 v[12:15], v[190:193], v[242:245], v[12:15]
	v_mfma_f32_16x16x32_bf16 v[8:11], v[198:201], v[242:245], v[8:11]
	v_mfma_f32_16x16x32_bf16 v[52:55], v[202:205], v[148:151], v[52:55]
	v_mfma_f32_16x16x32_bf16 v[48:51], v[210:213], v[148:151], v[48:51]
	v_mfma_f32_16x16x32_bf16 v[36:39], v[202:205], v[222:225], v[36:39]
	v_mfma_f32_16x16x32_bf16 v[32:35], v[210:213], v[222:225], v[32:35]
	v_mfma_f32_16x16x32_bf16 v[20:23], v[202:205], v[230:233], v[20:23]
	v_mfma_f32_16x16x32_bf16 v[16:19], v[210:213], v[230:233], v[16:19]
	v_mfma_f32_16x16x32_bf16 v[4:7], v[202:205], v[238:241], v[4:7]
	v_mfma_f32_16x16x32_bf16 v[0:3], v[210:213], v[238:241], v[0:3]
	v_mfma_f32_16x16x32_bf16 v[52:55], v[206:209], v[218:221], v[52:55]
	v_mfma_f32_16x16x32_bf16 v[48:51], v[214:217], v[218:221], v[48:51]
	v_mfma_f32_16x16x32_bf16 v[36:39], v[206:209], v[226:229], v[36:39]
	v_mfma_f32_16x16x32_bf16 v[32:35], v[214:217], v[226:229], v[32:35]
	v_mfma_f32_16x16x32_bf16 v[20:23], v[206:209], v[234:237], v[20:23]
	v_mfma_f32_16x16x32_bf16 v[16:19], v[214:217], v[234:237], v[16:19]
	v_mfma_f32_16x16x32_bf16 v[4:7], v[206:209], v[242:245], v[4:7]
	v_mfma_f32_16x16x32_bf16 v[0:3], v[214:217], v[242:245], v[0:3]
	s_barrier
	s_add_i32 s89, s89, 2
	s_addk_i32 s97, 0x100
	s_add_u32 s38, s38, 0x100
	s_addc_u32 s39, s39, 0
	s_cmp_gt_u32 s89, 29
	s_cbranch_scc1 .LBB0_831

; template <class Epi, class Sched, class Hook = NoHook>
; __device__ __forceinline__ void gemm_phase_w(LAS unsigned char* lds, const Sched& S, const Epi& E, int wave_id, const Hook& HK = Hook()) {
;     ...
;                     if (has_next) { gnxt_00 = S.grow_l(nxt, lds, nbuf, R0) + (unsigned)(C0 * 2); gnxt_01 = S.grow_l(nxt, lds, nbuf, R1) + (unsigned)(C1 * 2); gnxt_10 = S.grow_l(nxt, lds, nbuf, 128 + R0) + (unsigned)(C0 * 2); gnxt_11 = S.grow_l(nxt, lds, nbuf, 128 + R1) + (unsigned)(C1 * 2); }
.LBB0_1082:
	v_add_u32_e32 v147, s49, v163
	ds_read_b128 v[182:185], v147
	ds_read_b128 v[186:189], v147 offset:1024
	ds_read_b128 v[190:193], v147 offset:2048
	ds_read_b128 v[194:197], v147 offset:3072
	v_add_u32_e32 v147, s58, v163
	ds_read_b128 v[198:201], v147
	ds_read_b128 v[202:205], v147 offset:1024
	ds_read_b128 v[206:209], v147 offset:2048
	ds_read_b128 v[210:213], v147 offset:3072
	v_lshl_add_u64 v[246:247], s[38:39], 0, v[130:131]
	s_add_i32 m0, s63, 0xc000
	ds_read_b128 v[214:217], v179
	ds_read_b128 v[218:221], v179 offset:1024
	ds_read_b128 v[222:225], v179 offset:2048
	ds_read_b128 v[226:229], v179 offset:3072
	ds_read_b128 v[230:233], v179 offset:4096
	ds_read_b128 v[234:237], v179 offset:5120
	ds_read_b128 v[238:241], v179 offset:6144
	ds_read_b128 v[242:245], v179 offset:7168
	global_load_lds_dwordx4 v[246:247], off
	v_lshl_add_u64 v[246:247], s[38:39], 0, v[132:133]
	s_add_i32 m0, s63, 0xe000
	s_nop 0
	global_load_lds_dwordx4 v[246:247], off
	s_waitcnt vmcnt(8)
	s_waitcnt lgkmcnt(0)
	s_barrier
	s_waitcnt lgkmcnt(0)
	v_mfma_f32_16x16x32_bf16 v[124:127], v[182:185], v[214:217], v[124:127]
	v_mfma_f32_16x16x32_bf16 v[120:123], v[190:193], v[214:217], v[120:123]
	v_mfma_f32_16x16x32_bf16 v[108:111], v[182:185], v[222:225], v[108:111]
	v_mfma_f32_16x16x32_bf16 v[104:107], v[190:193], v[222:225], v[104:107]
	v_mfma_f32_16x16x32_bf16 v[92:95], v[182:185], v[230:233], v[92:95]
	v_mfma_f32_16x16x32_bf16 v[88:91], v[190:193], v[230:233], v[88:91]
	v_mfma_f32_16x16x32_bf16 v[76:79], v[182:185], v[238:241], v[76:79]
	v_mfma_f32_16x16x32_bf16 v[72:75], v[190:193], v[238:241], v[72:75]
	v_mfma_f32_16x16x32_bf16 v[124:127], v[186:189], v[218:221], v[124:127]
	v_mfma_f32_16x16x32_bf16 v[120:123], v[194:197], v[218:221], v[120:123]
	v_mfma_f32_16x16x32_bf16 v[108:111], v[186:189], v[226:229], v[108:111]
	v_mfma_f32_16x16x32_bf16 v[104:107], v[194:197], v[226:229], v[104:107]
	v_mfma_f32_16x16x32_bf16 v[92:95], v[186:189], v[234:237], v[92:95]
	v_mfma_f32_16x16x32_bf16 v[88:91], v[194:197], v[234:237], v[88:91]
	v_mfma_f32_16x16x32_bf16 v[76:79], v[186:189], v[242:245], v[76:79]
	v_mfma_f32_16x16x32_bf16 v[72:75], v[194:197], v[242:245], v[72:75]
	v_mfma_f32_16x16x32_bf16 v[116:119], v[198:201], v[214:217], v[116:119]
	v_mfma_f32_16x16x32_bf16 v[112:115], v[206:209], v[214:217], v[112:115]
	v_mfma_f32_16x16x32_bf16 v[100:103], v[198:201], v[222:225], v[100:103]
	v_mfma_f32_16x16x32_bf16 v[96:99], v[206:209], v[222:225], v[96:99]
	v_mfma_f32_16x16x32_bf16 v[84:87], v[198:201], v[230:233], v[84:87]
	v_mfma_f32_16x16x32_bf16 v[80:83], v[206:209], v[230:233], v[80:83]
	v_mfma_f32_16x16x32_bf16 v[68:71], v[198:201], v[238:241], v[68:71]
	v_mfma_f32_16x16x32_bf16 v[64:67], v[206:209], v[238:241], v[64:67]
	v_mfma_f32_16x16x32_bf16 v[116:119], v[202:205], v[218:221], v[116:119]
	v_mfma_f32_16x16x32_bf16 v[112:115], v[210:213], v[218:221], v[112:115]
	v_mfma_f32_16x16x32_bf16 v[100:103], v[202:205], v[226:229], v[100:103]
	v_mfma_f32_16x16x32_bf16 v[96:99], v[210:213], v[226:229], v[96:99]
	v_mfma_f32_16x16x32_bf16 v[84:87], v[202:205], v[234:237], v[84:87]
	v_mfma_f32_16x16x32_bf16 v[80:83], v[210:213], v[234:237], v[80:83]
	v_mfma_f32_16x16x32_bf16 v[68:71], v[202:205], v[242:245], v[68:71]
	v_mfma_f32_16x16x32_bf16 v[64:67], v[210:213], v[242:245], v[64:67]
	s_barrier
	s_and_b64 s[40:41], s[40:41], exec
	s_cselect_b32 s22, 0, s78
	s_add_i32 s84, s79, s22
	s_ashr_i32 s41, s84, 31
	s_add_u32 s40, s16, s84
	s_addc_u32 s41, s17, s41
	s_add_i32 s85, s49, s44
	v_lshl_add_u64 v[246:247], s[40:41], 0, v[136:137]
	s_mov_b32 m0, s85
	s_add_i32 s84, s84, 0x80000
	ds_read_b128 v[214:217], v179 offset:16384
	ds_read_b128 v[218:221], v179 offset:17408
	ds_read_b128 v[222:225], v179 offset:18432
	ds_read_b128 v[226:229], v179 offset:19456
	ds_read_b128 v[230:233], v179 offset:20480
	ds_read_b128 v[234:237], v179 offset:21504
	ds_read_b128 v[238:241], v179 offset:22528
	ds_read_b128 v[242:245], v179 offset:23552
	global_load_lds_dwordx4 v[246:247], off
	v_lshl_add_u64 v[246:247], s[40:41], 0, v[138:139]
	s_add_i32 m0, s85, 0x2000
	s_ashr_i32 s41, s84, 31
	s_add_u32 s40, s16, s84
	s_addc_u32 s41, s17, s41
	s_add_i32 s84, s58, s44
	global_load_lds_dwordx4 v[246:247], off
	v_lshl_add_u64 v[246:247], s[40:41], 0, v[136:137]
	s_mov_b32 m0, s84
	v_mov_b32_e32 v147, v141
	global_load_lds_dwordx4 v[246:247], off
	s_add_i32 m0, s84, 0x2000
	v_lshl_add_u64 v[246:247], s[40:41], 0, v[138:139]
	s_add_u32 s40, s14, s22
	global_load_lds_dwordx4 v[246:247], off
	s_addc_u32 s41, s15, 0
	s_mov_b32 m0, s63
	s_nop 0
	global_load_lds_dwordx4 v140, s[40:41]
	s_mov_b32 m0, s66
	s_nop 0
	global_load_lds_dwordx4 v146, s[40:41]
	s_waitcnt vmcnt(8)
	s_waitcnt lgkmcnt(0)
	s_barrier
	s_waitcnt lgkmcnt(0)
	v_mfma_f32_16x16x32_bf16 v[60:63], v[182:185], v[214:217], v[60:63]
	v_mfma_f32_16x16x32_bf16 v[56:59], v[190:193], v[214:217], v[56:59]
	v_mfma_f32_16x16x32_bf16 v[44:47], v[182:185], v[222:225], v[44:47]
	v_mfma_f32_16x16x32_bf16 v[40:43], v[190:193], v[222:225], v[40:43]
	v_mfma_f32_16x16x32_bf16 v[28:31], v[182:185], v[230:233], v[28:31]
	v_mfma_f32_16x16x32_bf16 v[24:27], v[190:193], v[230:233], v[24:27]
	v_mfma_f32_16x16x32_bf16 v[12:15], v[182:185], v[238:241], v[12:15]
	v_mfma_f32_16x16x32_bf16 v[8:11], v[190:193], v[238:241], v[8:11]
	v_mfma_f32_16x16x32_bf16 v[60:63], v[186:189], v[218:221], v[60:63]
	v_mfma_f32_16x16x32_bf16 v[56:59], v[194:197], v[218:221], v[56:59]
	v_mfma_f32_16x16x32_bf16 v[44:47], v[186:189], v[226:229], v[44:47]
	v_mfma_f32_16x16x32_bf16 v[40:43], v[194:197], v[226:229], v[40:43]
	v_mfma_f32_16x16x32_bf16 v[28:31], v[186:189], v[234:237], v[28:31]
	v_mfma_f32_16x16x32_bf16 v[24:27], v[194:197], v[234:237], v[24:27]
	v_mfma_f32_16x16x32_bf16 v[12:15], v[186:189], v[242:245], v[12:15]
	v_mfma_f32_16x16x32_bf16 v[8:11], v[194:197], v[242:245], v[8:11]
	v_mfma_f32_16x16x32_bf16 v[52:55], v[198:201], v[214:217], v[52:55]
	v_mfma_f32_16x16x32_bf16 v[48:51], v[206:209], v[214:217], v[48:51]
	v_mfma_f32_16x16x32_bf16 v[36:39], v[198:201], v[222:225], v[36:39]
	v_mfma_f32_16x16x32_bf16 v[32:35], v[206:209], v[222:225], v[32:35]
	v_mfma_f32_16x16x32_bf16 v[20:23], v[198:201], v[230:233], v[20:23]
	v_mfma_f32_16x16x32_bf16 v[16:19], v[206:209], v[230:233], v[16:19]
	v_mfma_f32_16x16x32_bf16 v[4:7], v[198:201], v[238:241], v[4:7]
	v_mfma_f32_16x16x32_bf16 v[0:3], v[206:209], v[238:241], v[0:3]
	v_mfma_f32_16x16x32_bf16 v[52:55], v[202:205], v[218:221], v[52:55]
	v_mfma_f32_16x16x32_bf16 v[48:51], v[210:213], v[218:221], v[48:51]
	v_mfma_f32_16x16x32_bf16 v[36:39], v[202:205], v[226:229], v[36:39]
	v_mfma_f32_16x16x32_bf16 v[32:35], v[210:213], v[226:229], v[32:35]
	v_mfma_f32_16x16x32_bf16 v[20:23], v[202:205], v[234:237], v[20:23]
	v_mfma_f32_16x16x32_bf16 v[16:19], v[210:213], v[234:237], v[16:19]
	v_mfma_f32_16x16x32_bf16 v[4:7], v[202:205], v[242:245], v[4:7]
	v_mfma_f32_16x16x32_bf16 v[0:3], v[210:213], v[242:245], v[0:3]
	s_barrier
	s_add_i32 s84, 0, 0x18000
	s_add_i32 s85, 0, 0x1c000
	v_add_u32_e32 v194, s84, v163
	v_add_u32_e32 v210, s85, v163
	ds_read_b128 v[182:185], v194
	ds_read_b128 v[186:189], v194 offset:1024
	ds_read_b128 v[190:193], v194 offset:2048
	ds_read_b128 v[194:197], v194 offset:3072
	ds_read_b128 v[198:201], v210
	ds_read_b128 v[202:205], v210 offset:1024
	ds_read_b128 v[206:209], v210 offset:2048
	ds_read_b128 v[210:213], v210 offset:3072
	s_mov_b32 m0, s67
	v_lshl_add_u64 v[148:149], s[40:41], 0, v[148:149]
	ds_read_b128 v[214:217], v179 offset:32768
	ds_read_b128 v[218:221], v179 offset:33792
	ds_read_b128 v[222:225], v179 offset:34816
	ds_read_b128 v[226:229], v179 offset:35840
	ds_read_b128 v[230:233], v179 offset:36864
	ds_read_b128 v[234:237], v179 offset:37888
	ds_read_b128 v[238:241], v179 offset:38912
	ds_read_b128 v[242:245], v179 offset:39936
	global_load_lds_dwordx4 v[148:149], off
	v_lshl_add_u64 v[148:149], s[40:41], 0, v[150:151]
	s_mov_b32 m0, s68
	s_nop 0
	global_load_lds_dwordx4 v[148:149], off
	s_waitcnt vmcnt(8)
	s_waitcnt lgkmcnt(0)
	s_barrier
	s_waitcnt lgkmcnt(0)
	v_mfma_f32_16x16x32_bf16 v[124:127], v[182:185], v[214:217], v[124:127]
	v_mfma_f32_16x16x32_bf16 v[120:123], v[190:193], v[214:217], v[120:123]
	v_mfma_f32_16x16x32_bf16 v[108:111], v[182:185], v[222:225], v[108:111]
	v_mfma_f32_16x16x32_bf16 v[104:107], v[190:193], v[222:225], v[104:107]
	v_mfma_f32_16x16x32_bf16 v[92:95], v[182:185], v[230:233], v[92:95]
	v_mfma_f32_16x16x32_bf16 v[88:91], v[190:193], v[230:233], v[88:91]
	v_mfma_f32_16x16x32_bf16 v[76:79], v[182:185], v[238:241], v[76:79]
	v_mfma_f32_16x16x32_bf16 v[72:75], v[190:193], v[238:241], v[72:75]
	v_mfma_f32_16x16x32_bf16 v[124:127], v[186:189], v[218:221], v[124:127]
	v_mfma_f32_16x16x32_bf16 v[120:123], v[194:197], v[218:221], v[120:123]
	v_mfma_f32_16x16x32_bf16 v[108:111], v[186:189], v[226:229], v[108:111]
	v_mfma_f32_16x16x32_bf16 v[104:107], v[194:197], v[226:229], v[104:107]
	v_mfma_f32_16x16x32_bf16 v[92:95], v[186:189], v[234:237], v[92:95]
	v_mfma_f32_16x16x32_bf16 v[88:91], v[194:197], v[234:237], v[88:91]
	v_mfma_f32_16x16x32_bf16 v[76:79], v[186:189], v[242:245], v[76:79]
	v_mfma_f32_16x16x32_bf16 v[72:75], v[194:197], v[242:245], v[72:75]
	v_mfma_f32_16x16x32_bf16 v[116:119], v[198:201], v[214:217], v[116:119]
	v_mfma_f32_16x16x32_bf16 v[112:115], v[206:209], v[214:217], v[112:115]
	v_mfma_f32_16x16x32_bf16 v[100:103], v[198:201], v[222:225], v[100:103]
	v_mfma_f32_16x16x32_bf16 v[96:99], v[206:209], v[222:225], v[96:99]
	v_mfma_f32_16x16x32_bf16 v[84:87], v[198:201], v[230:233], v[84:87]
	v_mfma_f32_16x16x32_bf16 v[80:83], v[206:209], v[230:233], v[80:83]
	v_mfma_f32_16x16x32_bf16 v[68:71], v[198:201], v[238:241], v[68:71]
	v_mfma_f32_16x16x32_bf16 v[64:67], v[206:209], v[238:241], v[64:67]
	v_mfma_f32_16x16x32_bf16 v[116:119], v[202:205], v[218:221], v[116:119]
	v_mfma_f32_16x16x32_bf16 v[112:115], v[210:213], v[218:221], v[112:115]
	v_mfma_f32_16x16x32_bf16 v[100:103], v[202:205], v[226:229], v[100:103]
	v_mfma_f32_16x16x32_bf16 v[96:99], v[210:213], v[226:229], v[96:99]
	v_mfma_f32_16x16x32_bf16 v[84:87], v[202:205], v[234:237], v[84:87]
	v_mfma_f32_16x16x32_bf16 v[80:83], v[210:213], v[234:237], v[80:83]
	v_mfma_f32_16x16x32_bf16 v[68:71], v[202:205], v[242:245], v[68:71]
	v_mfma_f32_16x16x32_bf16 v[64:67], v[210:213], v[242:245], v[64:67]
	s_barrier
; template <class Epi, class Sched, class Hook = NoHook>
; __device__ __forceinline__ void gemm_phase_w(LAS unsigned char* lds, const Sched& S, const Epi& E, int wave_id, const Hook& HK = Hook()) {
;     ...
;         if constexpr (!SEG2) {
;             for (int tt = 0; tt < nt; tt += 2) {
;                 if constexpr (GATHER) { if (tt == nt - 2) {
;                     if (has_next) { gnxt_00 = S.grow_l(nxt, lds, nbuf, R0) + (unsigned)(C0 * 2); gnxt_01 = S.grow_l(nxt, lds, nbuf, R1) + (unsigned)(C1 * 2); gnxt_10 = S.grow_l(nxt, lds, nbuf, 128 + R0) + (unsigned)(C0 * 2); gnxt_11 = S.grow_l(nxt, lds, nbuf, 128 + R1) + (unsigned)(C1 * 2); }
;                     else { gnxt_00 = gcur_00; gnxt_01 = gcur_01; gnxt_10 = gcur_10; gnxt_11 = gcur_11; } } }
;                 PG_TRIP(tt, false, false, false);
;             }
	s_bitset1_b32 s22, 7
	s_add_i32 s79, s79, s22
	s_ashr_i32 s41, s79, 31
	s_add_u32 s40, s16, s79
	s_addc_u32 s41, s17, s41
	s_add_i32 s84, s84, s44
	v_lshl_add_u64 v[242:243], s[40:41], 0, v[136:137]
	s_mov_b32 m0, s84
	s_add_i32 s79, s79, 0x80000
	ds_read_b128 v[148:151], v179 offset:49152
	ds_read_b128 v[214:217], v179 offset:50176
	ds_read_b128 v[218:221], v179 offset:51200
	ds_read_b128 v[222:225], v179 offset:52224
	ds_read_b128 v[226:229], v179 offset:53248
	ds_read_b128 v[230:233], v179 offset:54272
	ds_read_b128 v[234:237], v179 offset:55296
	ds_read_b128 v[238:241], v179 offset:56320
	global_load_lds_dwordx4 v[242:243], off
	v_lshl_add_u64 v[242:243], s[40:41], 0, v[138:139]
	s_add_i32 m0, s84, 0x2000
	s_ashr_i32 s41, s79, 31
	s_add_u32 s40, s16, s79
	s_addc_u32 s41, s17, s41
	s_add_i32 s79, s85, s44
	global_load_lds_dwordx4 v[242:243], off
	v_lshl_add_u64 v[242:243], s[40:41], 0, v[136:137]
	s_mov_b32 m0, s79
	v_lshl_add_u64 v[146:147], s[14:15], 0, v[146:147]
	global_load_lds_dwordx4 v[242:243], off
	v_lshl_add_u64 v[242:243], s[40:41], 0, v[138:139]
	s_add_i32 m0, s79, 0x2000
	v_lshl_add_u64 v[146:147], v[146:147], 0, s[22:23]
	global_load_lds_dwordx4 v[242:243], off
	v_lshl_add_u64 v[242:243], s[14:15], 0, v[140:141]
	v_lshl_add_u64 v[242:243], v[242:243], 0, s[22:23]
	s_mov_b32 m0, s59
	s_nop 0
	global_load_lds_dwordx4 v[242:243], off
	s_mov_b32 m0, s69
	s_nop 0
	global_load_lds_dwordx4 v[146:147], off
	s_waitcnt vmcnt(8)
	s_waitcnt lgkmcnt(0)
	s_barrier
	s_waitcnt lgkmcnt(0)
	v_mfma_f32_16x16x32_bf16 v[60:63], v[182:185], v[148:151], v[60:63]
	v_mfma_f32_16x16x32_bf16 v[56:59], v[190:193], v[148:151], v[56:59]
	v_mfma_f32_16x16x32_bf16 v[44:47], v[182:185], v[218:221], v[44:47]
	v_mfma_f32_16x16x32_bf16 v[40:43], v[190:193], v[218:221], v[40:43]
	v_mfma_f32_16x16x32_bf16 v[28:31], v[182:185], v[226:229], v[28:31]
	v_mfma_f32_16x16x32_bf16 v[24:27], v[190:193], v[226:229], v[24:27]
	v_mfma_f32_16x16x32_bf16 v[12:15], v[182:185], v[234:237], v[12:15]
	v_mfma_f32_16x16x32_bf16 v[8:11], v[190:193], v[234:237], v[8:11]
	v_mfma_f32_16x16x32_bf16 v[60:63], v[186:189], v[214:217], v[60:63]
	v_mfma_f32_16x16x32_bf16 v[56:59], v[194:197], v[214:217], v[56:59]
	v_mfma_f32_16x16x32_bf16 v[44:47], v[186:189], v[222:225], v[44:47]
	v_mfma_f32_16x16x32_bf16 v[40:43], v[194:197], v[222:225], v[40:43]
	v_mfma_f32_16x16x32_bf16 v[28:31], v[186:189], v[230:233], v[28:31]
	v_mfma_f32_16x16x32_bf16 v[24:27], v[194:197], v[230:233], v[24:27]
	v_mfma_f32_16x16x32_bf16 v[12:15], v[186:189], v[238:241], v[12:15]
	v_mfma_f32_16x16x32_bf16 v[8:11], v[194:197], v[238:241], v[8:11]
	v_mfma_f32_16x16x32_bf16 v[52:55], v[198:201], v[148:151], v[52:55]
	v_mfma_f32_16x16x32_bf16 v[48:51], v[206:209], v[148:151], v[48:51]
	v_mfma_f32_16x16x32_bf16 v[36:39], v[198:201], v[218:221], v[36:39]
	v_mfma_f32_16x16x32_bf16 v[32:35], v[206:209], v[218:221], v[32:35]
	v_mfma_f32_16x16x32_bf16 v[20:23], v[198:201], v[226:229], v[20:23]
	v_mfma_f32_16x16x32_bf16 v[16:19], v[206:209], v[226:229], v[16:19]
	v_mfma_f32_16x16x32_bf16 v[4:7], v[198:201], v[234:237], v[4:7]
	v_mfma_f32_16x16x32_bf16 v[0:3], v[206:209], v[234:237], v[0:3]
	v_mfma_f32_16x16x32_bf16 v[52:55], v[202:205], v[214:217], v[52:55]
	v_mfma_f32_16x16x32_bf16 v[48:51], v[210:213], v[214:217], v[48:51]
	v_mfma_f32_16x16x32_bf16 v[36:39], v[202:205], v[222:225], v[36:39]
	v_mfma_f32_16x16x32_bf16 v[32:35], v[210:213], v[222:225], v[32:35]
	v_mfma_f32_16x16x32_bf16 v[20:23], v[202:205], v[230:233], v[20:23]
	v_mfma_f32_16x16x32_bf16 v[16:19], v[210:213], v[230:233], v[16:19]
	v_mfma_f32_16x16x32_bf16 v[4:7], v[202:205], v[238:241], v[4:7]
	v_mfma_f32_16x16x32_bf16 v[0:3], v[210:213], v[238:241], v[0:3]
	s_barrier
	s_add_i32 s77, s77, 2
	s_addk_i32 s78, 0x100
	s_add_u32 s38, s38, 0x100
	s_addc_u32 s39, s39, 0
	s_cmp_gt_u32 s77, 29
	s_cbranch_scc1 .LBB0_1086

.LBB0_1194:
	ds_read_b128 v[160:163], v156
	ds_read_b128 v[164:167], v156 offset:1024
	ds_read_b128 v[168:171], v156 offset:2048
	ds_read_b128 v[172:175], v156 offset:3072
	ds_read_b128 v[176:179], v157
	ds_read_b128 v[180:183], v157 offset:1024
	ds_read_b128 v[184:187], v157 offset:2048
	ds_read_b128 v[188:191], v157 offset:3072
	s_add_i32 s22, s68, s12
	s_add_u32 s36, s28, s22
	s_addc_u32 s37, s29, 0
	s_add_i32 m0, s26, 0xc000
	s_add_i32 s71, s26, 0xe000
	s_add_i32 s72, s12, 0xfffc0080
	s_cmp_eq_u32 s19, 12
	s_cselect_b32 s22, s63, s68
	s_cselect_b32 s23, s66, s69
	v_lshl_add_u64 v[224:225], s[36:37], 0, v[130:131]
	ds_read_b128 v[192:195], v158
	ds_read_b128 v[196:199], v158 offset:1024
	ds_read_b128 v[200:203], v158 offset:2048
	ds_read_b128 v[204:207], v158 offset:3072
	ds_read_b128 v[208:211], v158 offset:4096
	ds_read_b128 v[212:215], v158 offset:5120
	ds_read_b128 v[216:219], v158 offset:6144
	ds_read_b128 v[220:223], v158 offset:7168
	global_load_lds_dwordx4 v[224:225], off
	v_lshl_add_u64 v[224:225], s[36:37], 0, v[132:133]
	s_mov_b32 m0, s71
	s_nop 0
	global_load_lds_dwordx4 v[224:225], off
	s_waitcnt vmcnt(8)
	s_waitcnt lgkmcnt(0)
	s_barrier
	s_waitcnt lgkmcnt(0)
	v_mfma_f32_16x16x32_bf16 v[124:127], v[160:163], v[192:195], v[124:127]
	v_mfma_f32_16x16x32_bf16 v[120:123], v[168:171], v[192:195], v[120:123]
	v_mfma_f32_16x16x32_bf16 v[108:111], v[160:163], v[200:203], v[108:111]
	v_mfma_f32_16x16x32_bf16 v[104:107], v[168:171], v[200:203], v[104:107]
	v_mfma_f32_16x16x32_bf16 v[92:95], v[160:163], v[208:211], v[92:95]
	v_mfma_f32_16x16x32_bf16 v[88:91], v[168:171], v[208:211], v[88:91]
	v_mfma_f32_16x16x32_bf16 v[76:79], v[160:163], v[216:219], v[76:79]
	v_mfma_f32_16x16x32_bf16 v[72:75], v[168:171], v[216:219], v[72:75]
	v_mfma_f32_16x16x32_bf16 v[124:127], v[164:167], v[196:199], v[124:127]
	v_mfma_f32_16x16x32_bf16 v[120:123], v[172:175], v[196:199], v[120:123]
	v_mfma_f32_16x16x32_bf16 v[108:111], v[164:167], v[204:207], v[108:111]
	v_mfma_f32_16x16x32_bf16 v[104:107], v[172:175], v[204:207], v[104:107]
	v_mfma_f32_16x16x32_bf16 v[92:95], v[164:167], v[212:215], v[92:95]
	v_mfma_f32_16x16x32_bf16 v[88:91], v[172:175], v[212:215], v[88:91]
	v_mfma_f32_16x16x32_bf16 v[76:79], v[164:167], v[220:223], v[76:79]
	v_mfma_f32_16x16x32_bf16 v[72:75], v[172:175], v[220:223], v[72:75]
	v_mfma_f32_16x16x32_bf16 v[116:119], v[176:179], v[192:195], v[116:119]
	v_mfma_f32_16x16x32_bf16 v[112:115], v[184:187], v[192:195], v[112:115]
	v_mfma_f32_16x16x32_bf16 v[100:103], v[176:179], v[200:203], v[100:103]
	v_mfma_f32_16x16x32_bf16 v[96:99], v[184:187], v[200:203], v[96:99]
	v_mfma_f32_16x16x32_bf16 v[84:87], v[176:179], v[208:211], v[84:87]
	v_mfma_f32_16x16x32_bf16 v[80:83], v[184:187], v[208:211], v[80:83]
	v_mfma_f32_16x16x32_bf16 v[68:71], v[176:179], v[216:219], v[68:71]
	v_mfma_f32_16x16x32_bf16 v[64:67], v[184:187], v[216:219], v[64:67]
	v_mfma_f32_16x16x32_bf16 v[116:119], v[180:183], v[196:199], v[116:119]
	v_mfma_f32_16x16x32_bf16 v[112:115], v[188:191], v[196:199], v[112:115]
	v_mfma_f32_16x16x32_bf16 v[100:103], v[180:183], v[204:207], v[100:103]
	v_mfma_f32_16x16x32_bf16 v[96:99], v[188:191], v[204:207], v[96:99]
	v_mfma_f32_16x16x32_bf16 v[84:87], v[180:183], v[212:215], v[84:87]
	v_mfma_f32_16x16x32_bf16 v[80:83], v[188:191], v[212:215], v[80:83]
	v_mfma_f32_16x16x32_bf16 v[68:71], v[180:183], v[220:223], v[68:71]
	v_mfma_f32_16x16x32_bf16 v[64:67], v[188:191], v[220:223], v[64:67]
	s_barrier
	s_cselect_b32 s71, 0, s72
	s_add_i32 s36, s71, s23
	s_ashr_i32 s37, s36, 31
	s_add_u32 s36, s10, s36
	s_addc_u32 s37, s11, s37
	s_add_i32 s72, s49, s34
	v_lshl_add_u64 v[224:225], s[36:37], 0, v[130:131]
	s_mov_b32 m0, s72
	ds_read_b128 v[192:195], v158 offset:16384
	ds_read_b128 v[196:199], v158 offset:17408
	ds_read_b128 v[200:203], v158 offset:18432
	ds_read_b128 v[204:207], v158 offset:19456
	ds_read_b128 v[208:211], v158 offset:20480
	ds_read_b128 v[212:215], v158 offset:21504
	ds_read_b128 v[216:219], v158 offset:22528
	ds_read_b128 v[220:223], v158 offset:23552
	global_load_lds_dwordx4 v[224:225], off
	s_add_i32 m0, s72, 0x2000
	s_add_i32 s72, s23, 0x40000
	v_lshl_add_u64 v[224:225], s[36:37], 0, v[132:133]
	s_add_i32 s36, s72, s71
	s_ashr_i32 s37, s36, 31
	s_add_u32 s36, s10, s36
	s_addc_u32 s37, s11, s37
	s_add_i32 s73, s58, s34
	global_load_lds_dwordx4 v[224:225], off
	v_lshl_add_u64 v[224:225], s[36:37], 0, v[130:131]
	s_mov_b32 m0, s73
	s_nop 0
	global_load_lds_dwordx4 v[224:225], off
	s_add_i32 m0, s73, 0x2000
	s_add_i32 s73, s71, s22
	v_lshl_add_u64 v[224:225], s[36:37], 0, v[132:133]
	s_add_u32 s36, s28, s73
	s_addc_u32 s37, s29, 0
	global_load_lds_dwordx4 v[224:225], off
	v_lshl_add_u64 v[224:225], s[36:37], 0, v[130:131]
	s_mov_b32 m0, s26
	s_nop 0
	global_load_lds_dwordx4 v[224:225], off
	v_lshl_add_u64 v[224:225], s[36:37], 0, v[132:133]
	s_mov_b32 m0, s27
	s_nop 0
	global_load_lds_dwordx4 v[224:225], off
	s_waitcnt vmcnt(8)
	s_waitcnt lgkmcnt(0)
	s_barrier
	s_waitcnt lgkmcnt(0)
	v_mfma_f32_16x16x32_bf16 v[60:63], v[160:163], v[192:195], v[60:63]
	v_mfma_f32_16x16x32_bf16 v[56:59], v[168:171], v[192:195], v[56:59]
	v_mfma_f32_16x16x32_bf16 v[44:47], v[160:163], v[200:203], v[44:47]
	v_mfma_f32_16x16x32_bf16 v[40:43], v[168:171], v[200:203], v[40:43]
	v_mfma_f32_16x16x32_bf16 v[28:31], v[160:163], v[208:211], v[28:31]
	v_mfma_f32_16x16x32_bf16 v[24:27], v[168:171], v[208:211], v[24:27]
	v_mfma_f32_16x16x32_bf16 v[12:15], v[160:163], v[216:219], v[12:15]
	v_mfma_f32_16x16x32_bf16 v[8:11], v[168:171], v[216:219], v[8:11]
	v_mfma_f32_16x16x32_bf16 v[60:63], v[164:167], v[196:199], v[60:63]
	v_mfma_f32_16x16x32_bf16 v[56:59], v[172:175], v[196:199], v[56:59]
	v_mfma_f32_16x16x32_bf16 v[44:47], v[164:167], v[204:207], v[44:47]
	v_mfma_f32_16x16x32_bf16 v[40:43], v[172:175], v[204:207], v[40:43]
	v_mfma_f32_16x16x32_bf16 v[28:31], v[164:167], v[212:215], v[28:31]
	v_mfma_f32_16x16x32_bf16 v[24:27], v[172:175], v[212:215], v[24:27]
	v_mfma_f32_16x16x32_bf16 v[12:15], v[164:167], v[220:223], v[12:15]
	v_mfma_f32_16x16x32_bf16 v[8:11], v[172:175], v[220:223], v[8:11]
	v_mfma_f32_16x16x32_bf16 v[52:55], v[176:179], v[192:195], v[52:55]
	v_mfma_f32_16x16x32_bf16 v[48:51], v[184:187], v[192:195], v[48:51]
	v_mfma_f32_16x16x32_bf16 v[36:39], v[176:179], v[200:203], v[36:39]
	v_mfma_f32_16x16x32_bf16 v[32:35], v[184:187], v[200:203], v[32:35]
	v_mfma_f32_16x16x32_bf16 v[20:23], v[176:179], v[208:211], v[20:23]
	v_mfma_f32_16x16x32_bf16 v[16:19], v[184:187], v[208:211], v[16:19]
	v_mfma_f32_16x16x32_bf16 v[4:7], v[176:179], v[216:219], v[4:7]
	v_mfma_f32_16x16x32_bf16 v[0:3], v[184:187], v[216:219], v[0:3]
	v_mfma_f32_16x16x32_bf16 v[52:55], v[180:183], v[196:199], v[52:55]
	v_mfma_f32_16x16x32_bf16 v[48:51], v[188:191], v[196:199], v[48:51]
	v_mfma_f32_16x16x32_bf16 v[36:39], v[180:183], v[204:207], v[36:39]
	v_mfma_f32_16x16x32_bf16 v[32:35], v[188:191], v[204:207], v[32:35]
	v_mfma_f32_16x16x32_bf16 v[20:23], v[180:183], v[212:215], v[20:23]
	v_mfma_f32_16x16x32_bf16 v[16:19], v[188:191], v[212:215], v[16:19]
	v_mfma_f32_16x16x32_bf16 v[4:7], v[180:183], v[220:223], v[4:7]
	v_mfma_f32_16x16x32_bf16 v[0:3], v[188:191], v[220:223], v[0:3]
	s_barrier
	s_add_i32 s74, 0, 0x18000
	v_add_u32_e32 v159, s74, v140
	s_add_i32 s75, 0, 0x1c000
	ds_read_b128 v[160:163], v159
	ds_read_b128 v[164:167], v159 offset:1024
	ds_read_b128 v[168:171], v159 offset:2048
	ds_read_b128 v[172:175], v159 offset:3072
	v_add_u32_e32 v159, s75, v140
	ds_read_b128 v[176:179], v159
	ds_read_b128 v[180:183], v159 offset:1024
	ds_read_b128 v[184:187], v159 offset:2048
	ds_read_b128 v[188:191], v159 offset:3072
	s_add_i32 s73, s73, 0x40000
	s_add_u32 s36, s28, s73
	s_addc_u32 s37, s29, 0
	s_mov_b32 m0, s33
	v_lshl_add_u64 v[224:225], s[36:37], 0, v[130:131]
	ds_read_b128 v[192:195], v158 offset:32768
	ds_read_b128 v[196:199], v158 offset:33792
	ds_read_b128 v[200:203], v158 offset:34816
	ds_read_b128 v[204:207], v158 offset:35840
	ds_read_b128 v[208:211], v158 offset:36864
	ds_read_b128 v[212:215], v158 offset:37888
	ds_read_b128 v[216:219], v158 offset:38912
	ds_read_b128 v[220:223], v158 offset:39936
	global_load_lds_dwordx4 v[224:225], off
	v_lshl_add_u64 v[224:225], s[36:37], 0, v[132:133]
	s_mov_b32 m0, s41
	s_nop 0
	global_load_lds_dwordx4 v[224:225], off
	s_waitcnt vmcnt(8)
	s_waitcnt lgkmcnt(0)
	s_barrier
	s_waitcnt lgkmcnt(0)
	v_mfma_f32_16x16x32_bf16 v[124:127], v[160:163], v[192:195], v[124:127]
	v_mfma_f32_16x16x32_bf16 v[120:123], v[168:171], v[192:195], v[120:123]
	v_mfma_f32_16x16x32_bf16 v[108:111], v[160:163], v[200:203], v[108:111]
	v_mfma_f32_16x16x32_bf16 v[104:107], v[168:171], v[200:203], v[104:107]
	v_mfma_f32_16x16x32_bf16 v[92:95], v[160:163], v[208:211], v[92:95]
	v_mfma_f32_16x16x32_bf16 v[88:91], v[168:171], v[208:211], v[88:91]
	v_mfma_f32_16x16x32_bf16 v[76:79], v[160:163], v[216:219], v[76:79]
	v_mfma_f32_16x16x32_bf16 v[72:75], v[168:171], v[216:219], v[72:75]
	v_mfma_f32_16x16x32_bf16 v[124:127], v[164:167], v[196:199], v[124:127]
	v_mfma_f32_16x16x32_bf16 v[120:123], v[172:175], v[196:199], v[120:123]
	v_mfma_f32_16x16x32_bf16 v[108:111], v[164:167], v[204:207], v[108:111]
	v_mfma_f32_16x16x32_bf16 v[104:107], v[172:175], v[204:207], v[104:107]
	v_mfma_f32_16x16x32_bf16 v[92:95], v[164:167], v[212:215], v[92:95]
	v_mfma_f32_16x16x32_bf16 v[88:91], v[172:175], v[212:215], v[88:91]
	v_mfma_f32_16x16x32_bf16 v[76:79], v[164:167], v[220:223], v[76:79]
	v_mfma_f32_16x16x32_bf16 v[72:75], v[172:175], v[220:223], v[72:75]
	v_mfma_f32_16x16x32_bf16 v[116:119], v[176:179], v[192:195], v[116:119]
	v_mfma_f32_16x16x32_bf16 v[112:115], v[184:187], v[192:195], v[112:115]
	v_mfma_f32_16x16x32_bf16 v[100:103], v[176:179], v[200:203], v[100:103]
	v_mfma_f32_16x16x32_bf16 v[96:99], v[184:187], v[200:203], v[96:99]
	v_mfma_f32_16x16x32_bf16 v[84:87], v[176:179], v[208:211], v[84:87]
	v_mfma_f32_16x16x32_bf16 v[80:83], v[184:187], v[208:211], v[80:83]
	v_mfma_f32_16x16x32_bf16 v[68:71], v[176:179], v[216:219], v[68:71]
	v_mfma_f32_16x16x32_bf16 v[64:67], v[184:187], v[216:219], v[64:67]
	v_mfma_f32_16x16x32_bf16 v[116:119], v[180:183], v[196:199], v[116:119]
	v_mfma_f32_16x16x32_bf16 v[112:115], v[188:191], v[196:199], v[112:115]
	v_mfma_f32_16x16x32_bf16 v[100:103], v[180:183], v[204:207], v[100:103]
	v_mfma_f32_16x16x32_bf16 v[96:99], v[188:191], v[204:207], v[96:99]
	v_mfma_f32_16x16x32_bf16 v[84:87], v[180:183], v[212:215], v[84:87]
	v_mfma_f32_16x16x32_bf16 v[80:83], v[188:191], v[212:215], v[80:83]
	v_mfma_f32_16x16x32_bf16 v[68:71], v[180:183], v[220:223], v[68:71]
	v_mfma_f32_16x16x32_bf16 v[64:67], v[188:191], v[220:223], v[64:67]
	s_barrier
; template <class Epi, class Sched, class Hook = NoHook>
; __device__ __forceinline__ void gemm_phase_w(LAS unsigned char* lds, const Sched& S, const Epi& E, int wave_id, const Hook& HK = Hook()) {
;     ...
;         if constexpr (!SEG2) {
;             for (int tt = 0; tt < nt; tt += 2) {
;                 if constexpr (GATHER) { if (tt == nt - 2) {
;                     if (has_next) { gnxt_00 = S.grow_l(nxt, lds, nbuf, R0) + (unsigned)(C0 * 2); gnxt_01 = S.grow_l(nxt, lds, nbuf, R1) + (unsigned)(C1 * 2); gnxt_10 = S.grow_l(nxt, lds, nbuf, 128 + R0) + (unsigned)(C0 * 2); gnxt_11 = S.grow_l(nxt, lds, nbuf, 128 + R1) + (unsigned)(C1 * 2); }
;                     else { gnxt_00 = gcur_00; gnxt_01 = gcur_01; gnxt_10 = gcur_10; gnxt_11 = gcur_11; } } }
;                 PG_TRIP(tt, false, false, false);
;             }
	s_bitset1_b32 s71, 7
	s_add_i32 s23, s71, s23
	s_ashr_i32 s37, s23, 31
	s_add_u32 s36, s10, s23
	s_addc_u32 s37, s11, s37
	s_add_i32 s23, s74, s34
	v_lshl_add_u64 v[224:225], s[36:37], 0, v[130:131]
	s_mov_b32 m0, s23
	ds_read_b128 v[192:195], v158 offset:49152
	ds_read_b128 v[196:199], v158 offset:50176
	ds_read_b128 v[200:203], v158 offset:51200
	ds_read_b128 v[204:207], v158 offset:52224
	ds_read_b128 v[208:211], v158 offset:53248
	ds_read_b128 v[212:215], v158 offset:54272
	ds_read_b128 v[216:219], v158 offset:55296
	ds_read_b128 v[220:223], v158 offset:56320
	global_load_lds_dwordx4 v[224:225], off
	s_add_i32 m0, s23, 0x2000
	s_add_i32 s23, s71, s72
	v_lshl_add_u64 v[224:225], s[36:37], 0, v[132:133]
	s_ashr_i32 s37, s23, 31
	s_add_u32 s36, s10, s23
	s_addc_u32 s37, s11, s37
	s_add_i32 s23, s75, s34
	global_load_lds_dwordx4 v[224:225], off
	v_lshl_add_u64 v[224:225], s[36:37], 0, v[130:131]
	s_mov_b32 m0, s23
	s_add_i32 s71, s71, s22
	global_load_lds_dwordx4 v[224:225], off
	s_add_i32 m0, s23, 0x2000
	s_add_u32 s22, s28, s71
	v_lshl_add_u64 v[224:225], s[36:37], 0, v[132:133]
	s_addc_u32 s23, s29, 0
	global_load_lds_dwordx4 v[224:225], off
	v_lshl_add_u64 v[224:225], s[22:23], 0, v[130:131]
	s_mov_b32 m0, s42
	s_nop 0
	global_load_lds_dwordx4 v[224:225], off
	v_lshl_add_u64 v[224:225], s[22:23], 0, v[132:133]
	s_mov_b32 m0, s43
	s_nop 0
	global_load_lds_dwordx4 v[224:225], off
	s_waitcnt vmcnt(8)
	s_waitcnt lgkmcnt(0)
	s_barrier
	s_waitcnt lgkmcnt(0)
	v_mfma_f32_16x16x32_bf16 v[60:63], v[160:163], v[192:195], v[60:63]
	v_mfma_f32_16x16x32_bf16 v[56:59], v[168:171], v[192:195], v[56:59]
	v_mfma_f32_16x16x32_bf16 v[44:47], v[160:163], v[200:203], v[44:47]
	v_mfma_f32_16x16x32_bf16 v[40:43], v[168:171], v[200:203], v[40:43]
	v_mfma_f32_16x16x32_bf16 v[28:31], v[160:163], v[208:211], v[28:31]
	v_mfma_f32_16x16x32_bf16 v[24:27], v[168:171], v[208:211], v[24:27]
	v_mfma_f32_16x16x32_bf16 v[12:15], v[160:163], v[216:219], v[12:15]
	v_mfma_f32_16x16x32_bf16 v[8:11], v[168:171], v[216:219], v[8:11]
	v_mfma_f32_16x16x32_bf16 v[60:63], v[164:167], v[196:199], v[60:63]
	v_mfma_f32_16x16x32_bf16 v[56:59], v[172:175], v[196:199], v[56:59]
	v_mfma_f32_16x16x32_bf16 v[44:47], v[164:167], v[204:207], v[44:47]
	v_mfma_f32_16x16x32_bf16 v[40:43], v[172:175], v[204:207], v[40:43]
	v_mfma_f32_16x16x32_bf16 v[28:31], v[164:167], v[212:215], v[28:31]
	v_mfma_f32_16x16x32_bf16 v[24:27], v[172:175], v[212:215], v[24:27]
	v_mfma_f32_16x16x32_bf16 v[12:15], v[164:167], v[220:223], v[12:15]
	v_mfma_f32_16x16x32_bf16 v[8:11], v[172:175], v[220:223], v[8:11]
	v_mfma_f32_16x16x32_bf16 v[52:55], v[176:179], v[192:195], v[52:55]
	v_mfma_f32_16x16x32_bf16 v[48:51], v[184:187], v[192:195], v[48:51]
	v_mfma_f32_16x16x32_bf16 v[36:39], v[176:179], v[200:203], v[36:39]
	v_mfma_f32_16x16x32_bf16 v[32:35], v[184:187], v[200:203], v[32:35]
	v_mfma_f32_16x16x32_bf16 v[20:23], v[176:179], v[208:211], v[20:23]
	v_mfma_f32_16x16x32_bf16 v[16:19], v[184:187], v[208:211], v[16:19]
	v_mfma_f32_16x16x32_bf16 v[4:7], v[176:179], v[216:219], v[4:7]
	v_mfma_f32_16x16x32_bf16 v[0:3], v[184:187], v[216:219], v[0:3]
	v_mfma_f32_16x16x32_bf16 v[52:55], v[180:183], v[196:199], v[52:55]
	v_mfma_f32_16x16x32_bf16 v[48:51], v[188:191], v[196:199], v[48:51]
	v_mfma_f32_16x16x32_bf16 v[36:39], v[180:183], v[204:207], v[36:39]
	v_mfma_f32_16x16x32_bf16 v[32:35], v[188:191], v[204:207], v[32:35]
	v_mfma_f32_16x16x32_bf16 v[20:23], v[180:183], v[212:215], v[20:23]
	v_mfma_f32_16x16x32_bf16 v[16:19], v[188:191], v[212:215], v[16:19]
	v_mfma_f32_16x16x32_bf16 v[4:7], v[180:183], v[220:223], v[4:7]
	v_mfma_f32_16x16x32_bf16 v[0:3], v[188:191], v[220:223], v[0:3]
	s_barrier
	s_addk_i32 s12, 0x100
	s_add_i32 s19, s19, 2
	s_cmp_gt_u32 s19, 13
	s_cbranch_scc0 .LBB0_1194
	s_and_b64 vcc, exec, s[0:1]
	s_cbranch_vccz .LBB0_1197
	s_barrier

.LBB0_1442:
	ds_read_b128 v[156:159], v153
	ds_read_b128 v[160:163], v153 offset:1024
	ds_read_b128 v[164:167], v153 offset:2048
	ds_read_b128 v[168:171], v153 offset:3072
	ds_read_b128 v[172:175], v154
	ds_read_b128 v[176:179], v154 offset:1024
	ds_read_b128 v[180:183], v154 offset:2048
	ds_read_b128 v[184:187], v154 offset:3072
	s_add_i32 s22, s61, s12
	s_add_u32 s66, s28, s22
	s_addc_u32 s67, s29, 0
	s_add_i32 m0, s33, 0xc000
	s_add_i32 s68, s33, 0xe000
	s_add_i32 s69, s12, 0xfffc0080
	s_cmp_eq_u32 s19, 12
	s_cselect_b32 s22, s58, s61
	s_cselect_b32 s23, s59, s62
	v_lshl_add_u64 v[220:221], s[66:67], 0, v[130:131]
	ds_read_b128 v[188:191], v155
	ds_read_b128 v[192:195], v155 offset:1024
	ds_read_b128 v[196:199], v155 offset:2048
	ds_read_b128 v[200:203], v155 offset:3072
	ds_read_b128 v[204:207], v155 offset:4096
	ds_read_b128 v[208:211], v155 offset:5120
	ds_read_b128 v[212:215], v155 offset:6144
	ds_read_b128 v[216:219], v155 offset:7168
	global_load_lds_dwordx4 v[220:221], off
	v_lshl_add_u64 v[220:221], s[66:67], 0, v[132:133]
	s_mov_b32 m0, s68
	s_nop 0
	global_load_lds_dwordx4 v[220:221], off
	s_waitcnt vmcnt(8)
	s_waitcnt lgkmcnt(0)
	s_barrier
	s_waitcnt lgkmcnt(0)
	v_mfma_f32_16x16x32_bf16 v[124:127], v[156:159], v[188:191], v[124:127]
	v_mfma_f32_16x16x32_bf16 v[120:123], v[164:167], v[188:191], v[120:123]
	v_mfma_f32_16x16x32_bf16 v[108:111], v[156:159], v[196:199], v[108:111]
	v_mfma_f32_16x16x32_bf16 v[104:107], v[164:167], v[196:199], v[104:107]
	v_mfma_f32_16x16x32_bf16 v[92:95], v[156:159], v[204:207], v[92:95]
	v_mfma_f32_16x16x32_bf16 v[88:91], v[164:167], v[204:207], v[88:91]
	v_mfma_f32_16x16x32_bf16 v[76:79], v[156:159], v[212:215], v[76:79]
	v_mfma_f32_16x16x32_bf16 v[72:75], v[164:167], v[212:215], v[72:75]
	v_mfma_f32_16x16x32_bf16 v[124:127], v[160:163], v[192:195], v[124:127]
	v_mfma_f32_16x16x32_bf16 v[120:123], v[168:171], v[192:195], v[120:123]
	v_mfma_f32_16x16x32_bf16 v[108:111], v[160:163], v[200:203], v[108:111]
	v_mfma_f32_16x16x32_bf16 v[104:107], v[168:171], v[200:203], v[104:107]
	v_mfma_f32_16x16x32_bf16 v[92:95], v[160:163], v[208:211], v[92:95]
	v_mfma_f32_16x16x32_bf16 v[88:91], v[168:171], v[208:211], v[88:91]
	v_mfma_f32_16x16x32_bf16 v[76:79], v[160:163], v[216:219], v[76:79]
	v_mfma_f32_16x16x32_bf16 v[72:75], v[168:171], v[216:219], v[72:75]
	v_mfma_f32_16x16x32_bf16 v[116:119], v[172:175], v[188:191], v[116:119]
	v_mfma_f32_16x16x32_bf16 v[112:115], v[180:183], v[188:191], v[112:115]
	v_mfma_f32_16x16x32_bf16 v[100:103], v[172:175], v[196:199], v[100:103]
	v_mfma_f32_16x16x32_bf16 v[96:99], v[180:183], v[196:199], v[96:99]
	v_mfma_f32_16x16x32_bf16 v[84:87], v[172:175], v[204:207], v[84:87]
	v_mfma_f32_16x16x32_bf16 v[80:83], v[180:183], v[204:207], v[80:83]
	v_mfma_f32_16x16x32_bf16 v[68:71], v[172:175], v[212:215], v[68:71]
	v_mfma_f32_16x16x32_bf16 v[64:67], v[180:183], v[212:215], v[64:67]
	v_mfma_f32_16x16x32_bf16 v[116:119], v[176:179], v[192:195], v[116:119]
	v_mfma_f32_16x16x32_bf16 v[112:115], v[184:187], v[192:195], v[112:115]
	v_mfma_f32_16x16x32_bf16 v[100:103], v[176:179], v[200:203], v[100:103]
	v_mfma_f32_16x16x32_bf16 v[96:99], v[184:187], v[200:203], v[96:99]
	v_mfma_f32_16x16x32_bf16 v[84:87], v[176:179], v[208:211], v[84:87]
	v_mfma_f32_16x16x32_bf16 v[80:83], v[184:187], v[208:211], v[80:83]
	v_mfma_f32_16x16x32_bf16 v[68:71], v[176:179], v[216:219], v[68:71]
	v_mfma_f32_16x16x32_bf16 v[64:67], v[184:187], v[216:219], v[64:67]
	s_barrier
	s_cselect_b32 s68, 0, s69
	s_add_i32 s66, s68, s23
	s_ashr_i32 s67, s66, 31
	s_add_u32 s66, s10, s66
	s_addc_u32 s67, s11, s67
	s_add_i32 s69, s37, s34
	v_lshl_add_u64 v[220:221], s[66:67], 0, v[130:131]
	s_mov_b32 m0, s69
	ds_read_b128 v[188:191], v155 offset:16384
	ds_read_b128 v[192:195], v155 offset:17408
	ds_read_b128 v[196:199], v155 offset:18432
	ds_read_b128 v[200:203], v155 offset:19456
	ds_read_b128 v[204:207], v155 offset:20480
	ds_read_b128 v[208:211], v155 offset:21504
	ds_read_b128 v[212:215], v155 offset:22528
	ds_read_b128 v[216:219], v155 offset:23552
	global_load_lds_dwordx4 v[220:221], off
	s_add_i32 m0, s69, 0x2000
	s_add_i32 s69, s23, 0x40000
	v_lshl_add_u64 v[220:221], s[66:67], 0, v[132:133]
	s_add_i32 s66, s69, s68
	s_ashr_i32 s67, s66, 31
	s_add_u32 s66, s10, s66
	s_addc_u32 s67, s11, s67
	s_add_i32 s70, s38, s34
	global_load_lds_dwordx4 v[220:221], off
	v_lshl_add_u64 v[220:221], s[66:67], 0, v[130:131]
	s_mov_b32 m0, s70
	s_nop 0
	global_load_lds_dwordx4 v[220:221], off
	s_add_i32 m0, s70, 0x2000
	s_add_i32 s70, s68, s22
	v_lshl_add_u64 v[220:221], s[66:67], 0, v[132:133]
	s_add_u32 s66, s28, s70
	s_addc_u32 s67, s29, 0
	global_load_lds_dwordx4 v[220:221], off
	v_lshl_add_u64 v[220:221], s[66:67], 0, v[130:131]
	s_mov_b32 m0, s33
	s_nop 0
	global_load_lds_dwordx4 v[220:221], off
	v_lshl_add_u64 v[220:221], s[66:67], 0, v[132:133]
	s_mov_b32 m0, s40
	s_nop 0
	global_load_lds_dwordx4 v[220:221], off
	s_waitcnt vmcnt(8)
	s_waitcnt lgkmcnt(0)
	s_barrier
	s_waitcnt lgkmcnt(0)
	v_mfma_f32_16x16x32_bf16 v[60:63], v[156:159], v[188:191], v[60:63]
	v_mfma_f32_16x16x32_bf16 v[56:59], v[164:167], v[188:191], v[56:59]
	v_mfma_f32_16x16x32_bf16 v[44:47], v[156:159], v[196:199], v[44:47]
	v_mfma_f32_16x16x32_bf16 v[40:43], v[164:167], v[196:199], v[40:43]
	v_mfma_f32_16x16x32_bf16 v[28:31], v[156:159], v[204:207], v[28:31]
	v_mfma_f32_16x16x32_bf16 v[24:27], v[164:167], v[204:207], v[24:27]
	v_mfma_f32_16x16x32_bf16 v[12:15], v[156:159], v[212:215], v[12:15]
	v_mfma_f32_16x16x32_bf16 v[8:11], v[164:167], v[212:215], v[8:11]
	v_mfma_f32_16x16x32_bf16 v[60:63], v[160:163], v[192:195], v[60:63]
	v_mfma_f32_16x16x32_bf16 v[56:59], v[168:171], v[192:195], v[56:59]
	v_mfma_f32_16x16x32_bf16 v[44:47], v[160:163], v[200:203], v[44:47]
	v_mfma_f32_16x16x32_bf16 v[40:43], v[168:171], v[200:203], v[40:43]
	v_mfma_f32_16x16x32_bf16 v[28:31], v[160:163], v[208:211], v[28:31]
	v_mfma_f32_16x16x32_bf16 v[24:27], v[168:171], v[208:211], v[24:27]
	v_mfma_f32_16x16x32_bf16 v[12:15], v[160:163], v[216:219], v[12:15]
	v_mfma_f32_16x16x32_bf16 v[8:11], v[168:171], v[216:219], v[8:11]
	v_mfma_f32_16x16x32_bf16 v[52:55], v[172:175], v[188:191], v[52:55]
	v_mfma_f32_16x16x32_bf16 v[48:51], v[180:183], v[188:191], v[48:51]
	v_mfma_f32_16x16x32_bf16 v[36:39], v[172:175], v[196:199], v[36:39]
	v_mfma_f32_16x16x32_bf16 v[32:35], v[180:183], v[196:199], v[32:35]
	v_mfma_f32_16x16x32_bf16 v[20:23], v[172:175], v[204:207], v[20:23]
	v_mfma_f32_16x16x32_bf16 v[16:19], v[180:183], v[204:207], v[16:19]
	v_mfma_f32_16x16x32_bf16 v[4:7], v[172:175], v[212:215], v[4:7]
	v_mfma_f32_16x16x32_bf16 v[0:3], v[180:183], v[212:215], v[0:3]
	v_mfma_f32_16x16x32_bf16 v[52:55], v[176:179], v[192:195], v[52:55]
	v_mfma_f32_16x16x32_bf16 v[48:51], v[184:187], v[192:195], v[48:51]
	v_mfma_f32_16x16x32_bf16 v[36:39], v[176:179], v[200:203], v[36:39]
	v_mfma_f32_16x16x32_bf16 v[32:35], v[184:187], v[200:203], v[32:35]
	v_mfma_f32_16x16x32_bf16 v[20:23], v[176:179], v[208:211], v[20:23]
	v_mfma_f32_16x16x32_bf16 v[16:19], v[184:187], v[208:211], v[16:19]
	v_mfma_f32_16x16x32_bf16 v[4:7], v[176:179], v[216:219], v[4:7]
	v_mfma_f32_16x16x32_bf16 v[0:3], v[184:187], v[216:219], v[0:3]
	s_barrier
	s_add_i32 s71, 0, 0x18000
	s_add_i32 s72, 0, 0x1c000
	v_add_u32_e32 v168, s71, v137
	v_add_u32_e32 v184, s72, v137
	ds_read_b128 v[156:159], v168
	ds_read_b128 v[160:163], v168 offset:1024
	ds_read_b128 v[164:167], v168 offset:2048
	ds_read_b128 v[168:171], v168 offset:3072
	ds_read_b128 v[172:175], v184
	ds_read_b128 v[176:179], v184 offset:1024
	ds_read_b128 v[180:183], v184 offset:2048
	ds_read_b128 v[184:187], v184 offset:3072
	s_add_i32 s70, s70, 0x40000
	s_add_u32 s66, s28, s70
	s_addc_u32 s67, s29, 0
	s_mov_b32 m0, s41
	v_lshl_add_u64 v[220:221], s[66:67], 0, v[130:131]
	ds_read_b128 v[188:191], v155 offset:32768
	ds_read_b128 v[192:195], v155 offset:33792
	ds_read_b128 v[196:199], v155 offset:34816
	ds_read_b128 v[200:203], v155 offset:35840
	ds_read_b128 v[204:207], v155 offset:36864
	ds_read_b128 v[208:211], v155 offset:37888
	ds_read_b128 v[212:215], v155 offset:38912
	ds_read_b128 v[216:219], v155 offset:39936
	global_load_lds_dwordx4 v[220:221], off
	v_lshl_add_u64 v[220:221], s[66:67], 0, v[132:133]
	s_mov_b32 m0, s42
	s_nop 0
	global_load_lds_dwordx4 v[220:221], off
	s_waitcnt vmcnt(8)
	s_waitcnt lgkmcnt(0)
	s_barrier
	s_waitcnt lgkmcnt(0)
	v_mfma_f32_16x16x32_bf16 v[124:127], v[156:159], v[188:191], v[124:127]
	v_mfma_f32_16x16x32_bf16 v[120:123], v[164:167], v[188:191], v[120:123]
	v_mfma_f32_16x16x32_bf16 v[108:111], v[156:159], v[196:199], v[108:111]
	v_mfma_f32_16x16x32_bf16 v[104:107], v[164:167], v[196:199], v[104:107]
	v_mfma_f32_16x16x32_bf16 v[92:95], v[156:159], v[204:207], v[92:95]
	v_mfma_f32_16x16x32_bf16 v[88:91], v[164:167], v[204:207], v[88:91]
	v_mfma_f32_16x16x32_bf16 v[76:79], v[156:159], v[212:215], v[76:79]
	v_mfma_f32_16x16x32_bf16 v[72:75], v[164:167], v[212:215], v[72:75]
	v_mfma_f32_16x16x32_bf16 v[124:127], v[160:163], v[192:195], v[124:127]
	v_mfma_f32_16x16x32_bf16 v[120:123], v[168:171], v[192:195], v[120:123]
	v_mfma_f32_16x16x32_bf16 v[108:111], v[160:163], v[200:203], v[108:111]
	v_mfma_f32_16x16x32_bf16 v[104:107], v[168:171], v[200:203], v[104:107]
	v_mfma_f32_16x16x32_bf16 v[92:95], v[160:163], v[208:211], v[92:95]
	v_mfma_f32_16x16x32_bf16 v[88:91], v[168:171], v[208:211], v[88:91]
	v_mfma_f32_16x16x32_bf16 v[76:79], v[160:163], v[216:219], v[76:79]
	v_mfma_f32_16x16x32_bf16 v[72:75], v[168:171], v[216:219], v[72:75]
	v_mfma_f32_16x16x32_bf16 v[116:119], v[172:175], v[188:191], v[116:119]
	v_mfma_f32_16x16x32_bf16 v[112:115], v[180:183], v[188:191], v[112:115]
	v_mfma_f32_16x16x32_bf16 v[100:103], v[172:175], v[196:199], v[100:103]
	v_mfma_f32_16x16x32_bf16 v[96:99], v[180:183], v[196:199], v[96:99]
	v_mfma_f32_16x16x32_bf16 v[84:87], v[172:175], v[204:207], v[84:87]
	v_mfma_f32_16x16x32_bf16 v[80:83], v[180:183], v[204:207], v[80:83]
	v_mfma_f32_16x16x32_bf16 v[68:71], v[172:175], v[212:215], v[68:71]
	v_mfma_f32_16x16x32_bf16 v[64:67], v[180:183], v[212:215], v[64:67]
	v_mfma_f32_16x16x32_bf16 v[116:119], v[176:179], v[192:195], v[116:119]
	v_mfma_f32_16x16x32_bf16 v[112:115], v[184:187], v[192:195], v[112:115]
	v_mfma_f32_16x16x32_bf16 v[100:103], v[176:179], v[200:203], v[100:103]
	v_mfma_f32_16x16x32_bf16 v[96:99], v[184:187], v[200:203], v[96:99]
	v_mfma_f32_16x16x32_bf16 v[84:87], v[176:179], v[208:211], v[84:87]
	v_mfma_f32_16x16x32_bf16 v[80:83], v[184:187], v[208:211], v[80:83]
	v_mfma_f32_16x16x32_bf16 v[68:71], v[176:179], v[216:219], v[68:71]
	v_mfma_f32_16x16x32_bf16 v[64:67], v[184:187], v[216:219], v[64:67]
	s_barrier
; template <class Epi, class Sched, class Hook = NoHook>
; __device__ __forceinline__ void gemm_phase_w(LAS unsigned char* lds, const Sched& S, const Epi& E, int wave_id, const Hook& HK = Hook()) {
;     ...
;         if constexpr (!SEG2) {
;             for (int tt = 0; tt < nt; tt += 2) {
;                 if constexpr (GATHER) { if (tt == nt - 2) {
;                     if (has_next) { gnxt_00 = S.grow_l(nxt, lds, nbuf, R0) + (unsigned)(C0 * 2); gnxt_01 = S.grow_l(nxt, lds, nbuf, R1) + (unsigned)(C1 * 2); gnxt_10 = S.grow_l(nxt, lds, nbuf, 128 + R0) + (unsigned)(C0 * 2); gnxt_11 = S.grow_l(nxt, lds, nbuf, 128 + R1) + (unsigned)(C1 * 2); }
;                     else { gnxt_00 = gcur_00; gnxt_01 = gcur_01; gnxt_10 = gcur_10; gnxt_11 = gcur_11; } } }
;                 PG_TRIP(tt, false, false, false);
;             }
	s_bitset1_b32 s68, 7
	s_add_i32 s23, s68, s23
	s_ashr_i32 s67, s23, 31
	s_add_u32 s66, s10, s23
	s_addc_u32 s67, s11, s67
	s_add_i32 s23, s71, s34
	v_lshl_add_u64 v[220:221], s[66:67], 0, v[130:131]
	s_mov_b32 m0, s23
	ds_read_b128 v[188:191], v155 offset:49152
	ds_read_b128 v[192:195], v155 offset:50176
	ds_read_b128 v[196:199], v155 offset:51200
	ds_read_b128 v[200:203], v155 offset:52224
	ds_read_b128 v[204:207], v155 offset:53248
	ds_read_b128 v[208:211], v155 offset:54272
	ds_read_b128 v[212:215], v155 offset:55296
	ds_read_b128 v[216:219], v155 offset:56320
	global_load_lds_dwordx4 v[220:221], off
	s_add_i32 m0, s23, 0x2000
	s_add_i32 s23, s68, s69
	v_lshl_add_u64 v[220:221], s[66:67], 0, v[132:133]
	s_ashr_i32 s67, s23, 31
	s_add_u32 s66, s10, s23
	s_addc_u32 s67, s11, s67
	s_add_i32 s23, s72, s34
	global_load_lds_dwordx4 v[220:221], off
	v_lshl_add_u64 v[220:221], s[66:67], 0, v[130:131]
	s_mov_b32 m0, s23
	s_add_i32 s68, s68, s22
	global_load_lds_dwordx4 v[220:221], off
	s_add_i32 m0, s23, 0x2000
	s_add_u32 s22, s28, s68
	v_lshl_add_u64 v[220:221], s[66:67], 0, v[132:133]
	s_addc_u32 s23, s29, 0
	global_load_lds_dwordx4 v[220:221], off
	v_lshl_add_u64 v[220:221], s[22:23], 0, v[130:131]
	s_mov_b32 m0, s39
	s_nop 0
	global_load_lds_dwordx4 v[220:221], off
	v_lshl_add_u64 v[220:221], s[22:23], 0, v[132:133]
	s_mov_b32 m0, s43
	s_nop 0
	global_load_lds_dwordx4 v[220:221], off
	s_waitcnt vmcnt(8)
	s_waitcnt lgkmcnt(0)
	s_barrier
	s_waitcnt lgkmcnt(0)
	v_mfma_f32_16x16x32_bf16 v[60:63], v[156:159], v[188:191], v[60:63]
	v_mfma_f32_16x16x32_bf16 v[56:59], v[164:167], v[188:191], v[56:59]
	v_mfma_f32_16x16x32_bf16 v[44:47], v[156:159], v[196:199], v[44:47]
	v_mfma_f32_16x16x32_bf16 v[40:43], v[164:167], v[196:199], v[40:43]
	v_mfma_f32_16x16x32_bf16 v[28:31], v[156:159], v[204:207], v[28:31]
	v_mfma_f32_16x16x32_bf16 v[24:27], v[164:167], v[204:207], v[24:27]
	v_mfma_f32_16x16x32_bf16 v[12:15], v[156:159], v[212:215], v[12:15]
	v_mfma_f32_16x16x32_bf16 v[8:11], v[164:167], v[212:215], v[8:11]
	v_mfma_f32_16x16x32_bf16 v[60:63], v[160:163], v[192:195], v[60:63]
	v_mfma_f32_16x16x32_bf16 v[56:59], v[168:171], v[192:195], v[56:59]
	v_mfma_f32_16x16x32_bf16 v[44:47], v[160:163], v[200:203], v[44:47]
	v_mfma_f32_16x16x32_bf16 v[40:43], v[168:171], v[200:203], v[40:43]
	v_mfma_f32_16x16x32_bf16 v[28:31], v[160:163], v[208:211], v[28:31]
	v_mfma_f32_16x16x32_bf16 v[24:27], v[168:171], v[208:211], v[24:27]
	v_mfma_f32_16x16x32_bf16 v[12:15], v[160:163], v[216:219], v[12:15]
	v_mfma_f32_16x16x32_bf16 v[8:11], v[168:171], v[216:219], v[8:11]
	v_mfma_f32_16x16x32_bf16 v[52:55], v[172:175], v[188:191], v[52:55]
	v_mfma_f32_16x16x32_bf16 v[48:51], v[180:183], v[188:191], v[48:51]
	v_mfma_f32_16x16x32_bf16 v[36:39], v[172:175], v[196:199], v[36:39]
	v_mfma_f32_16x16x32_bf16 v[32:35], v[180:183], v[196:199], v[32:35]
	v_mfma_f32_16x16x32_bf16 v[20:23], v[172:175], v[204:207], v[20:23]
	v_mfma_f32_16x16x32_bf16 v[16:19], v[180:183], v[204:207], v[16:19]
	v_mfma_f32_16x16x32_bf16 v[4:7], v[172:175], v[212:215], v[4:7]
	v_mfma_f32_16x16x32_bf16 v[0:3], v[180:183], v[212:215], v[0:3]
	v_mfma_f32_16x16x32_bf16 v[52:55], v[176:179], v[192:195], v[52:55]
	v_mfma_f32_16x16x32_bf16 v[48:51], v[184:187], v[192:195], v[48:51]
	v_mfma_f32_16x16x32_bf16 v[36:39], v[176:179], v[200:203], v[36:39]
	v_mfma_f32_16x16x32_bf16 v[32:35], v[184:187], v[200:203], v[32:35]
	v_mfma_f32_16x16x32_bf16 v[20:23], v[176:179], v[208:211], v[20:23]
	v_mfma_f32_16x16x32_bf16 v[16:19], v[184:187], v[208:211], v[16:19]
	v_mfma_f32_16x16x32_bf16 v[4:7], v[176:179], v[216:219], v[4:7]
	v_mfma_f32_16x16x32_bf16 v[0:3], v[184:187], v[216:219], v[0:3]
	s_barrier
	s_addk_i32 s12, 0x100
	s_add_i32 s19, s19, 2
	s_cmp_gt_u32 s19, 13
	s_cbranch_scc0 .LBB0_1442
	s_and_b64 vcc, exec, s[0:1]
	s_cbranch_vccz .LBB0_1445
	s_barrier

.LBB0_1585:
	ds_read_b128 v[82:85], v75
	ds_read_b128 v[86:89], v75 offset:1024
	ds_read_b128 v[90:93], v75 offset:2048
	ds_read_b128 v[94:97], v75 offset:3072
	s_add_i32 s61, s39, s20
	s_add_u32 s62, s8, s61
	s_addc_u32 s63, s9, 0
	s_add_i32 s61, s20, 0xfffe0080
	s_cmp_eq_u32 s21, 4
	s_cselect_b32 s66, s59, s39
	s_cselect_b32 s67, s51, s60
	s_cselect_b32 s68, s58, s38
	s_mov_b32 m0, s40
	v_lshl_add_u64 v[130:131], s[62:63], 0, v[64:65]
	ds_read_b128 v[98:101], v76
	ds_read_b128 v[102:105], v76 offset:1024
	ds_read_b128 v[106:109], v76 offset:2048
	ds_read_b128 v[110:113], v76 offset:3072
	ds_read_b128 v[114:117], v76 offset:4096
	ds_read_b128 v[118:121], v76 offset:5120
	ds_read_b128 v[122:125], v76 offset:6144
	ds_read_b128 v[126:129], v76 offset:7168
	global_load_lds_dwordx4 v[130:131], off
	v_lshl_add_u64 v[130:131], s[62:63], 0, v[66:67]
	s_mov_b32 m0, s41
	s_nop 0
	global_load_lds_dwordx4 v[130:131], off
	s_waitcnt vmcnt(8)
	s_waitcnt lgkmcnt(0)
	s_barrier
	s_waitcnt lgkmcnt(0)
	v_mfma_f32_16x16x32_bf16 v[60:63], v[82:85], v[98:101], v[60:63]
	v_mfma_f32_16x16x32_bf16 v[56:59], v[90:93], v[98:101], v[56:59]
	v_mfma_f32_16x16x32_bf16 v[52:55], v[82:85], v[106:109], v[52:55]
	v_mfma_f32_16x16x32_bf16 v[48:51], v[90:93], v[106:109], v[48:51]
	v_mfma_f32_16x16x32_bf16 v[44:47], v[82:85], v[114:117], v[44:47]
	v_mfma_f32_16x16x32_bf16 v[40:43], v[90:93], v[114:117], v[40:43]
	v_mfma_f32_16x16x32_bf16 v[36:39], v[82:85], v[122:125], v[36:39]
	v_mfma_f32_16x16x32_bf16 v[32:35], v[90:93], v[122:125], v[32:35]
	v_mfma_f32_16x16x32_bf16 v[60:63], v[86:89], v[102:105], v[60:63]
	v_mfma_f32_16x16x32_bf16 v[56:59], v[94:97], v[102:105], v[56:59]
	v_mfma_f32_16x16x32_bf16 v[52:55], v[86:89], v[110:113], v[52:55]
	v_mfma_f32_16x16x32_bf16 v[48:51], v[94:97], v[110:113], v[48:51]
	v_mfma_f32_16x16x32_bf16 v[44:47], v[86:89], v[118:121], v[44:47]
	v_mfma_f32_16x16x32_bf16 v[40:43], v[94:97], v[118:121], v[40:43]
	v_mfma_f32_16x16x32_bf16 v[36:39], v[86:89], v[126:129], v[36:39]
	v_mfma_f32_16x16x32_bf16 v[32:35], v[94:97], v[126:129], v[32:35]
	s_barrier
	s_cselect_b32 s61, 0, s61
	s_add_i32 s62, s61, s68
	s_ashr_i32 s63, s62, 31
	s_add_u32 s62, s3, s62
	s_addc_u32 s63, s22, s63
	s_mov_b32 m0, s42
	v_lshl_add_u64 v[130:131], s[62:63], 0, v[64:65]
	s_add_i32 s67, s68, s67
	ds_read_b128 v[98:101], v76 offset:16384
	ds_read_b128 v[102:105], v76 offset:17408
	ds_read_b128 v[106:109], v76 offset:18432
	ds_read_b128 v[110:113], v76 offset:19456
	ds_read_b128 v[114:117], v76 offset:20480
	ds_read_b128 v[118:121], v76 offset:21504
	ds_read_b128 v[122:125], v76 offset:22528
	ds_read_b128 v[126:129], v76 offset:23552
	global_load_lds_dwordx4 v[130:131], off
	v_lshl_add_u64 v[130:131], s[62:63], 0, v[66:67]
	s_add_i32 s62, s67, s61
	s_ashr_i32 s63, s62, 31
	s_add_u32 s62, s3, s62
	s_mov_b32 m0, s43
	s_addc_u32 s63, s22, s63
	global_load_lds_dwordx4 v[130:131], off
	v_lshl_add_u64 v[130:131], s[62:63], 0, v[64:65]
	s_mov_b32 m0, s24
	s_add_i32 s69, s61, s66
	global_load_lds_dwordx4 v[130:131], off
	v_lshl_add_u64 v[130:131], s[62:63], 0, v[66:67]
	s_add_u32 s62, s8, s69
	s_mov_b32 m0, s25
	s_addc_u32 s63, s9, 0
	global_load_lds_dwordx4 v[130:131], off
	v_lshl_add_u64 v[130:131], s[62:63], 0, v[64:65]
	s_mov_b32 m0, s23
	s_nop 0
	global_load_lds_dwordx4 v[130:131], off
	v_lshl_add_u64 v[130:131], s[62:63], 0, v[66:67]
	s_mov_b32 m0, s28
	s_nop 0
	global_load_lds_dwordx4 v[130:131], off
	s_waitcnt vmcnt(8)
	s_waitcnt lgkmcnt(0)
	s_barrier
	s_waitcnt lgkmcnt(0)
	v_mfma_f32_16x16x32_bf16 v[28:31], v[82:85], v[98:101], v[28:31]
	v_mfma_f32_16x16x32_bf16 v[24:27], v[90:93], v[98:101], v[24:27]
	v_mfma_f32_16x16x32_bf16 v[20:23], v[82:85], v[106:109], v[20:23]
	v_mfma_f32_16x16x32_bf16 v[16:19], v[90:93], v[106:109], v[16:19]
	v_mfma_f32_16x16x32_bf16 v[12:15], v[82:85], v[114:117], v[12:15]
	v_mfma_f32_16x16x32_bf16 v[8:11], v[90:93], v[114:117], v[8:11]
	v_mfma_f32_16x16x32_bf16 v[4:7], v[82:85], v[122:125], v[4:7]
	v_mfma_f32_16x16x32_bf16 v[0:3], v[90:93], v[122:125], v[0:3]
	v_mfma_f32_16x16x32_bf16 v[28:31], v[86:89], v[102:105], v[28:31]
	v_mfma_f32_16x16x32_bf16 v[24:27], v[94:97], v[102:105], v[24:27]
	v_mfma_f32_16x16x32_bf16 v[20:23], v[86:89], v[110:113], v[20:23]
	v_mfma_f32_16x16x32_bf16 v[16:19], v[94:97], v[110:113], v[16:19]
	v_mfma_f32_16x16x32_bf16 v[12:15], v[86:89], v[118:121], v[12:15]
	v_mfma_f32_16x16x32_bf16 v[8:11], v[94:97], v[118:121], v[8:11]
	v_mfma_f32_16x16x32_bf16 v[4:7], v[86:89], v[126:129], v[4:7]
	v_mfma_f32_16x16x32_bf16 v[0:3], v[94:97], v[126:129], v[0:3]
	s_barrier
; template <class Epi, class Sched, class Hook = NoHook>
; __device__ __forceinline__ void gemm_phase_w(LAS unsigned char* lds, const Sched& S, const Epi& E, int wave_id, const Hook& HK = Hook()) {
;     ...
;         if constexpr (!SEG2) {
;             for (int tt = 0; tt < nt; tt += 2) {
;                 if constexpr (GATHER) { if (tt == nt - 2) {
;                     if (has_next) { gnxt_00 = S.grow_l(nxt, lds, nbuf, R0) + (unsigned)(C0 * 2); gnxt_01 = S.grow_l(nxt, lds, nbuf, R1) + (unsigned)(C1 * 2); gnxt_10 = S.grow_l(nxt, lds, nbuf, 128 + R0) + (unsigned)(C0 * 2); gnxt_11 = S.grow_l(nxt, lds, nbuf, 128 + R1) + (unsigned)(C1 * 2); }
;                     else { gnxt_00 = gcur_00; gnxt_01 = gcur_01; gnxt_10 = gcur_10; gnxt_11 = gcur_11; } } }
;                 PG_TRIP(tt, false, false, false);
;             }
	ds_read_b128 v[82:85], v81
	ds_read_b128 v[86:89], v81 offset:1024
	ds_read_b128 v[90:93], v81 offset:2048
	ds_read_b128 v[94:97], v81 offset:3072
	s_add_i32 s69, s69, 0x20000
	s_add_u32 s62, s8, s69
	s_addc_u32 s63, s9, 0
	s_mov_b32 m0, s29
	v_lshl_add_u64 v[130:131], s[62:63], 0, v[64:65]
	ds_read_b128 v[98:101], v76 offset:32768
	ds_read_b128 v[102:105], v76 offset:33792
	ds_read_b128 v[106:109], v76 offset:34816
	ds_read_b128 v[110:113], v76 offset:35840
	ds_read_b128 v[114:117], v76 offset:36864
	ds_read_b128 v[118:121], v76 offset:37888
	ds_read_b128 v[122:125], v76 offset:38912
	ds_read_b128 v[126:129], v76 offset:39936
	global_load_lds_dwordx4 v[130:131], off
	v_lshl_add_u64 v[130:131], s[62:63], 0, v[66:67]
	s_mov_b32 m0, s30
	s_nop 0
	global_load_lds_dwordx4 v[130:131], off
	s_waitcnt vmcnt(8)
	s_waitcnt lgkmcnt(0)
	s_barrier
	s_waitcnt lgkmcnt(0)
	v_mfma_f32_16x16x32_bf16 v[60:63], v[82:85], v[98:101], v[60:63]
	v_mfma_f32_16x16x32_bf16 v[56:59], v[90:93], v[98:101], v[56:59]
	v_mfma_f32_16x16x32_bf16 v[52:55], v[82:85], v[106:109], v[52:55]
	v_mfma_f32_16x16x32_bf16 v[48:51], v[90:93], v[106:109], v[48:51]
	v_mfma_f32_16x16x32_bf16 v[44:47], v[82:85], v[114:117], v[44:47]
	v_mfma_f32_16x16x32_bf16 v[40:43], v[90:93], v[114:117], v[40:43]
	v_mfma_f32_16x16x32_bf16 v[36:39], v[82:85], v[122:125], v[36:39]
	v_mfma_f32_16x16x32_bf16 v[32:35], v[90:93], v[122:125], v[32:35]
	v_mfma_f32_16x16x32_bf16 v[60:63], v[86:89], v[102:105], v[60:63]
	v_mfma_f32_16x16x32_bf16 v[56:59], v[94:97], v[102:105], v[56:59]
	v_mfma_f32_16x16x32_bf16 v[52:55], v[86:89], v[110:113], v[52:55]
	v_mfma_f32_16x16x32_bf16 v[48:51], v[94:97], v[110:113], v[48:51]
	v_mfma_f32_16x16x32_bf16 v[44:47], v[86:89], v[118:121], v[44:47]
	v_mfma_f32_16x16x32_bf16 v[40:43], v[94:97], v[118:121], v[40:43]
	v_mfma_f32_16x16x32_bf16 v[36:39], v[86:89], v[126:129], v[36:39]
	v_mfma_f32_16x16x32_bf16 v[32:35], v[94:97], v[126:129], v[32:35]
	s_barrier
	s_bitset1_b32 s61, 7
	s_add_i32 s62, s61, s68
	s_ashr_i32 s63, s62, 31
	s_add_u32 s62, s3, s62
	s_addc_u32 s63, s22, s63
	s_mov_b32 m0, s44
	v_lshl_add_u64 v[130:131], s[62:63], 0, v[64:65]
	ds_read_b128 v[98:101], v76 offset:49152
	ds_read_b128 v[102:105], v76 offset:50176
	ds_read_b128 v[106:109], v76 offset:51200
	ds_read_b128 v[110:113], v76 offset:52224
	ds_read_b128 v[114:117], v76 offset:53248
	ds_read_b128 v[118:121], v76 offset:54272
	ds_read_b128 v[122:125], v76 offset:55296
	ds_read_b128 v[126:129], v76 offset:56320
	global_load_lds_dwordx4 v[130:131], off
	v_lshl_add_u64 v[130:131], s[62:63], 0, v[66:67]
	s_add_i32 s62, s61, s67
	s_ashr_i32 s63, s62, 31
	s_add_u32 s62, s3, s62
	s_mov_b32 m0, s45
	s_addc_u32 s63, s22, s63
	global_load_lds_dwordx4 v[130:131], off
	v_lshl_add_u64 v[130:131], s[62:63], 0, v[64:65]
	s_mov_b32 m0, s36
	s_add_i32 s61, s61, s66
	global_load_lds_dwordx4 v[130:131], off
	v_lshl_add_u64 v[130:131], s[62:63], 0, v[66:67]
	s_add_u32 s62, s8, s61
	s_mov_b32 m0, s37
	s_addc_u32 s63, s9, 0
	global_load_lds_dwordx4 v[130:131], off
	v_lshl_add_u64 v[130:131], s[62:63], 0, v[64:65]
	s_mov_b32 m0, s34
	s_nop 0
	global_load_lds_dwordx4 v[130:131], off
	v_lshl_add_u64 v[130:131], s[62:63], 0, v[66:67]
	s_mov_b32 m0, s35
	s_nop 0
	global_load_lds_dwordx4 v[130:131], off
	s_waitcnt vmcnt(8)
	s_waitcnt lgkmcnt(0)
	s_barrier
	s_waitcnt lgkmcnt(0)
	v_mfma_f32_16x16x32_bf16 v[28:31], v[82:85], v[98:101], v[28:31]
	v_mfma_f32_16x16x32_bf16 v[24:27], v[90:93], v[98:101], v[24:27]
	v_mfma_f32_16x16x32_bf16 v[20:23], v[82:85], v[106:109], v[20:23]
	v_mfma_f32_16x16x32_bf16 v[16:19], v[90:93], v[106:109], v[16:19]
	v_mfma_f32_16x16x32_bf16 v[12:15], v[82:85], v[114:117], v[12:15]
	v_mfma_f32_16x16x32_bf16 v[8:11], v[90:93], v[114:117], v[8:11]
	v_mfma_f32_16x16x32_bf16 v[4:7], v[82:85], v[122:125], v[4:7]
	v_mfma_f32_16x16x32_bf16 v[0:3], v[90:93], v[122:125], v[0:3]
	v_mfma_f32_16x16x32_bf16 v[28:31], v[86:89], v[102:105], v[28:31]
	v_mfma_f32_16x16x32_bf16 v[24:27], v[94:97], v[102:105], v[24:27]
	v_mfma_f32_16x16x32_bf16 v[20:23], v[86:89], v[110:113], v[20:23]
	v_mfma_f32_16x16x32_bf16 v[16:19], v[94:97], v[110:113], v[16:19]
	v_mfma_f32_16x16x32_bf16 v[12:15], v[86:89], v[118:121], v[12:15]
	v_mfma_f32_16x16x32_bf16 v[8:11], v[94:97], v[118:121], v[8:11]
	v_mfma_f32_16x16x32_bf16 v[4:7], v[86:89], v[126:129], v[4:7]
	v_mfma_f32_16x16x32_bf16 v[0:3], v[94:97], v[126:129], v[0:3]
	s_barrier
	s_addk_i32 s20, 0x100
	s_add_i32 s21, s21, 2
	s_cmp_gt_u32 s21, 5
	s_cbranch_scc0 .LBB0_1585
	s_and_b64 vcc, exec, s[16:17]
	s_cbranch_vccz .LBB0_1590
	s_barrier
	s_andn2_b64 vcc, exec, s[6:7]
	s_mov_b64 s[20:21], -1
	s_cbranch_vccz .LBB0_1591

.LBB0_1776:
	s_add_i32 s27, 0, 0x10000
	s_add_i32 s59, 0, 0x14000
	v_add_u32_e32 v128, s27, v171
	v_add_u32_e32 v129, s59, v171
	ds_read_b128 v[130:133], v128
	ds_read_b128 v[162:165], v128 offset:1024
	ds_read_b128 v[178:181], v128 offset:2048
	ds_read_b128 v[182:185], v128 offset:3072
	ds_read_b128 v[186:189], v129
	ds_read_b128 v[190:193], v129 offset:1024
	ds_read_b128 v[194:197], v129 offset:2048
	ds_read_b128 v[198:201], v129 offset:3072
	s_add_i32 s26, s84, s5
	s_add_u32 s60, s3, s26
	s_addc_u32 s61, s36, 0
	s_add_i32 vcc_lo, s63, 0xc000
	s_add_i32 s35, s63, 0xe000
	s_add_i32 s42, s5, 0xfffe0080
	s_cmp_eq_u32 s70, s34
	s_cselect_b32 s50, s4, s84
	s_cselect_b32 s58, s85, s97
	s_mov_b32 m0, vcc_lo
	v_lshl_add_u64 v[134:135], s[60:61], 0, v[148:149]
	ds_read_b128 v[202:205], v172
	ds_read_b128 v[206:209], v172 offset:1024
	ds_read_b128 v[210:213], v172 offset:2048
	ds_read_b128 v[214:217], v172 offset:3072
	ds_read_b128 v[218:221], v172 offset:4096
	ds_read_b128 v[222:225], v172 offset:5120
	ds_read_b128 v[226:229], v172 offset:6144
	ds_read_b128 v[230:233], v172 offset:7168
	global_load_lds_dwordx4 v[134:135], off
	v_lshl_add_u64 v[134:135], s[60:61], 0, v[146:147]
	s_mov_b32 m0, s35
	s_nop 0
	global_load_lds_dwordx4 v[134:135], off
	s_waitcnt vmcnt(8)
	s_waitcnt lgkmcnt(0)
	s_barrier
	s_waitcnt lgkmcnt(0)
	v_mfma_f32_16x16x32_bf16 v[124:127], v[130:133], v[202:205], v[124:127]
	v_mfma_f32_16x16x32_bf16 v[120:123], v[178:181], v[202:205], v[120:123]
	v_mfma_f32_16x16x32_bf16 v[116:119], v[130:133], v[210:213], v[116:119]
	v_mfma_f32_16x16x32_bf16 v[112:115], v[178:181], v[210:213], v[112:115]
	v_mfma_f32_16x16x32_bf16 v[108:111], v[130:133], v[218:221], v[108:111]
	v_mfma_f32_16x16x32_bf16 v[104:107], v[178:181], v[218:221], v[104:107]
	v_mfma_f32_16x16x32_bf16 v[100:103], v[130:133], v[226:229], v[100:103]
	v_mfma_f32_16x16x32_bf16 v[96:99], v[178:181], v[226:229], v[96:99]
	v_mfma_f32_16x16x32_bf16 v[124:127], v[162:165], v[206:209], v[124:127]
	v_mfma_f32_16x16x32_bf16 v[120:123], v[182:185], v[206:209], v[120:123]
	v_mfma_f32_16x16x32_bf16 v[116:119], v[162:165], v[214:217], v[116:119]
	v_mfma_f32_16x16x32_bf16 v[112:115], v[182:185], v[214:217], v[112:115]
	v_mfma_f32_16x16x32_bf16 v[108:111], v[162:165], v[222:225], v[108:111]
	v_mfma_f32_16x16x32_bf16 v[104:107], v[182:185], v[222:225], v[104:107]
	v_mfma_f32_16x16x32_bf16 v[100:103], v[162:165], v[230:233], v[100:103]
	v_mfma_f32_16x16x32_bf16 v[96:99], v[182:185], v[230:233], v[96:99]
	v_mfma_f32_16x16x32_bf16 v[92:95], v[186:189], v[202:205], v[92:95]
	v_mfma_f32_16x16x32_bf16 v[88:91], v[194:197], v[202:205], v[88:91]
	v_mfma_f32_16x16x32_bf16 v[84:87], v[186:189], v[210:213], v[84:87]
	v_mfma_f32_16x16x32_bf16 v[80:83], v[194:197], v[210:213], v[80:83]
	v_mfma_f32_16x16x32_bf16 v[76:79], v[186:189], v[218:221], v[76:79]
	v_mfma_f32_16x16x32_bf16 v[72:75], v[194:197], v[218:221], v[72:75]
	v_mfma_f32_16x16x32_bf16 v[68:71], v[186:189], v[226:229], v[68:71]
	v_mfma_f32_16x16x32_bf16 v[64:67], v[194:197], v[226:229], v[64:67]
	v_mfma_f32_16x16x32_bf16 v[92:95], v[190:193], v[206:209], v[92:95]
	v_mfma_f32_16x16x32_bf16 v[88:91], v[198:201], v[206:209], v[88:91]
	v_mfma_f32_16x16x32_bf16 v[84:87], v[190:193], v[214:217], v[84:87]
	v_mfma_f32_16x16x32_bf16 v[80:83], v[198:201], v[214:217], v[80:83]
	v_mfma_f32_16x16x32_bf16 v[76:79], v[190:193], v[222:225], v[76:79]
	v_mfma_f32_16x16x32_bf16 v[72:75], v[198:201], v[222:225], v[72:75]
	v_mfma_f32_16x16x32_bf16 v[68:71], v[190:193], v[230:233], v[68:71]
	v_mfma_f32_16x16x32_bf16 v[64:67], v[198:201], v[230:233], v[64:67]
	s_barrier
	s_cselect_b32 s44, 0, s42
	s_add_i32 s42, s44, s58
	s_ashr_i32 s43, s42, 31
	s_add_u32 s60, s6, s42
	s_addc_u32 s61, s7, s43
	s_add_i32 s51, s58, 0xffffff00
	s_add_i32 s27, s27, s48
	s_add_i32 s42, s51, s44
	v_lshl_add_u64 v[134:135], s[60:61], 0, v[144:145]
	s_mov_b32 m0, s27
	s_add_i32 vcc_hi, s27, 0x2000
	s_ashr_i32 s43, s42, 31
	ds_read_b128 v[202:205], v172 offset:16384
	ds_read_b128 v[206:209], v172 offset:17408
	ds_read_b128 v[210:213], v172 offset:18432
	ds_read_b128 v[214:217], v172 offset:19456
	ds_read_b128 v[218:221], v172 offset:20480
	ds_read_b128 v[222:225], v172 offset:21504
	ds_read_b128 v[226:229], v172 offset:22528
	ds_read_b128 v[230:233], v172 offset:23552
	global_load_lds_dwordx4 v[134:135], off
	v_lshl_add_u64 v[134:135], s[60:61], 0, v[142:143]
	s_add_u32 s60, s6, s42
	s_mov_b32 m0, vcc_hi
	s_addc_u32 s61, s7, s43
	s_add_i32 s59, s59, s48
	global_load_lds_dwordx4 v[134:135], off
	v_lshl_add_u64 v[134:135], s[60:61], 0, v[144:145]
	s_mov_b32 m0, s59
	s_add_i32 s49, s44, s50
	global_load_lds_dwordx4 v[134:135], off
	v_lshl_add_u64 v[134:135], s[60:61], 0, v[142:143]
	s_add_i32 s60, s59, 0x2000
	s_add_u32 s42, s3, s49
	s_mov_b32 m0, s60
	s_addc_u32 s43, s36, 0
	global_load_lds_dwordx4 v[134:135], off
	v_lshl_add_u64 v[134:135], s[42:43], 0, v[148:149]
	s_mov_b32 m0, s63
	s_nop 0
	global_load_lds_dwordx4 v[134:135], off
	v_lshl_add_u64 v[134:135], s[42:43], 0, v[146:147]
	s_mov_b32 m0, s66
	s_nop 0
	global_load_lds_dwordx4 v[134:135], off
	s_waitcnt vmcnt(8)
	s_waitcnt lgkmcnt(0)
	s_barrier
	s_waitcnt lgkmcnt(0)
	v_mfma_f32_16x16x32_bf16 v[60:63], v[130:133], v[202:205], v[60:63]
	v_mfma_f32_16x16x32_bf16 v[56:59], v[178:181], v[202:205], v[56:59]
	v_mfma_f32_16x16x32_bf16 v[52:55], v[130:133], v[210:213], v[52:55]
	v_mfma_f32_16x16x32_bf16 v[48:51], v[178:181], v[210:213], v[48:51]
	v_mfma_f32_16x16x32_bf16 v[44:47], v[130:133], v[218:221], v[44:47]
	v_mfma_f32_16x16x32_bf16 v[40:43], v[178:181], v[218:221], v[40:43]
	v_mfma_f32_16x16x32_bf16 v[36:39], v[130:133], v[226:229], v[36:39]
	v_mfma_f32_16x16x32_bf16 v[32:35], v[178:181], v[226:229], v[32:35]
	v_mfma_f32_16x16x32_bf16 v[60:63], v[162:165], v[206:209], v[60:63]
	v_mfma_f32_16x16x32_bf16 v[56:59], v[182:185], v[206:209], v[56:59]
	v_mfma_f32_16x16x32_bf16 v[52:55], v[162:165], v[214:217], v[52:55]
	v_mfma_f32_16x16x32_bf16 v[48:51], v[182:185], v[214:217], v[48:51]
	v_mfma_f32_16x16x32_bf16 v[44:47], v[162:165], v[222:225], v[44:47]
	v_mfma_f32_16x16x32_bf16 v[40:43], v[182:185], v[222:225], v[40:43]
	v_mfma_f32_16x16x32_bf16 v[36:39], v[162:165], v[230:233], v[36:39]
	v_mfma_f32_16x16x32_bf16 v[32:35], v[182:185], v[230:233], v[32:35]
	v_mfma_f32_16x16x32_bf16 v[28:31], v[186:189], v[202:205], v[28:31]
	v_mfma_f32_16x16x32_bf16 v[24:27], v[194:197], v[202:205], v[24:27]
	v_mfma_f32_16x16x32_bf16 v[20:23], v[186:189], v[210:213], v[20:23]
	v_mfma_f32_16x16x32_bf16 v[16:19], v[194:197], v[210:213], v[16:19]
	v_mfma_f32_16x16x32_bf16 v[12:15], v[186:189], v[218:221], v[12:15]
	v_mfma_f32_16x16x32_bf16 v[8:11], v[194:197], v[218:221], v[8:11]
	v_mfma_f32_16x16x32_bf16 v[4:7], v[186:189], v[226:229], v[4:7]
	v_mfma_f32_16x16x32_bf16 v[0:3], v[194:197], v[226:229], v[0:3]
	v_mfma_f32_16x16x32_bf16 v[28:31], v[190:193], v[206:209], v[28:31]
	v_mfma_f32_16x16x32_bf16 v[24:27], v[198:201], v[206:209], v[24:27]
	v_mfma_f32_16x16x32_bf16 v[20:23], v[190:193], v[214:217], v[20:23]
	v_mfma_f32_16x16x32_bf16 v[16:19], v[198:201], v[214:217], v[16:19]
	v_mfma_f32_16x16x32_bf16 v[12:15], v[190:193], v[222:225], v[12:15]
	v_mfma_f32_16x16x32_bf16 v[8:11], v[198:201], v[222:225], v[8:11]
	v_mfma_f32_16x16x32_bf16 v[4:7], v[190:193], v[230:233], v[4:7]
	v_mfma_f32_16x16x32_bf16 v[0:3], v[198:201], v[230:233], v[0:3]
	s_barrier
	s_add_i32 s61, 0, 0x18000
	s_add_i32 s26, 0, 0x1c000
	v_add_u32_e32 v130, s61, v171
	v_add_u32_e32 v131, s26, v171
	ds_read_b128 v[132:135], v130
	ds_read_b128 v[162:165], v130 offset:1024
	ds_read_b128 v[178:181], v130 offset:2048
	ds_read_b128 v[182:185], v130 offset:3072
	ds_read_b128 v[186:189], v131
	ds_read_b128 v[190:193], v131 offset:1024
	ds_read_b128 v[194:197], v131 offset:2048
	ds_read_b128 v[198:201], v131 offset:3072
	s_add_i32 s49, s49, 0x20000
	s_add_u32 s42, s3, s49
	s_addc_u32 s43, s36, 0
	s_mov_b32 m0, s67
	v_lshl_add_u64 v[166:167], s[42:43], 0, v[148:149]
	ds_read_b128 v[202:205], v172 offset:32768
	ds_read_b128 v[206:209], v172 offset:33792
	ds_read_b128 v[210:213], v172 offset:34816
	ds_read_b128 v[214:217], v172 offset:35840
	ds_read_b128 v[218:221], v172 offset:36864
	ds_read_b128 v[222:225], v172 offset:37888
	ds_read_b128 v[226:229], v172 offset:38912
	ds_read_b128 v[230:233], v172 offset:39936
	global_load_lds_dwordx4 v[166:167], off
	v_lshl_add_u64 v[166:167], s[42:43], 0, v[146:147]
	s_mov_b32 m0, s68
	s_nop 0
	global_load_lds_dwordx4 v[166:167], off
	s_waitcnt vmcnt(8)
	s_waitcnt lgkmcnt(0)
	s_barrier
	s_waitcnt lgkmcnt(0)
	v_mfma_f32_16x16x32_bf16 v[124:127], v[132:135], v[202:205], v[124:127]
	v_mfma_f32_16x16x32_bf16 v[120:123], v[178:181], v[202:205], v[120:123]
	v_mfma_f32_16x16x32_bf16 v[116:119], v[132:135], v[210:213], v[116:119]
	v_mfma_f32_16x16x32_bf16 v[112:115], v[178:181], v[210:213], v[112:115]
	v_mfma_f32_16x16x32_bf16 v[108:111], v[132:135], v[218:221], v[108:111]
	v_mfma_f32_16x16x32_bf16 v[104:107], v[178:181], v[218:221], v[104:107]
	v_mfma_f32_16x16x32_bf16 v[100:103], v[132:135], v[226:229], v[100:103]
	v_mfma_f32_16x16x32_bf16 v[96:99], v[178:181], v[226:229], v[96:99]
	v_mfma_f32_16x16x32_bf16 v[124:127], v[162:165], v[206:209], v[124:127]
	v_mfma_f32_16x16x32_bf16 v[120:123], v[182:185], v[206:209], v[120:123]
	v_mfma_f32_16x16x32_bf16 v[116:119], v[162:165], v[214:217], v[116:119]
	v_mfma_f32_16x16x32_bf16 v[112:115], v[182:185], v[214:217], v[112:115]
	v_mfma_f32_16x16x32_bf16 v[108:111], v[162:165], v[222:225], v[108:111]
	v_mfma_f32_16x16x32_bf16 v[104:107], v[182:185], v[222:225], v[104:107]
	v_mfma_f32_16x16x32_bf16 v[100:103], v[162:165], v[230:233], v[100:103]
	v_mfma_f32_16x16x32_bf16 v[96:99], v[182:185], v[230:233], v[96:99]
	v_mfma_f32_16x16x32_bf16 v[92:95], v[186:189], v[202:205], v[92:95]
	v_mfma_f32_16x16x32_bf16 v[88:91], v[194:197], v[202:205], v[88:91]
	v_mfma_f32_16x16x32_bf16 v[84:87], v[186:189], v[210:213], v[84:87]
	v_mfma_f32_16x16x32_bf16 v[80:83], v[194:197], v[210:213], v[80:83]
	v_mfma_f32_16x16x32_bf16 v[76:79], v[186:189], v[218:221], v[76:79]
	v_mfma_f32_16x16x32_bf16 v[72:75], v[194:197], v[218:221], v[72:75]
	v_mfma_f32_16x16x32_bf16 v[68:71], v[186:189], v[226:229], v[68:71]
	v_mfma_f32_16x16x32_bf16 v[64:67], v[194:197], v[226:229], v[64:67]
	v_mfma_f32_16x16x32_bf16 v[92:95], v[190:193], v[206:209], v[92:95]
	v_mfma_f32_16x16x32_bf16 v[88:91], v[198:201], v[206:209], v[88:91]
	v_mfma_f32_16x16x32_bf16 v[84:87], v[190:193], v[214:217], v[84:87]
	v_mfma_f32_16x16x32_bf16 v[80:83], v[198:201], v[214:217], v[80:83]
	v_mfma_f32_16x16x32_bf16 v[76:79], v[190:193], v[222:225], v[76:79]
	v_mfma_f32_16x16x32_bf16 v[72:75], v[198:201], v[222:225], v[72:75]
	v_mfma_f32_16x16x32_bf16 v[68:71], v[190:193], v[230:233], v[68:71]
	v_mfma_f32_16x16x32_bf16 v[64:67], v[198:201], v[230:233], v[64:67]
	s_barrier
; template <class Epi, class Sched, class Hook = NoHook>
; __device__ __forceinline__ void gemm_phase_w(LAS unsigned char* lds, const Sched& S, const Epi& E, int wave_id, const Hook& HK = Hook()) {
;     ...
;         if constexpr (!SEG2) {
;             for (int tt = 0; tt < nt; tt += 2) {
;                 if constexpr (GATHER) { if (tt == nt - 2) {
;                     if (has_next) { gnxt_00 = S.grow_l(nxt, lds, nbuf, R0) + (unsigned)(C0 * 2); gnxt_01 = S.grow_l(nxt, lds, nbuf, R1) + (unsigned)(C1 * 2); gnxt_10 = S.grow_l(nxt, lds, nbuf, 128 + R0) + (unsigned)(C0 * 2); gnxt_11 = S.grow_l(nxt, lds, nbuf, 128 + R1) + (unsigned)(C1 * 2); }
;                     else { gnxt_00 = gcur_00; gnxt_01 = gcur_01; gnxt_10 = gcur_10; gnxt_11 = gcur_11; } } }
;                 PG_TRIP(tt, false, false, false);
;             }
;         } else {
;             for (int tt = 0; tt < nt - 4; tt += 2) PG_TRIP(tt, false, false, false);
;             PG_TRIP(nt - 4, false, true, false);
;             PG_TRIP(nt - 2, true, false, true);
	s_or_b32 s18, s44, 0x80
	s_add_i32 s19, s18, s58
	s_ashr_i32 s43, s19, 31
	s_add_u32 s42, s6, s19
	s_addc_u32 s43, s7, s43
	s_add_i32 s61, s61, s48
	v_lshl_add_u64 v[166:167], s[42:43], 0, v[144:145]
	s_mov_b32 m0, s61
	s_add_i32 s19, s18, s51
	ds_read_b128 v[202:205], v172 offset:49152
	ds_read_b128 v[206:209], v172 offset:50176
	ds_read_b128 v[210:213], v172 offset:51200
	ds_read_b128 v[214:217], v172 offset:52224
	ds_read_b128 v[218:221], v172 offset:53248
	ds_read_b128 v[222:225], v172 offset:54272
	ds_read_b128 v[226:229], v172 offset:55296
	ds_read_b128 v[230:233], v172 offset:56320
	global_load_lds_dwordx4 v[166:167], off
	v_lshl_add_u64 v[166:167], s[42:43], 0, v[142:143]
	s_add_i32 s49, s61, 0x2000
	s_ashr_i32 s43, s19, 31
	s_add_u32 s42, s6, s19
	s_mov_b32 m0, s49
	s_addc_u32 s43, s7, s43
	s_add_i32 s26, s26, s48
	global_load_lds_dwordx4 v[166:167], off
	v_lshl_add_u64 v[166:167], s[42:43], 0, v[144:145]
	s_mov_b32 m0, s26
	s_add_i32 s44, s26, 0x2000
	s_add_i32 s18, s18, s50
	global_load_lds_dwordx4 v[166:167], off
	v_lshl_add_u64 v[166:167], s[42:43], 0, v[142:143]
	s_add_u32 s42, s3, s18
	s_mov_b32 m0, s44
	s_addc_u32 s43, s36, 0
	global_load_lds_dwordx4 v[166:167], off
	v_lshl_add_u64 v[166:167], s[42:43], 0, v[148:149]
	s_mov_b32 m0, s71
	s_nop 0
	global_load_lds_dwordx4 v[166:167], off
	v_lshl_add_u64 v[166:167], s[42:43], 0, v[146:147]
	s_mov_b32 m0, s72
	s_nop 0
	global_load_lds_dwordx4 v[166:167], off
	s_waitcnt vmcnt(8)
	s_waitcnt lgkmcnt(0)
	s_barrier
	s_waitcnt lgkmcnt(0)
	v_mfma_f32_16x16x32_bf16 v[60:63], v[132:135], v[202:205], v[60:63]
	v_mfma_f32_16x16x32_bf16 v[56:59], v[178:181], v[202:205], v[56:59]
	v_mfma_f32_16x16x32_bf16 v[52:55], v[132:135], v[210:213], v[52:55]
	v_mfma_f32_16x16x32_bf16 v[48:51], v[178:181], v[210:213], v[48:51]
	v_mfma_f32_16x16x32_bf16 v[44:47], v[132:135], v[218:221], v[44:47]
	v_mfma_f32_16x16x32_bf16 v[40:43], v[178:181], v[218:221], v[40:43]
	v_mfma_f32_16x16x32_bf16 v[36:39], v[132:135], v[226:229], v[36:39]
	v_mfma_f32_16x16x32_bf16 v[32:35], v[178:181], v[226:229], v[32:35]
	v_mfma_f32_16x16x32_bf16 v[60:63], v[162:165], v[206:209], v[60:63]
	v_mfma_f32_16x16x32_bf16 v[56:59], v[182:185], v[206:209], v[56:59]
	v_mfma_f32_16x16x32_bf16 v[52:55], v[162:165], v[214:217], v[52:55]
	v_mfma_f32_16x16x32_bf16 v[48:51], v[182:185], v[214:217], v[48:51]
	v_mfma_f32_16x16x32_bf16 v[44:47], v[162:165], v[222:225], v[44:47]
	v_mfma_f32_16x16x32_bf16 v[40:43], v[182:185], v[222:225], v[40:43]
	v_mfma_f32_16x16x32_bf16 v[36:39], v[162:165], v[230:233], v[36:39]
	v_mfma_f32_16x16x32_bf16 v[32:35], v[182:185], v[230:233], v[32:35]
	v_mfma_f32_16x16x32_bf16 v[28:31], v[186:189], v[202:205], v[28:31]
	v_mfma_f32_16x16x32_bf16 v[24:27], v[194:197], v[202:205], v[24:27]
	v_mfma_f32_16x16x32_bf16 v[20:23], v[186:189], v[210:213], v[20:23]
	v_mfma_f32_16x16x32_bf16 v[16:19], v[194:197], v[210:213], v[16:19]
	v_mfma_f32_16x16x32_bf16 v[12:15], v[186:189], v[218:221], v[12:15]
	v_mfma_f32_16x16x32_bf16 v[8:11], v[194:197], v[218:221], v[8:11]
	v_mfma_f32_16x16x32_bf16 v[4:7], v[186:189], v[226:229], v[4:7]
	v_mfma_f32_16x16x32_bf16 v[0:3], v[194:197], v[226:229], v[0:3]
	v_mfma_f32_16x16x32_bf16 v[28:31], v[190:193], v[206:209], v[28:31]
	v_mfma_f32_16x16x32_bf16 v[24:27], v[198:201], v[206:209], v[24:27]
	v_mfma_f32_16x16x32_bf16 v[20:23], v[190:193], v[214:217], v[20:23]
	v_mfma_f32_16x16x32_bf16 v[16:19], v[198:201], v[214:217], v[16:19]
	v_mfma_f32_16x16x32_bf16 v[12:15], v[190:193], v[222:225], v[12:15]
	v_mfma_f32_16x16x32_bf16 v[8:11], v[198:201], v[222:225], v[8:11]
	v_mfma_f32_16x16x32_bf16 v[4:7], v[190:193], v[230:233], v[4:7]
	v_mfma_f32_16x16x32_bf16 v[0:3], v[198:201], v[230:233], v[0:3]
	s_barrier
	s_addk_i32 s5, 0x100
	s_add_i32 s18, s34, 2
	s_add_i32 s19, s34, 4
	s_cmp_ge_u32 s19, s70
	s_mov_b32 s34, s18
	s_cbranch_scc0 .LBB0_1776
	ds_read_b128 v[132:135], v128
	ds_read_b128 v[162:165], v128 offset:1024
	ds_read_b128 v[178:181], v128 offset:2048
	ds_read_b128 v[182:185], v128 offset:3072
	ds_read_b128 v[186:189], v129
	ds_read_b128 v[190:193], v129 offset:1024
	ds_read_b128 v[194:197], v129 offset:2048
	ds_read_b128 v[198:201], v129 offset:3072
	s_add_i32 s5, s73, s84
	s_add_u32 s50, s3, s5
	s_addc_u32 s51, s36, 0
	s_mov_b32 m0, vcc_lo
	v_lshl_add_u64 v[166:167], s[50:51], 0, v[148:149]
	ds_read_b128 v[202:205], v172
	ds_read_b128 v[206:209], v172 offset:1024
	ds_read_b128 v[210:213], v172 offset:2048
	ds_read_b128 v[214:217], v172 offset:3072
	ds_read_b128 v[218:221], v172 offset:4096
	ds_read_b128 v[222:225], v172 offset:5120
	ds_read_b128 v[226:229], v172 offset:6144
	ds_read_b128 v[230:233], v172 offset:7168
	global_load_lds_dwordx4 v[166:167], off
	v_lshl_add_u64 v[166:167], s[50:51], 0, v[146:147]
	s_mov_b32 m0, s35
	s_nop 0
	global_load_lds_dwordx4 v[166:167], off
	s_waitcnt vmcnt(8)
	s_waitcnt lgkmcnt(0)
	s_barrier
; template <class Epi, class Sched, class Hook = NoHook>
; __device__ __forceinline__ void gemm_phase_w(LAS unsigned char* lds, const Sched& S, const Epi& E, int wave_id, const Hook& HK = Hook()) {
;     ...
;             PG_TRIP(nt - 4, false, true, false);
;             PG_TRIP(nt - 2, true, false, true);
	s_waitcnt lgkmcnt(0)
	v_mfma_f32_16x16x32_bf16 v[124:127], v[132:135], v[202:205], v[124:127]
	v_mfma_f32_16x16x32_bf16 v[120:123], v[178:181], v[202:205], v[120:123]
	v_mfma_f32_16x16x32_bf16 v[116:119], v[132:135], v[210:213], v[116:119]
	v_mfma_f32_16x16x32_bf16 v[112:115], v[178:181], v[210:213], v[112:115]
	v_mfma_f32_16x16x32_bf16 v[108:111], v[132:135], v[218:221], v[108:111]
	v_mfma_f32_16x16x32_bf16 v[104:107], v[178:181], v[218:221], v[104:107]
	v_mfma_f32_16x16x32_bf16 v[100:103], v[132:135], v[226:229], v[100:103]
	v_mfma_f32_16x16x32_bf16 v[96:99], v[178:181], v[226:229], v[96:99]
	v_mfma_f32_16x16x32_bf16 v[124:127], v[162:165], v[206:209], v[124:127]
	v_mfma_f32_16x16x32_bf16 v[120:123], v[182:185], v[206:209], v[120:123]
	v_mfma_f32_16x16x32_bf16 v[116:119], v[162:165], v[214:217], v[116:119]
	v_mfma_f32_16x16x32_bf16 v[112:115], v[182:185], v[214:217], v[112:115]
	v_mfma_f32_16x16x32_bf16 v[108:111], v[162:165], v[222:225], v[108:111]
	v_mfma_f32_16x16x32_bf16 v[104:107], v[182:185], v[222:225], v[104:107]
	v_mfma_f32_16x16x32_bf16 v[100:103], v[162:165], v[230:233], v[100:103]
	v_mfma_f32_16x16x32_bf16 v[96:99], v[182:185], v[230:233], v[96:99]
	v_mfma_f32_16x16x32_bf16 v[92:95], v[186:189], v[202:205], v[92:95]
	v_mfma_f32_16x16x32_bf16 v[88:91], v[194:197], v[202:205], v[88:91]
	v_mfma_f32_16x16x32_bf16 v[84:87], v[186:189], v[210:213], v[84:87]
	v_mfma_f32_16x16x32_bf16 v[80:83], v[194:197], v[210:213], v[80:83]
	v_mfma_f32_16x16x32_bf16 v[76:79], v[186:189], v[218:221], v[76:79]
	v_mfma_f32_16x16x32_bf16 v[72:75], v[194:197], v[218:221], v[72:75]
	v_mfma_f32_16x16x32_bf16 v[68:71], v[186:189], v[226:229], v[68:71]
	v_mfma_f32_16x16x32_bf16 v[64:67], v[194:197], v[226:229], v[64:67]
	v_mfma_f32_16x16x32_bf16 v[92:95], v[190:193], v[206:209], v[92:95]
	v_mfma_f32_16x16x32_bf16 v[88:91], v[198:201], v[206:209], v[88:91]
	v_mfma_f32_16x16x32_bf16 v[84:87], v[190:193], v[214:217], v[84:87]
	v_mfma_f32_16x16x32_bf16 v[80:83], v[198:201], v[214:217], v[80:83]
	v_mfma_f32_16x16x32_bf16 v[76:79], v[190:193], v[222:225], v[76:79]
	v_mfma_f32_16x16x32_bf16 v[72:75], v[198:201], v[222:225], v[72:75]
	v_mfma_f32_16x16x32_bf16 v[68:71], v[190:193], v[230:233], v[68:71]
	v_mfma_f32_16x16x32_bf16 v[64:67], v[198:201], v[230:233], v[64:67]
	s_barrier
	s_ashr_i32 s5, s31, 31
	s_add_u32 s50, s8, s31
	s_addc_u32 s51, s9, s5
	s_add_i32 s5, s31, 0x8000
	s_mov_b32 m0, s27
	v_lshl_add_u64 v[166:167], s[50:51], 0, v[138:139]
	s_ashr_i32 s34, s5, 31
	ds_read_b128 v[202:205], v172 offset:16384
	ds_read_b128 v[206:209], v172 offset:17408
	ds_read_b128 v[210:213], v172 offset:18432
	ds_read_b128 v[214:217], v172 offset:19456
	ds_read_b128 v[218:221], v172 offset:20480
	ds_read_b128 v[222:225], v172 offset:21504
	ds_read_b128 v[226:229], v172 offset:22528
	ds_read_b128 v[230:233], v172 offset:23552
	global_load_lds_dwordx4 v[166:167], off
	v_lshl_add_u64 v[166:167], s[50:51], 0, v[140:141]
	s_add_u32 s50, s8, s5
	s_mov_b32 m0, vcc_hi
	s_addc_u32 s51, s9, s34
	global_load_lds_dwordx4 v[166:167], off
	v_lshl_add_u64 v[166:167], s[50:51], 0, v[138:139]
	s_mov_b32 m0, s59
	s_nop 0
	global_load_lds_dwordx4 v[166:167], off
	v_lshl_add_u64 v[166:167], s[50:51], 0, v[140:141]
	s_add_u32 s50, s37, s89
	s_mov_b32 m0, s60
	s_addc_u32 s51, s38, 0
	global_load_lds_dwordx4 v[166:167], off
	v_lshl_add_u64 v[166:167], s[50:51], 0, v[138:139]
	s_mov_b32 m0, s63
	s_nop 0
	global_load_lds_dwordx4 v[166:167], off
	v_lshl_add_u64 v[166:167], s[50:51], 0, v[140:141]
	s_mov_b32 m0, s66
	s_nop 0
	global_load_lds_dwordx4 v[166:167], off
	s_waitcnt vmcnt(8)
	s_waitcnt lgkmcnt(0)
	s_barrier
	s_waitcnt lgkmcnt(0)
	v_mfma_f32_16x16x32_bf16 v[60:63], v[132:135], v[202:205], v[60:63]
	v_mfma_f32_16x16x32_bf16 v[56:59], v[178:181], v[202:205], v[56:59]
	v_mfma_f32_16x16x32_bf16 v[52:55], v[132:135], v[210:213], v[52:55]
	v_mfma_f32_16x16x32_bf16 v[48:51], v[178:181], v[210:213], v[48:51]
	v_mfma_f32_16x16x32_bf16 v[44:47], v[132:135], v[218:221], v[44:47]
	v_mfma_f32_16x16x32_bf16 v[40:43], v[178:181], v[218:221], v[40:43]
	v_mfma_f32_16x16x32_bf16 v[36:39], v[132:135], v[226:229], v[36:39]
	v_mfma_f32_16x16x32_bf16 v[32:35], v[178:181], v[226:229], v[32:35]
	v_mfma_f32_16x16x32_bf16 v[60:63], v[162:165], v[206:209], v[60:63]
	v_mfma_f32_16x16x32_bf16 v[56:59], v[182:185], v[206:209], v[56:59]
	v_mfma_f32_16x16x32_bf16 v[52:55], v[162:165], v[214:217], v[52:55]
	v_mfma_f32_16x16x32_bf16 v[48:51], v[182:185], v[214:217], v[48:51]
	v_mfma_f32_16x16x32_bf16 v[44:47], v[162:165], v[222:225], v[44:47]
	v_mfma_f32_16x16x32_bf16 v[40:43], v[182:185], v[222:225], v[40:43]
	v_mfma_f32_16x16x32_bf16 v[36:39], v[162:165], v[230:233], v[36:39]
	v_mfma_f32_16x16x32_bf16 v[32:35], v[182:185], v[230:233], v[32:35]
	v_mfma_f32_16x16x32_bf16 v[28:31], v[186:189], v[202:205], v[28:31]
	v_mfma_f32_16x16x32_bf16 v[24:27], v[194:197], v[202:205], v[24:27]
	v_mfma_f32_16x16x32_bf16 v[20:23], v[186:189], v[210:213], v[20:23]
	v_mfma_f32_16x16x32_bf16 v[16:19], v[194:197], v[210:213], v[16:19]
	v_mfma_f32_16x16x32_bf16 v[4:7], v[186:189], v[226:229], v[4:7]
	v_mfma_f32_16x16x32_bf16 v[0:3], v[194:197], v[226:229], v[0:3]
	v_mfma_f32_16x16x32_bf16 v[28:31], v[190:193], v[206:209], v[28:31]
	v_mfma_f32_16x16x32_bf16 v[24:27], v[198:201], v[206:209], v[24:27]
	v_mfma_f32_16x16x32_bf16 v[20:23], v[190:193], v[214:217], v[20:23]
	v_mfma_f32_16x16x32_bf16 v[16:19], v[198:201], v[214:217], v[16:19]
	v_mfma_f32_16x16x32_bf16 v[12:15], v[186:189], v[218:221], v[12:15]
	v_mfma_f32_16x16x32_bf16 v[8:11], v[194:197], v[218:221], v[8:11]
	v_mfma_f32_16x16x32_bf16 v[4:7], v[190:193], v[230:233], v[4:7]
	v_mfma_f32_16x16x32_bf16 v[0:3], v[198:201], v[230:233], v[0:3]
	v_mfma_f32_16x16x32_bf16 v[12:15], v[190:193], v[222:225], v[12:15]
	v_mfma_f32_16x16x32_bf16 v[8:11], v[198:201], v[222:225], v[8:11]
	s_barrier
; template <class Epi, class Sched, class Hook = NoHook>
; __device__ __forceinline__ void gemm_phase_w(LAS unsigned char* lds, const Sched& S, const Epi& E, int wave_id, const Hook& HK = Hook()) {
;     ...
;             PG_TRIP(nt - 4, false, true, false);
;             PG_TRIP(nt - 2, true, false, true);
	ds_read_b128 v[132:135], v130
	ds_read_b128 v[162:165], v130 offset:1024
	ds_read_b128 v[178:181], v130 offset:2048
	ds_read_b128 v[182:185], v130 offset:3072
	ds_read_b128 v[186:189], v131
	ds_read_b128 v[190:193], v131 offset:1024
	ds_read_b128 v[194:197], v131 offset:2048
	ds_read_b128 v[198:201], v131 offset:3072
	s_add_i32 s5, s89, 0x8000
	s_add_u32 s50, s37, s5
	s_addc_u32 s51, s38, 0
	s_mov_b32 m0, s67
	v_lshl_add_u64 v[166:167], s[50:51], 0, v[138:139]
	ds_read_b128 v[202:205], v172 offset:32768
	ds_read_b128 v[206:209], v172 offset:33792
	ds_read_b128 v[210:213], v172 offset:34816
	ds_read_b128 v[214:217], v172 offset:35840
	ds_read_b128 v[218:221], v172 offset:36864
	ds_read_b128 v[222:225], v172 offset:37888
	ds_read_b128 v[226:229], v172 offset:38912
	ds_read_b128 v[230:233], v172 offset:39936
	global_load_lds_dwordx4 v[166:167], off
	v_lshl_add_u64 v[166:167], s[50:51], 0, v[140:141]
	s_mov_b32 m0, s68
	s_nop 0
	global_load_lds_dwordx4 v[166:167], off
	s_waitcnt vmcnt(8)
	s_waitcnt lgkmcnt(0)
	s_barrier
	s_waitcnt lgkmcnt(0)
	v_mfma_f32_16x16x32_bf16 v[124:127], v[132:135], v[202:205], v[124:127]
	v_mfma_f32_16x16x32_bf16 v[120:123], v[178:181], v[202:205], v[120:123]
	v_mfma_f32_16x16x32_bf16 v[116:119], v[132:135], v[210:213], v[116:119]
	v_mfma_f32_16x16x32_bf16 v[112:115], v[178:181], v[210:213], v[112:115]
	v_mfma_f32_16x16x32_bf16 v[108:111], v[132:135], v[218:221], v[108:111]
	v_mfma_f32_16x16x32_bf16 v[104:107], v[178:181], v[218:221], v[104:107]
	v_mfma_f32_16x16x32_bf16 v[100:103], v[132:135], v[226:229], v[100:103]
	v_mfma_f32_16x16x32_bf16 v[96:99], v[178:181], v[226:229], v[96:99]
	v_mfma_f32_16x16x32_bf16 v[124:127], v[162:165], v[206:209], v[124:127]
	v_mfma_f32_16x16x32_bf16 v[120:123], v[182:185], v[206:209], v[120:123]
	v_mfma_f32_16x16x32_bf16 v[116:119], v[162:165], v[214:217], v[116:119]
	v_mfma_f32_16x16x32_bf16 v[112:115], v[182:185], v[214:217], v[112:115]
	v_mfma_f32_16x16x32_bf16 v[108:111], v[162:165], v[222:225], v[108:111]
	v_mfma_f32_16x16x32_bf16 v[104:107], v[182:185], v[222:225], v[104:107]
	v_mfma_f32_16x16x32_bf16 v[100:103], v[162:165], v[230:233], v[100:103]
	v_mfma_f32_16x16x32_bf16 v[96:99], v[182:185], v[230:233], v[96:99]
	v_mfma_f32_16x16x32_bf16 v[92:95], v[186:189], v[202:205], v[92:95]
	v_mfma_f32_16x16x32_bf16 v[88:91], v[194:197], v[202:205], v[88:91]
	v_mfma_f32_16x16x32_bf16 v[84:87], v[186:189], v[210:213], v[84:87]
	v_mfma_f32_16x16x32_bf16 v[80:83], v[194:197], v[210:213], v[80:83]
	v_mfma_f32_16x16x32_bf16 v[76:79], v[186:189], v[218:221], v[76:79]
	v_mfma_f32_16x16x32_bf16 v[72:75], v[194:197], v[218:221], v[72:75]
	v_mfma_f32_16x16x32_bf16 v[68:71], v[186:189], v[226:229], v[68:71]
	v_mfma_f32_16x16x32_bf16 v[64:67], v[194:197], v[226:229], v[64:67]
	v_mfma_f32_16x16x32_bf16 v[92:95], v[190:193], v[206:209], v[92:95]
	v_mfma_f32_16x16x32_bf16 v[88:91], v[198:201], v[206:209], v[88:91]
	v_mfma_f32_16x16x32_bf16 v[84:87], v[190:193], v[214:217], v[84:87]
	v_mfma_f32_16x16x32_bf16 v[80:83], v[198:201], v[214:217], v[80:83]
	v_mfma_f32_16x16x32_bf16 v[76:79], v[190:193], v[222:225], v[76:79]
	v_mfma_f32_16x16x32_bf16 v[72:75], v[198:201], v[222:225], v[72:75]
	v_mfma_f32_16x16x32_bf16 v[68:71], v[190:193], v[230:233], v[68:71]
	v_mfma_f32_16x16x32_bf16 v[64:67], v[198:201], v[230:233], v[64:67]
	s_barrier
	s_add_i32 s50, s31, 0x80
	s_ashr_i32 s51, s50, 31
	s_add_i32 s5, s31, 0x8080
	s_mov_b32 m0, s61
	v_lshl_add_u64 v[166:167], v[154:155], 0, s[50:51]
	s_ashr_i32 s31, s5, 31
	ds_read_b128 v[202:205], v172 offset:49152
	ds_read_b128 v[206:209], v172 offset:50176
	ds_read_b128 v[210:213], v172 offset:51200
	ds_read_b128 v[214:217], v172 offset:52224
	ds_read_b128 v[218:221], v172 offset:53248
	ds_read_b128 v[222:225], v172 offset:54272
	ds_read_b128 v[226:229], v172 offset:55296
	ds_read_b128 v[230:233], v172 offset:56320
	global_load_lds_dwordx4 v[166:167], off
	v_lshl_add_u64 v[166:167], v[156:157], 0, s[50:51]
	s_add_u32 s50, s8, s5
	s_mov_b32 m0, s49
	s_addc_u32 s51, s9, s31
	global_load_lds_dwordx4 v[166:167], off
	v_lshl_add_u64 v[166:167], s[50:51], 0, v[138:139]
	s_mov_b32 m0, s26
	s_add_i32 s5, s89, 0x80
	global_load_lds_dwordx4 v[166:167], off
	v_lshl_add_u64 v[166:167], s[50:51], 0, v[140:141]
	s_add_u32 s50, s37, s5
	s_mov_b32 m0, s44
	s_addc_u32 s51, s38, 0
	global_load_lds_dwordx4 v[166:167], off
	v_lshl_add_u64 v[166:167], s[50:51], 0, v[138:139]
	s_mov_b32 m0, s71
	s_nop 0
	global_load_lds_dwordx4 v[166:167], off
	v_lshl_add_u64 v[166:167], s[50:51], 0, v[140:141]
	s_mov_b32 m0, s72
	s_nop 0
	global_load_lds_dwordx4 v[166:167], off
	s_waitcnt vmcnt(8)
	s_waitcnt lgkmcnt(0)
	s_barrier
; template <class Epi, class Sched, class Hook = NoHook>
; __device__ __forceinline__ void gemm_phase_w(LAS unsigned char* lds, const Sched& S, const Epi& E, int wave_id, const Hook& HK = Hook()) {
;     ...
;             PG_TRIP(nt - 4, false, true, false);
;             PG_TRIP(nt - 2, true, false, true);
	s_waitcnt lgkmcnt(0)
	v_mfma_f32_16x16x32_bf16 v[60:63], v[132:135], v[202:205], v[60:63]
	v_mfma_f32_16x16x32_bf16 v[56:59], v[178:181], v[202:205], v[56:59]
	v_mfma_f32_16x16x32_bf16 v[52:55], v[132:135], v[210:213], v[52:55]
	v_mfma_f32_16x16x32_bf16 v[48:51], v[178:181], v[210:213], v[48:51]
	v_mfma_f32_16x16x32_bf16 v[44:47], v[132:135], v[218:221], v[44:47]
	v_mfma_f32_16x16x32_bf16 v[40:43], v[178:181], v[218:221], v[40:43]
	v_mfma_f32_16x16x32_bf16 v[36:39], v[132:135], v[226:229], v[36:39]
	v_mfma_f32_16x16x32_bf16 v[32:35], v[178:181], v[226:229], v[32:35]
	v_mfma_f32_16x16x32_bf16 v[60:63], v[162:165], v[206:209], v[60:63]
	v_mfma_f32_16x16x32_bf16 v[56:59], v[182:185], v[206:209], v[56:59]
	v_mfma_f32_16x16x32_bf16 v[52:55], v[162:165], v[214:217], v[52:55]
	v_mfma_f32_16x16x32_bf16 v[48:51], v[182:185], v[214:217], v[48:51]
	v_mfma_f32_16x16x32_bf16 v[44:47], v[162:165], v[222:225], v[44:47]
	v_mfma_f32_16x16x32_bf16 v[40:43], v[182:185], v[222:225], v[40:43]
	v_mfma_f32_16x16x32_bf16 v[36:39], v[162:165], v[230:233], v[36:39]
	v_mfma_f32_16x16x32_bf16 v[32:35], v[182:185], v[230:233], v[32:35]
	v_mfma_f32_16x16x32_bf16 v[28:31], v[186:189], v[202:205], v[28:31]
	v_mfma_f32_16x16x32_bf16 v[24:27], v[194:197], v[202:205], v[24:27]
	v_mfma_f32_16x16x32_bf16 v[20:23], v[186:189], v[210:213], v[20:23]
	v_mfma_f32_16x16x32_bf16 v[16:19], v[194:197], v[210:213], v[16:19]
	v_mfma_f32_16x16x32_bf16 v[4:7], v[186:189], v[226:229], v[4:7]
	v_mfma_f32_16x16x32_bf16 v[0:3], v[194:197], v[226:229], v[0:3]
	v_mfma_f32_16x16x32_bf16 v[28:31], v[190:193], v[206:209], v[28:31]
	v_mfma_f32_16x16x32_bf16 v[24:27], v[198:201], v[206:209], v[24:27]
	v_mfma_f32_16x16x32_bf16 v[20:23], v[190:193], v[214:217], v[20:23]
	v_mfma_f32_16x16x32_bf16 v[16:19], v[198:201], v[214:217], v[16:19]
	v_mfma_f32_16x16x32_bf16 v[12:15], v[186:189], v[218:221], v[12:15]
	v_mfma_f32_16x16x32_bf16 v[8:11], v[194:197], v[218:221], v[8:11]
	v_mfma_f32_16x16x32_bf16 v[4:7], v[190:193], v[230:233], v[4:7]
	v_mfma_f32_16x16x32_bf16 v[0:3], v[198:201], v[230:233], v[0:3]
	v_mfma_f32_16x16x32_bf16 v[12:15], v[190:193], v[222:225], v[12:15]
	v_mfma_f32_16x16x32_bf16 v[8:11], v[198:201], v[222:225], v[8:11]
	s_barrier
	ds_read_b128 v[132:135], v128
	ds_read_b128 v[162:165], v128 offset:1024
	ds_read_b128 v[178:181], v128 offset:2048
	ds_read_b128 v[182:185], v128 offset:3072
	ds_read_b128 v[186:189], v129
	ds_read_b128 v[190:193], v129 offset:1024
	ds_read_b128 v[194:197], v129 offset:2048
	ds_read_b128 v[198:201], v129 offset:3072
	s_add_i32 s5, s89, 0x8080
	s_add_u32 s50, s37, s5
	s_addc_u32 s51, s38, 0
	s_mov_b32 m0, vcc_lo
	v_lshl_add_u64 v[128:129], s[50:51], 0, v[138:139]
	ds_read_b128 v[202:205], v172
	ds_read_b128 v[206:209], v172 offset:1024
	ds_read_b128 v[210:213], v172 offset:2048
	ds_read_b128 v[214:217], v172 offset:3072
	ds_read_b128 v[218:221], v172 offset:4096
	ds_read_b128 v[222:225], v172 offset:5120
	ds_read_b128 v[226:229], v172 offset:6144
	ds_read_b128 v[230:233], v172 offset:7168
	global_load_lds_dwordx4 v[128:129], off
	v_lshl_add_u64 v[128:129], s[50:51], 0, v[140:141]
	s_mov_b32 m0, s35
	s_nop 0
	global_load_lds_dwordx4 v[128:129], off
	s_waitcnt vmcnt(8)
	s_waitcnt lgkmcnt(0)
	s_barrier
	s_waitcnt lgkmcnt(0)
	v_mfma_f32_16x16x32_bf16 v[124:127], v[132:135], v[202:205], v[124:127]
	v_mfma_f32_16x16x32_bf16 v[120:123], v[178:181], v[202:205], v[120:123]
	v_mfma_f32_16x16x32_bf16 v[116:119], v[132:135], v[210:213], v[116:119]
	v_mfma_f32_16x16x32_bf16 v[112:115], v[178:181], v[210:213], v[112:115]
	v_mfma_f32_16x16x32_bf16 v[108:111], v[132:135], v[218:221], v[108:111]
	v_mfma_f32_16x16x32_bf16 v[104:107], v[178:181], v[218:221], v[104:107]
	v_mfma_f32_16x16x32_bf16 v[124:127], v[162:165], v[206:209], v[124:127]
	v_mfma_f32_16x16x32_bf16 v[120:123], v[182:185], v[206:209], v[120:123]
	v_mfma_f32_16x16x32_bf16 v[116:119], v[162:165], v[214:217], v[116:119]
	v_mfma_f32_16x16x32_bf16 v[112:115], v[182:185], v[214:217], v[112:115]
	v_mfma_f32_16x16x32_bf16 v[108:111], v[162:165], v[222:225], v[108:111]
	v_mfma_f32_16x16x32_bf16 v[104:107], v[182:185], v[222:225], v[104:107]
	v_mfma_f32_16x16x32_bf16 v[100:103], v[132:135], v[226:229], v[100:103]
	v_mfma_f32_16x16x32_bf16 v[96:99], v[178:181], v[226:229], v[96:99]
	v_mfma_f32_16x16x32_bf16 v[234:237], v[162:165], v[230:233], v[100:103]
	v_mfma_f32_16x16x32_bf16 v[238:241], v[182:185], v[230:233], v[96:99]
	v_mfma_f32_16x16x32_bf16 v[92:95], v[186:189], v[202:205], v[92:95]
	v_mfma_f32_16x16x32_bf16 v[88:91], v[194:197], v[202:205], v[88:91]
	v_mfma_f32_16x16x32_bf16 v[76:79], v[186:189], v[218:221], v[76:79]
	v_mfma_f32_16x16x32_bf16 v[72:75], v[194:197], v[218:221], v[72:75]
	v_mfma_f32_16x16x32_bf16 v[68:71], v[186:189], v[226:229], v[68:71]
	v_mfma_f32_16x16x32_bf16 v[64:67], v[194:197], v[226:229], v[64:67]
	v_mfma_f32_16x16x32_bf16 v[92:95], v[190:193], v[206:209], v[92:95]
	v_mfma_f32_16x16x32_bf16 v[88:91], v[198:201], v[206:209], v[88:91]
	v_mfma_f32_16x16x32_bf16 v[84:87], v[186:189], v[210:213], v[84:87]
	v_mfma_f32_16x16x32_bf16 v[80:83], v[194:197], v[210:213], v[80:83]
	v_mfma_f32_16x16x32_bf16 v[76:79], v[190:193], v[222:225], v[76:79]
	v_mfma_f32_16x16x32_bf16 v[72:75], v[198:201], v[222:225], v[72:75]
	v_mfma_f32_16x16x32_bf16 v[68:71], v[190:193], v[230:233], v[68:71]
	v_mfma_f32_16x16x32_bf16 v[64:67], v[198:201], v[230:233], v[64:67]
	v_mfma_f32_16x16x32_bf16 v[202:205], v[190:193], v[214:217], v[84:87]
	v_mfma_f32_16x16x32_bf16 v[206:209], v[198:201], v[214:217], v[80:83]
	s_barrier
; template <class Epi, class Sched, class Hook = NoHook>
; __device__ __forceinline__ void gemm_phase_w(LAS unsigned char* lds, const Sched& S, const Epi& E, int wave_id, const Hook& HK = Hook()) {
;     ...
;             PG_TRIP(nt - 2, true, false, true);
	s_ashr_i32 s5, s85, 31
	s_add_u32 s34, s6, s85
	s_addc_u32 s35, s7, s5
	s_add_i32 s5, s85, 0xffffff00
	s_mov_b32 m0, s27
	v_lshl_add_u64 v[128:129], s[34:35], 0, v[144:145]
	s_ashr_i32 s27, s5, 31
	ds_read_b128 v[80:83], v172 offset:16384
	ds_read_b128 v[84:87], v172 offset:17408
	ds_read_b128 v[96:99], v172 offset:18432
	ds_read_b128 v[100:103], v172 offset:19456
	ds_read_b128 v[210:213], v172 offset:20480
	ds_read_b128 v[214:217], v172 offset:21504
	ds_read_b128 v[218:221], v172 offset:22528
	ds_read_b128 v[222:225], v172 offset:23552
	global_load_lds_dwordx4 v[128:129], off
	v_lshl_add_u64 v[128:129], s[34:35], 0, v[142:143]
	s_add_u32 s34, s6, s5
	s_mov_b32 m0, vcc_hi
	s_addc_u32 s35, s7, s27
	global_load_lds_dwordx4 v[128:129], off
	v_lshl_add_u64 v[128:129], s[34:35], 0, v[144:145]
	s_mov_b32 m0, s59
	s_nop 0
	global_load_lds_dwordx4 v[128:129], off
	v_lshl_add_u64 v[128:129], s[34:35], 0, v[142:143]
	s_add_u32 s34, s3, s4
	s_mov_b32 m0, s60
	s_addc_u32 s35, s36, 0
	global_load_lds_dwordx4 v[128:129], off
	v_lshl_add_u64 v[128:129], s[34:35], 0, v[148:149]
	s_mov_b32 m0, s63
	s_nop 0
	global_load_lds_dwordx4 v[128:129], off
	v_lshl_add_u64 v[128:129], s[34:35], 0, v[146:147]
	s_mov_b32 m0, s66
	s_nop 0
	global_load_lds_dwordx4 v[128:129], off
	s_waitcnt vmcnt(8)
	s_waitcnt lgkmcnt(0)
	s_barrier
	s_waitcnt lgkmcnt(0)
	v_mfma_f32_16x16x32_bf16 v[60:63], v[132:135], v[80:83], v[60:63]
	v_mfma_f32_16x16x32_bf16 v[56:59], v[178:181], v[80:83], v[56:59]
	v_mfma_f32_16x16x32_bf16 v[52:55], v[132:135], v[96:99], v[52:55]
	v_mfma_f32_16x16x32_bf16 v[48:51], v[178:181], v[96:99], v[48:51]
	v_mfma_f32_16x16x32_bf16 v[44:47], v[132:135], v[210:213], v[44:47]
	v_mfma_f32_16x16x32_bf16 v[40:43], v[178:181], v[210:213], v[40:43]
	v_mfma_f32_16x16x32_bf16 v[60:63], v[162:165], v[84:87], v[60:63]
	v_mfma_f32_16x16x32_bf16 v[56:59], v[182:185], v[84:87], v[56:59]
	v_mfma_f32_16x16x32_bf16 v[52:55], v[162:165], v[100:103], v[52:55]
	v_mfma_f32_16x16x32_bf16 v[48:51], v[182:185], v[100:103], v[48:51]
	v_mfma_f32_16x16x32_bf16 v[44:47], v[162:165], v[214:217], v[44:47]
	v_mfma_f32_16x16x32_bf16 v[40:43], v[182:185], v[214:217], v[40:43]
	v_mfma_f32_16x16x32_bf16 v[36:39], v[132:135], v[218:221], v[36:39]
	v_mfma_f32_16x16x32_bf16 v[32:35], v[178:181], v[218:221], v[32:35]
	v_mfma_f32_16x16x32_bf16 v[162:165], v[162:165], v[222:225], v[36:39]
	v_mfma_f32_16x16x32_bf16 v[178:181], v[182:185], v[222:225], v[32:35]
	v_mfma_f32_16x16x32_bf16 v[28:31], v[186:189], v[80:83], v[28:31]
	v_mfma_f32_16x16x32_bf16 v[24:27], v[194:197], v[80:83], v[24:27]
	v_mfma_f32_16x16x32_bf16 v[4:7], v[186:189], v[218:221], v[4:7]
	v_mfma_f32_16x16x32_bf16 v[0:3], v[194:197], v[218:221], v[0:3]
	v_mfma_f32_16x16x32_bf16 v[28:31], v[190:193], v[84:87], v[28:31]
	v_mfma_f32_16x16x32_bf16 v[24:27], v[198:201], v[84:87], v[24:27]
	v_mfma_f32_16x16x32_bf16 v[20:23], v[186:189], v[96:99], v[20:23]
	v_mfma_f32_16x16x32_bf16 v[16:19], v[194:197], v[96:99], v[16:19]
	v_mfma_f32_16x16x32_bf16 v[12:15], v[186:189], v[210:213], v[12:15]
	v_mfma_f32_16x16x32_bf16 v[8:11], v[194:197], v[210:213], v[8:11]
	v_mfma_f32_16x16x32_bf16 v[4:7], v[190:193], v[222:225], v[4:7]
	v_mfma_f32_16x16x32_bf16 v[0:3], v[198:201], v[222:225], v[0:3]
	v_mfma_f32_16x16x32_bf16 v[182:185], v[190:193], v[100:103], v[20:23]
	v_mfma_f32_16x16x32_bf16 v[226:229], v[198:201], v[100:103], v[16:19]
	v_mfma_f32_16x16x32_bf16 v[12:15], v[190:193], v[214:217], v[12:15]
	v_mfma_f32_16x16x32_bf16 v[8:11], v[198:201], v[214:217], v[8:11]
	s_barrier
	ds_read_b128 v[16:19], v130
	ds_read_b128 v[20:23], v130 offset:1024
	ds_read_b128 v[186:189], v130 offset:2048
	ds_read_b128 v[190:193], v130 offset:3072
	ds_read_b128 v[194:197], v131
	ds_read_b128 v[198:201], v131 offset:1024
	ds_read_b128 v[210:213], v131 offset:2048
	ds_read_b128 v[214:217], v131 offset:3072
	s_add_i32 s5, s4, 0x20000
	s_add_u32 s34, s3, s5
	s_addc_u32 s35, s36, 0
	s_mov_b32 m0, s67
	v_lshl_add_u64 v[80:81], s[34:35], 0, v[148:149]
	ds_read_b128 v[32:35], v172 offset:32768
	ds_read_b128 v[36:39], v172 offset:33792
	ds_read_b128 v[218:221], v172 offset:34816
	ds_read_b128 v[222:225], v172 offset:35840
	ds_read_b128 v[230:233], v172 offset:36864
	ds_read_b128 v[242:245], v172 offset:37888
	ds_read_b128 v[246:249], v172 offset:38912
	ds_read_b128 v[250:253], v172 offset:39936
	global_load_lds_dwordx4 v[80:81], off
	v_lshl_add_u64 v[80:81], s[34:35], 0, v[146:147]
	s_mov_b32 m0, s68
	s_nop 0
	global_load_lds_dwordx4 v[80:81], off
	s_waitcnt vmcnt(8)
	s_waitcnt lgkmcnt(0)
	s_barrier
; #define PG_BAR __builtin_amdgcn_s_barrier()
; template <class Epi, class Sched, class Hook = NoHook>
; __device__ __forceinline__ void gemm_phase_w(LAS unsigned char* lds, const Sched& S, const Epi& E, int wave_id, const Hook& HK = Hook()) {
;     ...
;         if constexpr (!SEG2) {
;             for (int tt = 0; tt < nt; tt += 2) {
;                 if constexpr (GATHER) { if (tt == nt - 2) {
;                     if (has_next) { gnxt_00 = S.grow_l(nxt, lds, nbuf, R0) + (unsigned)(C0 * 2); gnxt_01 = S.grow_l(nxt, lds, nbuf, R1) + (unsigned)(C1 * 2); gnxt_10 = S.grow_l(nxt, lds, nbuf, 128 + R0) + (unsigned)(C0 * 2); gnxt_11 = S.grow_l(nxt, lds, nbuf, 128 + R1) + (unsigned)(C1 * 2); }
;                     else { gnxt_00 = gcur_00; gnxt_01 = gcur_01; gnxt_10 = gcur_10; gnxt_11 = gcur_11; } } }
;                 PG_TRIP(tt, false, false, false);
;             }
;         } else {
;             for (int tt = 0; tt < nt - 4; tt += 2) PG_TRIP(tt, false, false, false);
;             PG_TRIP(nt - 4, false, true, false);
;             PG_TRIP(nt - 2, true, false, true);
;         }
;     ...
;         if (wr == 0) PG_BAR;
	s_waitcnt lgkmcnt(0)
	v_mfma_f32_16x16x32_bf16 v[80:83], v[16:19], v[32:35], v[124:127]
	v_mfma_f32_16x16x32_bf16 v[132:135], v[20:23], v[36:39], v[80:83]
	v_mfma_f32_16x16x32_bf16 v[80:83], v[186:189], v[32:35], v[120:123]
	v_mfma_f32_16x16x32_bf16 v[128:131], v[190:193], v[36:39], v[80:83]
	v_mfma_f32_16x16x32_bf16 v[80:83], v[16:19], v[218:221], v[116:119]
	v_mfma_f32_16x16x32_bf16 v[116:119], v[20:23], v[222:225], v[80:83]
	v_mfma_f32_16x16x32_bf16 v[80:83], v[186:189], v[218:221], v[112:115]
	v_mfma_f32_16x16x32_bf16 v[112:115], v[190:193], v[222:225], v[80:83]
	v_mfma_f32_16x16x32_bf16 v[80:83], v[16:19], v[230:233], v[108:111]
	v_mfma_f32_16x16x32_bf16 v[100:103], v[20:23], v[242:245], v[80:83]
	v_mfma_f32_16x16x32_bf16 v[80:83], v[186:189], v[230:233], v[104:107]
	v_mfma_f32_16x16x32_bf16 v[96:99], v[190:193], v[242:245], v[80:83]
	v_mfma_f32_16x16x32_bf16 v[80:83], v[16:19], v[246:249], v[234:237]
	v_mfma_f32_16x16x32_bf16 v[84:87], v[20:23], v[250:253], v[80:83]
	v_mfma_f32_16x16x32_bf16 v[80:83], v[186:189], v[246:249], v[238:241]
	v_mfma_f32_16x16x32_bf16 v[80:83], v[190:193], v[250:253], v[80:83]
	v_mfma_f32_16x16x32_bf16 v[92:95], v[194:197], v[32:35], v[92:95]
	v_mfma_f32_16x16x32_bf16 v[32:35], v[210:213], v[32:35], v[88:91]
	v_mfma_f32_16x16x32_bf16 v[120:123], v[214:217], v[36:39], v[32:35]
	v_mfma_f32_16x16x32_bf16 v[32:35], v[194:197], v[218:221], v[202:205]
	v_mfma_f32_16x16x32_bf16 v[108:111], v[198:201], v[222:225], v[32:35]
	v_mfma_f32_16x16x32_bf16 v[32:35], v[210:213], v[218:221], v[206:209]
	v_mfma_f32_16x16x32_bf16 v[104:107], v[214:217], v[222:225], v[32:35]
	v_mfma_f32_16x16x32_bf16 v[32:35], v[194:197], v[230:233], v[76:79]
	v_mfma_f32_16x16x32_bf16 v[124:127], v[198:201], v[36:39], v[92:95]
	v_mfma_f32_16x16x32_bf16 v[92:95], v[198:201], v[242:245], v[32:35]
	v_mfma_f32_16x16x32_bf16 v[32:35], v[210:213], v[230:233], v[72:75]
	v_mfma_f32_16x16x32_bf16 v[88:91], v[214:217], v[242:245], v[32:35]
	v_mfma_f32_16x16x32_bf16 v[32:35], v[194:197], v[246:249], v[68:71]
	v_mfma_f32_16x16x32_bf16 v[76:79], v[198:201], v[250:253], v[32:35]
	v_mfma_f32_16x16x32_bf16 v[32:35], v[210:213], v[246:249], v[64:67]
	v_mfma_f32_16x16x32_bf16 v[72:75], v[214:217], v[250:253], v[32:35]
	s_barrier
	s_add_i32 s34, s85, 0x80
	s_ashr_i32 s35, s34, 31
	s_add_i32 s5, s85, 0xffffff80
	s_mov_b32 m0, s61
	s_nop 0
	v_lshl_add_u64 v[32:33], v[158:159], 0, s[34:35]
	s_ashr_i32 s27, s5, 31
	ds_read_b128 v[202:205], v172 offset:49152
	ds_read_b128 v[206:209], v172 offset:50176
	ds_read_b128 v[218:221], v172 offset:51200
	ds_read_b128 v[222:225], v172 offset:52224
	ds_read_b128 v[230:233], v172 offset:53248
	ds_read_b128 v[234:237], v172 offset:54272
	ds_read_b128 v[238:241], v172 offset:55296
	ds_read_b128 v[242:245], v172 offset:56320
	global_load_lds_dwordx4 v[32:33], off
	v_lshl_add_u64 v[32:33], v[160:161], 0, s[34:35]
	s_add_u32 s34, s6, s5
	s_mov_b32 m0, s49
	s_addc_u32 s35, s7, s27
	s_add_i32 s5, s4, 0x80
	global_load_lds_dwordx4 v[32:33], off
	v_lshl_add_u64 v[32:33], s[34:35], 0, v[144:145]
	s_mov_b32 m0, s26
	s_add_u32 s26, s3, s5
	global_load_lds_dwordx4 v[32:33], off
	v_lshl_add_u64 v[32:33], s[34:35], 0, v[142:143]
	s_mov_b32 m0, s44
	s_addc_u32 s27, s36, 0
	global_load_lds_dwordx4 v[32:33], off
	v_lshl_add_u64 v[32:33], s[26:27], 0, v[148:149]
	s_mov_b32 m0, s71
	s_nop 0
	global_load_lds_dwordx4 v[32:33], off
	v_lshl_add_u64 v[32:33], s[26:27], 0, v[146:147]
	s_mov_b32 m0, s72
	s_nop 0
	global_load_lds_dwordx4 v[32:33], off
	s_waitcnt vmcnt(8)
	s_waitcnt lgkmcnt(0)
	s_barrier
	s_waitcnt lgkmcnt(0)
	v_mfma_f32_16x16x32_bf16 v[32:35], v[16:19], v[202:205], v[60:63]
	v_mfma_f32_16x16x32_bf16 v[68:71], v[20:23], v[206:209], v[32:35]
	v_mfma_f32_16x16x32_bf16 v[32:35], v[186:189], v[202:205], v[56:59]
	v_mfma_f32_16x16x32_bf16 v[64:67], v[190:193], v[206:209], v[32:35]
	v_mfma_f32_16x16x32_bf16 v[32:35], v[16:19], v[218:221], v[52:55]
	v_mfma_f32_16x16x32_bf16 v[52:55], v[20:23], v[222:225], v[32:35]
	v_mfma_f32_16x16x32_bf16 v[32:35], v[186:189], v[218:221], v[48:51]
	v_mfma_f32_16x16x32_bf16 v[48:51], v[190:193], v[222:225], v[32:35]
	v_mfma_f32_16x16x32_bf16 v[32:35], v[16:19], v[230:233], v[44:47]
	v_mfma_f32_16x16x32_bf16 v[16:19], v[16:19], v[238:241], v[162:165]
	v_mfma_f32_16x16x32_bf16 v[36:39], v[20:23], v[234:237], v[32:35]
	v_mfma_f32_16x16x32_bf16 v[32:35], v[186:189], v[230:233], v[40:43]
	v_mfma_f32_16x16x32_bf16 v[20:23], v[20:23], v[242:245], v[16:19]
	v_mfma_f32_16x16x32_bf16 v[16:19], v[186:189], v[238:241], v[178:181]
	v_mfma_f32_16x16x32_bf16 v[32:35], v[190:193], v[234:237], v[32:35]
	v_mfma_f32_16x16x32_bf16 v[16:19], v[190:193], v[242:245], v[16:19]
	v_mfma_f32_16x16x32_bf16 v[24:27], v[210:213], v[202:205], v[24:27]
	v_mfma_f32_16x16x32_bf16 v[56:59], v[214:217], v[206:209], v[24:27]
	v_mfma_f32_16x16x32_bf16 v[24:27], v[194:197], v[218:221], v[182:185]
	v_mfma_f32_16x16x32_bf16 v[28:31], v[194:197], v[202:205], v[28:31]
	v_mfma_f32_16x16x32_bf16 v[44:47], v[198:201], v[222:225], v[24:27]
	v_mfma_f32_16x16x32_bf16 v[24:27], v[210:213], v[218:221], v[226:229]
	v_mfma_f32_16x16x32_bf16 v[12:15], v[194:197], v[230:233], v[12:15]
	v_mfma_f32_16x16x32_bf16 v[8:11], v[210:213], v[230:233], v[8:11]
	v_mfma_f32_16x16x32_bf16 v[4:7], v[194:197], v[238:241], v[4:7]
	v_mfma_f32_16x16x32_bf16 v[0:3], v[210:213], v[238:241], v[0:3]
	v_mfma_f32_16x16x32_bf16 v[60:63], v[198:201], v[206:209], v[28:31]
	v_mfma_f32_16x16x32_bf16 v[40:43], v[214:217], v[222:225], v[24:27]
	v_mfma_f32_16x16x32_bf16 v[28:31], v[198:201], v[234:237], v[12:15]
	v_mfma_f32_16x16x32_bf16 v[24:27], v[214:217], v[234:237], v[8:11]
	v_mfma_f32_16x16x32_bf16 v[4:7], v[198:201], v[242:245], v[4:7]
	v_mfma_f32_16x16x32_bf16 v[0:3], v[214:217], v[242:245], v[0:3]
	s_barrier
	s_and_b64 vcc, exec, s[64:65]
	s_cbranch_vccz .LBB0_1779
	s_barrier

.LBB0_1854:
	ds_read_b128 v[100:103], v197
	ds_read_b128 v[132:135], v197 offset:1024
	ds_read_b128 v[136:139], v197 offset:2048
	ds_read_b128 v[140:143], v197 offset:3072
	ds_read_b128 v[144:147], v198
	ds_read_b128 v[148:151], v198 offset:1024
	ds_read_b128 v[152:155], v198 offset:2048
	ds_read_b128 v[156:159], v198 offset:3072
	s_add_i32 s53, s21, 2
	s_cmp_eq_u32 s20, 0x9f000
	s_cselect_b32 s59, s48, s51
	s_cselect_b32 s60, 0, s53
	s_cselect_b32 s58, s49, s52
	s_add_i32 s61, s52, s20
	s_add_u32 s62, s3, s61
	s_addc_u32 s63, s30, 0
	v_lshl_add_u64 v[190:191], s[62:63], 0, v[164:165]
	s_add_i32 m0, s23, 0xc000
	ds_read_b128 v[160:163], v199
	ds_read_b128 v[174:177], v199 offset:1024
	ds_read_b128 v[178:181], v199 offset:2048
	ds_read_b128 v[182:185], v199 offset:3072
	ds_read_b128 v[186:189], v199 offset:4096
	ds_read_b128 v[200:203], v199 offset:5120
	ds_read_b128 v[204:207], v199 offset:6144
	ds_read_b128 v[208:211], v199 offset:7168
	global_load_lds_dwordx4 v[190:191], off
	v_lshl_add_u64 v[190:191], s[62:63], 0, v[166:167]
	s_add_i32 m0, s23, 0xe000
	s_nop 0
	global_load_lds_dwordx4 v[190:191], off
	s_waitcnt vmcnt(8)
	s_waitcnt lgkmcnt(0)
	s_barrier
	s_waitcnt lgkmcnt(0)
	v_mfma_f32_16x16x32_bf16 v[128:131], v[100:103], v[160:163], v[128:131]
	v_mfma_f32_16x16x32_bf16 v[124:127], v[136:139], v[160:163], v[124:127]
	v_mfma_f32_16x16x32_bf16 v[116:119], v[100:103], v[178:181], v[116:119]
	v_mfma_f32_16x16x32_bf16 v[108:111], v[136:139], v[178:181], v[108:111]
	v_mfma_f32_16x16x32_bf16 v[92:95], v[100:103], v[186:189], v[92:95]
	v_mfma_f32_16x16x32_bf16 v[84:87], v[136:139], v[186:189], v[84:87]
	v_mfma_f32_16x16x32_bf16 v[76:79], v[100:103], v[204:207], v[76:79]
	v_mfma_f32_16x16x32_bf16 v[68:71], v[136:139], v[204:207], v[68:71]
	v_mfma_f32_16x16x32_bf16 v[128:131], v[132:135], v[174:177], v[128:131]
	v_mfma_f32_16x16x32_bf16 v[124:127], v[140:143], v[174:177], v[124:127]
	v_mfma_f32_16x16x32_bf16 v[116:119], v[132:135], v[182:185], v[116:119]
	v_mfma_f32_16x16x32_bf16 v[108:111], v[140:143], v[182:185], v[108:111]
	v_mfma_f32_16x16x32_bf16 v[92:95], v[132:135], v[200:203], v[92:95]
	v_mfma_f32_16x16x32_bf16 v[84:87], v[140:143], v[200:203], v[84:87]
	v_mfma_f32_16x16x32_bf16 v[76:79], v[132:135], v[208:211], v[76:79]
	v_mfma_f32_16x16x32_bf16 v[68:71], v[140:143], v[208:211], v[68:71]
	v_mfma_f32_16x16x32_bf16 v[96:99], v[144:147], v[160:163], v[96:99]
	v_mfma_f32_16x16x32_bf16 v[120:123], v[152:155], v[160:163], v[120:123]
	v_mfma_f32_16x16x32_bf16 v[112:115], v[144:147], v[178:181], v[112:115]
	v_mfma_f32_16x16x32_bf16 v[104:107], v[152:155], v[178:181], v[104:107]
	v_mfma_f32_16x16x32_bf16 v[88:91], v[144:147], v[186:189], v[88:91]
	v_mfma_f32_16x16x32_bf16 v[80:83], v[152:155], v[186:189], v[80:83]
	v_mfma_f32_16x16x32_bf16 v[72:75], v[144:147], v[204:207], v[72:75]
	v_mfma_f32_16x16x32_bf16 v[64:67], v[152:155], v[204:207], v[64:67]
	v_mfma_f32_16x16x32_bf16 v[96:99], v[148:151], v[174:177], v[96:99]
	v_mfma_f32_16x16x32_bf16 v[120:123], v[156:159], v[174:177], v[120:123]
	v_mfma_f32_16x16x32_bf16 v[112:115], v[148:151], v[182:185], v[112:115]
	v_mfma_f32_16x16x32_bf16 v[104:107], v[156:159], v[182:185], v[104:107]
	v_mfma_f32_16x16x32_bf16 v[88:91], v[148:151], v[200:203], v[88:91]
	v_mfma_f32_16x16x32_bf16 v[80:83], v[156:159], v[200:203], v[80:83]
	v_mfma_f32_16x16x32_bf16 v[72:75], v[148:151], v[208:211], v[72:75]
	v_mfma_f32_16x16x32_bf16 v[64:67], v[156:159], v[208:211], v[64:67]
	s_barrier
	s_lshl_b32 s61, s60, 7
	s_add_i32 s62, s61, s59
	s_ashr_i32 s63, s62, 31
	s_add_u32 s62, s4, s62
	s_addc_u32 s63, s5, s63
	s_add_i32 s66, s42, s31
	v_lshl_add_u64 v[190:191], s[62:63], 0, v[168:169]
	s_mov_b32 m0, s66
	ds_read_b128 v[160:163], v199 offset:16384
	ds_read_b128 v[174:177], v199 offset:17408
	ds_read_b128 v[178:181], v199 offset:18432
	ds_read_b128 v[182:185], v199 offset:19456
	ds_read_b128 v[186:189], v199 offset:20480
	ds_read_b128 v[200:203], v199 offset:21504
	ds_read_b128 v[204:207], v199 offset:22528
	ds_read_b128 v[208:211], v199 offset:23552
	global_load_lds_dwordx4 v[190:191], off
	s_add_i32 m0, s66, 0x2000
	s_add_i32 s66, s59, 0x80000
	s_add_i32 s61, s66, s61
	v_lshl_add_u64 v[190:191], s[62:63], 0, v[170:171]
	s_ashr_i32 s63, s61, 31
	s_add_u32 s62, s4, s61
	s_addc_u32 s63, s5, s63
	s_add_i32 s61, s43, s31
	global_load_lds_dwordx4 v[190:191], off
	v_lshl_add_u64 v[190:191], s[62:63], 0, v[168:169]
	s_mov_b32 m0, s61
	s_nop 0
	global_load_lds_dwordx4 v[190:191], off
	s_add_i32 m0, s61, 0x2000
	s_lshl_b32 s61, s60, 12
	s_add_i32 s61, s61, s58
	v_lshl_add_u64 v[190:191], s[62:63], 0, v[170:171]
	s_add_u32 s62, s3, s61
	s_addc_u32 s63, s30, 0
	global_load_lds_dwordx4 v[190:191], off
	v_lshl_add_u64 v[190:191], s[62:63], 0, v[164:165]
	s_mov_b32 m0, s23
	s_nop 0
	global_load_lds_dwordx4 v[190:191], off
	v_lshl_add_u64 v[190:191], s[62:63], 0, v[166:167]
	s_mov_b32 m0, s24
	s_nop 0
	global_load_lds_dwordx4 v[190:191], off
	s_waitcnt vmcnt(8)
	s_waitcnt lgkmcnt(0)
	s_barrier
	s_waitcnt lgkmcnt(0)
	v_mfma_f32_16x16x32_bf16 v[60:63], v[100:103], v[160:163], v[60:63]
	v_mfma_f32_16x16x32_bf16 v[52:55], v[136:139], v[160:163], v[52:55]
	v_mfma_f32_16x16x32_bf16 v[44:47], v[100:103], v[178:181], v[44:47]
	v_mfma_f32_16x16x32_bf16 v[36:39], v[136:139], v[178:181], v[36:39]
	v_mfma_f32_16x16x32_bf16 v[28:31], v[100:103], v[186:189], v[28:31]
	v_mfma_f32_16x16x32_bf16 v[20:23], v[136:139], v[186:189], v[20:23]
	v_mfma_f32_16x16x32_bf16 v[12:15], v[100:103], v[204:207], v[12:15]
	v_mfma_f32_16x16x32_bf16 v[4:7], v[136:139], v[204:207], v[4:7]
	v_mfma_f32_16x16x32_bf16 v[60:63], v[132:135], v[174:177], v[60:63]
	v_mfma_f32_16x16x32_bf16 v[52:55], v[140:143], v[174:177], v[52:55]
	v_mfma_f32_16x16x32_bf16 v[44:47], v[132:135], v[182:185], v[44:47]
	v_mfma_f32_16x16x32_bf16 v[36:39], v[140:143], v[182:185], v[36:39]
	v_mfma_f32_16x16x32_bf16 v[28:31], v[132:135], v[200:203], v[28:31]
	v_mfma_f32_16x16x32_bf16 v[20:23], v[140:143], v[200:203], v[20:23]
	v_mfma_f32_16x16x32_bf16 v[12:15], v[132:135], v[208:211], v[12:15]
	v_mfma_f32_16x16x32_bf16 v[4:7], v[140:143], v[208:211], v[4:7]
	v_mfma_f32_16x16x32_bf16 v[56:59], v[144:147], v[160:163], v[56:59]
	v_mfma_f32_16x16x32_bf16 v[48:51], v[152:155], v[160:163], v[48:51]
	v_mfma_f32_16x16x32_bf16 v[40:43], v[144:147], v[178:181], v[40:43]
	v_mfma_f32_16x16x32_bf16 v[32:35], v[152:155], v[178:181], v[32:35]
	v_mfma_f32_16x16x32_bf16 v[24:27], v[144:147], v[186:189], v[24:27]
	v_mfma_f32_16x16x32_bf16 v[16:19], v[152:155], v[186:189], v[16:19]
	v_mfma_f32_16x16x32_bf16 v[8:11], v[144:147], v[204:207], v[8:11]
	v_mfma_f32_16x16x32_bf16 v[0:3], v[152:155], v[204:207], v[0:3]
	v_mfma_f32_16x16x32_bf16 v[56:59], v[148:151], v[174:177], v[56:59]
	v_mfma_f32_16x16x32_bf16 v[48:51], v[156:159], v[174:177], v[48:51]
	v_mfma_f32_16x16x32_bf16 v[40:43], v[148:151], v[182:185], v[40:43]
	v_mfma_f32_16x16x32_bf16 v[32:35], v[156:159], v[182:185], v[32:35]
	v_mfma_f32_16x16x32_bf16 v[24:27], v[148:151], v[200:203], v[24:27]
	v_mfma_f32_16x16x32_bf16 v[16:19], v[156:159], v[200:203], v[16:19]
	v_mfma_f32_16x16x32_bf16 v[8:11], v[148:151], v[208:211], v[8:11]
	v_mfma_f32_16x16x32_bf16 v[0:3], v[156:159], v[208:211], v[0:3]
	s_barrier
	s_add_i32 s67, 0, 0x18000
	s_add_i32 s68, 0, 0x1c000
	v_add_u32_e32 v140, s67, v195
	v_add_u32_e32 v156, s68, v195
	ds_read_b128 v[100:103], v140
	ds_read_b128 v[132:135], v140 offset:1024
	ds_read_b128 v[136:139], v140 offset:2048
	ds_read_b128 v[140:143], v140 offset:3072
	ds_read_b128 v[144:147], v156
	ds_read_b128 v[148:151], v156 offset:1024
	ds_read_b128 v[152:155], v156 offset:2048
	ds_read_b128 v[156:159], v156 offset:3072
	s_add_i32 s61, s61, 0x80000
	s_add_u32 s62, s3, s61
	s_addc_u32 s63, s30, 0
	s_mov_b32 m0, s25
	v_lshl_add_u64 v[190:191], s[62:63], 0, v[164:165]
	ds_read_b128 v[160:163], v199 offset:32768
	ds_read_b128 v[174:177], v199 offset:33792
	ds_read_b128 v[178:181], v199 offset:34816
	ds_read_b128 v[182:185], v199 offset:35840
	ds_read_b128 v[186:189], v199 offset:36864
	ds_read_b128 v[200:203], v199 offset:37888
	ds_read_b128 v[204:207], v199 offset:38912
	ds_read_b128 v[208:211], v199 offset:39936
	global_load_lds_dwordx4 v[190:191], off
	v_lshl_add_u64 v[190:191], s[62:63], 0, v[166:167]
	s_mov_b32 m0, s26
	s_nop 0
	global_load_lds_dwordx4 v[190:191], off
	s_waitcnt vmcnt(8)
	s_waitcnt lgkmcnt(0)
	s_barrier
	s_waitcnt lgkmcnt(0)
	v_mfma_f32_16x16x32_bf16 v[128:131], v[100:103], v[160:163], v[128:131]
	v_mfma_f32_16x16x32_bf16 v[124:127], v[136:139], v[160:163], v[124:127]
	v_mfma_f32_16x16x32_bf16 v[116:119], v[100:103], v[178:181], v[116:119]
	v_mfma_f32_16x16x32_bf16 v[108:111], v[136:139], v[178:181], v[108:111]
	v_mfma_f32_16x16x32_bf16 v[92:95], v[100:103], v[186:189], v[92:95]
	v_mfma_f32_16x16x32_bf16 v[84:87], v[136:139], v[186:189], v[84:87]
	v_mfma_f32_16x16x32_bf16 v[76:79], v[100:103], v[204:207], v[76:79]
	v_mfma_f32_16x16x32_bf16 v[68:71], v[136:139], v[204:207], v[68:71]
	v_mfma_f32_16x16x32_bf16 v[128:131], v[132:135], v[174:177], v[128:131]
	v_mfma_f32_16x16x32_bf16 v[124:127], v[140:143], v[174:177], v[124:127]
	v_mfma_f32_16x16x32_bf16 v[116:119], v[132:135], v[182:185], v[116:119]
	v_mfma_f32_16x16x32_bf16 v[108:111], v[140:143], v[182:185], v[108:111]
	v_mfma_f32_16x16x32_bf16 v[92:95], v[132:135], v[200:203], v[92:95]
	v_mfma_f32_16x16x32_bf16 v[84:87], v[140:143], v[200:203], v[84:87]
	v_mfma_f32_16x16x32_bf16 v[76:79], v[132:135], v[208:211], v[76:79]
	v_mfma_f32_16x16x32_bf16 v[68:71], v[140:143], v[208:211], v[68:71]
	v_mfma_f32_16x16x32_bf16 v[96:99], v[144:147], v[160:163], v[96:99]
	v_mfma_f32_16x16x32_bf16 v[120:123], v[152:155], v[160:163], v[120:123]
	v_mfma_f32_16x16x32_bf16 v[112:115], v[144:147], v[178:181], v[112:115]
	v_mfma_f32_16x16x32_bf16 v[104:107], v[152:155], v[178:181], v[104:107]
	v_mfma_f32_16x16x32_bf16 v[88:91], v[144:147], v[186:189], v[88:91]
	v_mfma_f32_16x16x32_bf16 v[80:83], v[152:155], v[186:189], v[80:83]
	v_mfma_f32_16x16x32_bf16 v[72:75], v[144:147], v[204:207], v[72:75]
	v_mfma_f32_16x16x32_bf16 v[64:67], v[152:155], v[204:207], v[64:67]
	v_mfma_f32_16x16x32_bf16 v[96:99], v[148:151], v[174:177], v[96:99]
	v_mfma_f32_16x16x32_bf16 v[120:123], v[156:159], v[174:177], v[120:123]
	v_mfma_f32_16x16x32_bf16 v[112:115], v[148:151], v[182:185], v[112:115]
	v_mfma_f32_16x16x32_bf16 v[104:107], v[156:159], v[182:185], v[104:107]
	v_mfma_f32_16x16x32_bf16 v[88:91], v[148:151], v[200:203], v[88:91]
	v_mfma_f32_16x16x32_bf16 v[80:83], v[156:159], v[200:203], v[80:83]
	v_mfma_f32_16x16x32_bf16 v[72:75], v[148:151], v[208:211], v[72:75]
	v_mfma_f32_16x16x32_bf16 v[64:67], v[156:159], v[208:211], v[64:67]
	s_barrier
; #define PG_BAR __builtin_amdgcn_s_barrier()
; template <class Epi, class Sched, class Hook = NoHook>
; __device__ __forceinline__ void gemm_phase_w(LAS unsigned char* lds, const Sched& S, const Epi& E, int wave_id, const Hook& HK = Hook()) {
;     ...
;         if constexpr (!SEG2) {
;             for (int tt = 0; tt < nt; tt += 2) {
;                 if constexpr (GATHER) { if (tt == nt - 2) {
;                     if (has_next) { gnxt_00 = S.grow_l(nxt, lds, nbuf, R0) + (unsigned)(C0 * 2); gnxt_01 = S.grow_l(nxt, lds, nbuf, R1) + (unsigned)(C1 * 2); gnxt_10 = S.grow_l(nxt, lds, nbuf, 128 + R0) + (unsigned)(C0 * 2); gnxt_11 = S.grow_l(nxt, lds, nbuf, 128 + R1) + (unsigned)(C1 * 2); }
;                     else { gnxt_00 = gcur_00; gnxt_01 = gcur_01; gnxt_10 = gcur_10; gnxt_11 = gcur_11; } } }
;                 PG_TRIP(tt, false, false, false);
;             }
;         } else {
;             for (int tt = 0; tt < nt - 4; tt += 2) PG_TRIP(tt, false, false, false);
;             PG_TRIP(nt - 4, false, true, false);
;             PG_TRIP(nt - 2, true, false, true);
;         }
;     ...
;         if (wr == 0) PG_BAR;
	s_or_b32 s62, s60, 1
	s_lshl_b32 s63, s62, 7
	s_add_i32 s59, s63, s59
	s_ashr_i32 s61, s59, 31
	s_add_u32 s60, s4, s59
	s_addc_u32 s61, s5, s61
	s_add_i32 s59, s67, s31
	v_lshl_add_u64 v[190:191], s[60:61], 0, v[168:169]
	s_mov_b32 m0, s59
	s_add_i32 s63, s63, s66
	ds_read_b128 v[160:163], v199 offset:49152
	ds_read_b128 v[174:177], v199 offset:50176
	ds_read_b128 v[178:181], v199 offset:51200
	ds_read_b128 v[182:185], v199 offset:52224
	ds_read_b128 v[186:189], v199 offset:53248
	ds_read_b128 v[200:203], v199 offset:54272
	ds_read_b128 v[204:207], v199 offset:55296
	ds_read_b128 v[208:211], v199 offset:56320
	global_load_lds_dwordx4 v[190:191], off
	s_add_i32 m0, s59, 0x2000
	s_ashr_i32 s59, s63, 31
	v_lshl_add_u64 v[190:191], s[60:61], 0, v[170:171]
	s_add_u32 s60, s4, s63
	s_addc_u32 s61, s5, s59
	s_add_i32 s59, s68, s31
	global_load_lds_dwordx4 v[190:191], off
	v_lshl_add_u64 v[190:191], s[60:61], 0, v[168:169]
	s_mov_b32 m0, s59
	s_nop 0
	global_load_lds_dwordx4 v[190:191], off
	s_add_i32 m0, s59, 0x2000
	s_lshl_b32 s59, s62, 12
	s_add_i32 s59, s59, s58
	s_add_u32 s58, s3, s59
	v_lshl_add_u64 v[190:191], s[60:61], 0, v[170:171]
	s_addc_u32 s59, s30, 0
	global_load_lds_dwordx4 v[190:191], off
	v_lshl_add_u64 v[190:191], s[58:59], 0, v[164:165]
	s_mov_b32 m0, s28
	s_nop 0
	global_load_lds_dwordx4 v[190:191], off
	v_lshl_add_u64 v[190:191], s[58:59], 0, v[166:167]
	s_mov_b32 m0, s29
	s_nop 0
	global_load_lds_dwordx4 v[190:191], off
	s_waitcnt vmcnt(8)
	s_waitcnt lgkmcnt(0)
	s_barrier
	s_waitcnt lgkmcnt(0)
	v_mfma_f32_16x16x32_bf16 v[60:63], v[100:103], v[160:163], v[60:63]
	v_mfma_f32_16x16x32_bf16 v[52:55], v[136:139], v[160:163], v[52:55]
	v_mfma_f32_16x16x32_bf16 v[44:47], v[100:103], v[178:181], v[44:47]
	v_mfma_f32_16x16x32_bf16 v[36:39], v[136:139], v[178:181], v[36:39]
	v_mfma_f32_16x16x32_bf16 v[28:31], v[100:103], v[186:189], v[28:31]
	v_mfma_f32_16x16x32_bf16 v[20:23], v[136:139], v[186:189], v[20:23]
	v_mfma_f32_16x16x32_bf16 v[12:15], v[100:103], v[204:207], v[12:15]
	v_mfma_f32_16x16x32_bf16 v[4:7], v[136:139], v[204:207], v[4:7]
	v_mfma_f32_16x16x32_bf16 v[60:63], v[132:135], v[174:177], v[60:63]
	v_mfma_f32_16x16x32_bf16 v[52:55], v[140:143], v[174:177], v[52:55]
	v_mfma_f32_16x16x32_bf16 v[44:47], v[132:135], v[182:185], v[44:47]
	v_mfma_f32_16x16x32_bf16 v[36:39], v[140:143], v[182:185], v[36:39]
	v_mfma_f32_16x16x32_bf16 v[28:31], v[132:135], v[200:203], v[28:31]
	v_mfma_f32_16x16x32_bf16 v[20:23], v[140:143], v[200:203], v[20:23]
	v_mfma_f32_16x16x32_bf16 v[12:15], v[132:135], v[208:211], v[12:15]
	v_mfma_f32_16x16x32_bf16 v[4:7], v[140:143], v[208:211], v[4:7]
	v_mfma_f32_16x16x32_bf16 v[56:59], v[144:147], v[160:163], v[56:59]
	v_mfma_f32_16x16x32_bf16 v[48:51], v[152:155], v[160:163], v[48:51]
	v_mfma_f32_16x16x32_bf16 v[40:43], v[144:147], v[178:181], v[40:43]
	v_mfma_f32_16x16x32_bf16 v[32:35], v[152:155], v[178:181], v[32:35]
	v_mfma_f32_16x16x32_bf16 v[24:27], v[144:147], v[186:189], v[24:27]
	v_mfma_f32_16x16x32_bf16 v[16:19], v[152:155], v[186:189], v[16:19]
	v_mfma_f32_16x16x32_bf16 v[8:11], v[144:147], v[204:207], v[8:11]
	v_mfma_f32_16x16x32_bf16 v[0:3], v[152:155], v[204:207], v[0:3]
	v_mfma_f32_16x16x32_bf16 v[56:59], v[148:151], v[174:177], v[56:59]
	v_mfma_f32_16x16x32_bf16 v[48:51], v[156:159], v[174:177], v[48:51]
	v_mfma_f32_16x16x32_bf16 v[40:43], v[148:151], v[182:185], v[40:43]
	v_mfma_f32_16x16x32_bf16 v[32:35], v[156:159], v[182:185], v[32:35]
	v_mfma_f32_16x16x32_bf16 v[24:27], v[148:151], v[200:203], v[24:27]
	v_mfma_f32_16x16x32_bf16 v[16:19], v[156:159], v[200:203], v[16:19]
	v_mfma_f32_16x16x32_bf16 v[8:11], v[148:151], v[208:211], v[8:11]
	v_mfma_f32_16x16x32_bf16 v[0:3], v[156:159], v[208:211], v[0:3]
	s_barrier
	s_addk_i32 s20, 0x2000
	s_cmp_gt_u32 s21, 29
	s_mov_b32 s21, s53
	s_cbranch_scc0 .LBB0_1854
	s_and_b64 vcc, exec, s[16:17]
	s_cbranch_vccz .LBB0_1857
	s_barrier

.LBB0_1983:
	ds_read_b128 v[100:103], v195
	ds_read_b128 v[132:135], v195 offset:1024
	ds_read_b128 v[136:139], v195 offset:2048
	ds_read_b128 v[140:143], v195 offset:3072
	ds_read_b128 v[144:147], v196
	ds_read_b128 v[148:151], v196 offset:1024
	ds_read_b128 v[152:155], v196 offset:2048
	ds_read_b128 v[156:159], v196 offset:3072
	s_add_i32 s45, s21, 2
	s_cmp_eq_u32 s20, 0x9f000
	s_cselect_b32 s49, s40, s43
	s_cselect_b32 s50, 0, s45
	s_cselect_b32 s48, s41, s44
	s_add_i32 s51, s44, s20
	s_add_u32 s52, s3, s51
	s_addc_u32 s53, s30, 0
	v_lshl_add_u64 v[190:191], s[52:53], 0, v[164:165]
	s_add_i32 m0, s24, 0xc000
	ds_read_b128 v[160:163], v197
	ds_read_b128 v[174:177], v197 offset:1024
	ds_read_b128 v[178:181], v197 offset:2048
	ds_read_b128 v[182:185], v197 offset:3072
	ds_read_b128 v[186:189], v197 offset:4096
	ds_read_b128 v[198:201], v197 offset:5120
	ds_read_b128 v[202:205], v197 offset:6144
	ds_read_b128 v[206:209], v197 offset:7168
	global_load_lds_dwordx4 v[190:191], off
	v_lshl_add_u64 v[190:191], s[52:53], 0, v[166:167]
	s_add_i32 m0, s24, 0xe000
	s_nop 0
	global_load_lds_dwordx4 v[190:191], off
	s_waitcnt vmcnt(8)
	s_waitcnt lgkmcnt(0)
	s_barrier
	s_waitcnt lgkmcnt(0)
	v_mfma_f32_16x16x32_bf16 v[128:131], v[100:103], v[160:163], v[128:131]
	v_mfma_f32_16x16x32_bf16 v[124:127], v[136:139], v[160:163], v[124:127]
	v_mfma_f32_16x16x32_bf16 v[116:119], v[100:103], v[178:181], v[116:119]
	v_mfma_f32_16x16x32_bf16 v[108:111], v[136:139], v[178:181], v[108:111]
	v_mfma_f32_16x16x32_bf16 v[92:95], v[100:103], v[186:189], v[92:95]
	v_mfma_f32_16x16x32_bf16 v[84:87], v[136:139], v[186:189], v[84:87]
	v_mfma_f32_16x16x32_bf16 v[76:79], v[100:103], v[202:205], v[76:79]
	v_mfma_f32_16x16x32_bf16 v[68:71], v[136:139], v[202:205], v[68:71]
	v_mfma_f32_16x16x32_bf16 v[128:131], v[132:135], v[174:177], v[128:131]
	v_mfma_f32_16x16x32_bf16 v[124:127], v[140:143], v[174:177], v[124:127]
	v_mfma_f32_16x16x32_bf16 v[116:119], v[132:135], v[182:185], v[116:119]
	v_mfma_f32_16x16x32_bf16 v[108:111], v[140:143], v[182:185], v[108:111]
	v_mfma_f32_16x16x32_bf16 v[92:95], v[132:135], v[198:201], v[92:95]
	v_mfma_f32_16x16x32_bf16 v[84:87], v[140:143], v[198:201], v[84:87]
	v_mfma_f32_16x16x32_bf16 v[76:79], v[132:135], v[206:209], v[76:79]
	v_mfma_f32_16x16x32_bf16 v[68:71], v[140:143], v[206:209], v[68:71]
	v_mfma_f32_16x16x32_bf16 v[96:99], v[144:147], v[160:163], v[96:99]
	v_mfma_f32_16x16x32_bf16 v[120:123], v[152:155], v[160:163], v[120:123]
	v_mfma_f32_16x16x32_bf16 v[112:115], v[144:147], v[178:181], v[112:115]
	v_mfma_f32_16x16x32_bf16 v[104:107], v[152:155], v[178:181], v[104:107]
	v_mfma_f32_16x16x32_bf16 v[88:91], v[144:147], v[186:189], v[88:91]
	v_mfma_f32_16x16x32_bf16 v[80:83], v[152:155], v[186:189], v[80:83]
	v_mfma_f32_16x16x32_bf16 v[72:75], v[144:147], v[202:205], v[72:75]
	v_mfma_f32_16x16x32_bf16 v[64:67], v[152:155], v[202:205], v[64:67]
	v_mfma_f32_16x16x32_bf16 v[96:99], v[148:151], v[174:177], v[96:99]
	v_mfma_f32_16x16x32_bf16 v[120:123], v[156:159], v[174:177], v[120:123]
	v_mfma_f32_16x16x32_bf16 v[112:115], v[148:151], v[182:185], v[112:115]
	v_mfma_f32_16x16x32_bf16 v[104:107], v[156:159], v[182:185], v[104:107]
	v_mfma_f32_16x16x32_bf16 v[88:91], v[148:151], v[198:201], v[88:91]
	v_mfma_f32_16x16x32_bf16 v[80:83], v[156:159], v[198:201], v[80:83]
	v_mfma_f32_16x16x32_bf16 v[72:75], v[148:151], v[206:209], v[72:75]
	v_mfma_f32_16x16x32_bf16 v[64:67], v[156:159], v[206:209], v[64:67]
	s_barrier
	s_lshl_b32 s51, s50, 7
	s_add_i32 s52, s51, s49
	s_ashr_i32 s53, s52, 31
	s_add_u32 s52, s4, s52
	s_addc_u32 s53, s5, s53
	s_add_i32 s58, s34, s31
	v_lshl_add_u64 v[190:191], s[52:53], 0, v[168:169]
	s_mov_b32 m0, s58
	ds_read_b128 v[160:163], v197 offset:16384
	ds_read_b128 v[174:177], v197 offset:17408
	ds_read_b128 v[178:181], v197 offset:18432
	ds_read_b128 v[182:185], v197 offset:19456
	ds_read_b128 v[186:189], v197 offset:20480
	ds_read_b128 v[198:201], v197 offset:21504
	ds_read_b128 v[202:205], v197 offset:22528
	ds_read_b128 v[206:209], v197 offset:23552
	global_load_lds_dwordx4 v[190:191], off
	s_add_i32 m0, s58, 0x2000
	s_add_i32 s58, s49, 0x80000
	s_add_i32 s51, s58, s51
	v_lshl_add_u64 v[190:191], s[52:53], 0, v[170:171]
	s_ashr_i32 s53, s51, 31
	s_add_u32 s52, s4, s51
	s_addc_u32 s53, s5, s53
	s_add_i32 s51, s36, s31
	global_load_lds_dwordx4 v[190:191], off
	v_lshl_add_u64 v[190:191], s[52:53], 0, v[168:169]
	s_mov_b32 m0, s51
	s_nop 0
	global_load_lds_dwordx4 v[190:191], off
	s_add_i32 m0, s51, 0x2000
	s_lshl_b32 s51, s50, 12
	s_add_i32 s51, s51, s48
	v_lshl_add_u64 v[190:191], s[52:53], 0, v[170:171]
	s_add_u32 s52, s3, s51
	s_addc_u32 s53, s30, 0
	global_load_lds_dwordx4 v[190:191], off
	v_lshl_add_u64 v[190:191], s[52:53], 0, v[164:165]
	s_mov_b32 m0, s24
	s_nop 0
	global_load_lds_dwordx4 v[190:191], off
	v_lshl_add_u64 v[190:191], s[52:53], 0, v[166:167]
	s_mov_b32 m0, s25
	s_nop 0
	global_load_lds_dwordx4 v[190:191], off
	s_waitcnt vmcnt(8)
	s_waitcnt lgkmcnt(0)
	s_barrier
	s_waitcnt lgkmcnt(0)
	v_mfma_f32_16x16x32_bf16 v[60:63], v[100:103], v[160:163], v[60:63]
	v_mfma_f32_16x16x32_bf16 v[52:55], v[136:139], v[160:163], v[52:55]
	v_mfma_f32_16x16x32_bf16 v[44:47], v[100:103], v[178:181], v[44:47]
	v_mfma_f32_16x16x32_bf16 v[36:39], v[136:139], v[178:181], v[36:39]
	v_mfma_f32_16x16x32_bf16 v[28:31], v[100:103], v[186:189], v[28:31]
	v_mfma_f32_16x16x32_bf16 v[20:23], v[136:139], v[186:189], v[20:23]
	v_mfma_f32_16x16x32_bf16 v[12:15], v[100:103], v[202:205], v[12:15]
	v_mfma_f32_16x16x32_bf16 v[4:7], v[136:139], v[202:205], v[4:7]
	v_mfma_f32_16x16x32_bf16 v[60:63], v[132:135], v[174:177], v[60:63]
	v_mfma_f32_16x16x32_bf16 v[52:55], v[140:143], v[174:177], v[52:55]
	v_mfma_f32_16x16x32_bf16 v[44:47], v[132:135], v[182:185], v[44:47]
	v_mfma_f32_16x16x32_bf16 v[36:39], v[140:143], v[182:185], v[36:39]
	v_mfma_f32_16x16x32_bf16 v[28:31], v[132:135], v[198:201], v[28:31]
	v_mfma_f32_16x16x32_bf16 v[20:23], v[140:143], v[198:201], v[20:23]
	v_mfma_f32_16x16x32_bf16 v[12:15], v[132:135], v[206:209], v[12:15]
	v_mfma_f32_16x16x32_bf16 v[4:7], v[140:143], v[206:209], v[4:7]
	v_mfma_f32_16x16x32_bf16 v[56:59], v[144:147], v[160:163], v[56:59]
	v_mfma_f32_16x16x32_bf16 v[48:51], v[152:155], v[160:163], v[48:51]
	v_mfma_f32_16x16x32_bf16 v[40:43], v[144:147], v[178:181], v[40:43]
	v_mfma_f32_16x16x32_bf16 v[32:35], v[152:155], v[178:181], v[32:35]
	v_mfma_f32_16x16x32_bf16 v[24:27], v[144:147], v[186:189], v[24:27]
	v_mfma_f32_16x16x32_bf16 v[16:19], v[152:155], v[186:189], v[16:19]
	v_mfma_f32_16x16x32_bf16 v[8:11], v[144:147], v[202:205], v[8:11]
	v_mfma_f32_16x16x32_bf16 v[0:3], v[152:155], v[202:205], v[0:3]
	v_mfma_f32_16x16x32_bf16 v[56:59], v[148:151], v[174:177], v[56:59]
	v_mfma_f32_16x16x32_bf16 v[48:51], v[156:159], v[174:177], v[48:51]
	v_mfma_f32_16x16x32_bf16 v[40:43], v[148:151], v[182:185], v[40:43]
	v_mfma_f32_16x16x32_bf16 v[32:35], v[156:159], v[182:185], v[32:35]
	v_mfma_f32_16x16x32_bf16 v[24:27], v[148:151], v[198:201], v[24:27]
	v_mfma_f32_16x16x32_bf16 v[16:19], v[156:159], v[198:201], v[16:19]
	v_mfma_f32_16x16x32_bf16 v[8:11], v[148:151], v[206:209], v[8:11]
	v_mfma_f32_16x16x32_bf16 v[0:3], v[156:159], v[206:209], v[0:3]
	s_barrier
	s_add_i32 s59, 0, 0x18000
	s_add_i32 s60, 0, 0x1c000
	v_add_u32_e32 v140, s59, v193
	v_add_u32_e32 v156, s60, v193
	ds_read_b128 v[100:103], v140
	ds_read_b128 v[132:135], v140 offset:1024
	ds_read_b128 v[136:139], v140 offset:2048
	ds_read_b128 v[140:143], v140 offset:3072
	ds_read_b128 v[144:147], v156
	ds_read_b128 v[148:151], v156 offset:1024
	ds_read_b128 v[152:155], v156 offset:2048
	ds_read_b128 v[156:159], v156 offset:3072
	s_add_i32 s51, s51, 0x80000
	s_add_u32 s52, s3, s51
	s_addc_u32 s53, s30, 0
	s_mov_b32 m0, s26
	v_lshl_add_u64 v[190:191], s[52:53], 0, v[164:165]
	ds_read_b128 v[160:163], v197 offset:32768
	ds_read_b128 v[174:177], v197 offset:33792
	ds_read_b128 v[178:181], v197 offset:34816
	ds_read_b128 v[182:185], v197 offset:35840
	ds_read_b128 v[186:189], v197 offset:36864
	ds_read_b128 v[198:201], v197 offset:37888
	ds_read_b128 v[202:205], v197 offset:38912
	ds_read_b128 v[206:209], v197 offset:39936
	global_load_lds_dwordx4 v[190:191], off
	v_lshl_add_u64 v[190:191], s[52:53], 0, v[166:167]
	s_mov_b32 m0, s27
	s_nop 0
	global_load_lds_dwordx4 v[190:191], off
	s_waitcnt vmcnt(8)
	s_waitcnt lgkmcnt(0)
	s_barrier
	s_waitcnt lgkmcnt(0)
	v_mfma_f32_16x16x32_bf16 v[128:131], v[100:103], v[160:163], v[128:131]
	v_mfma_f32_16x16x32_bf16 v[124:127], v[136:139], v[160:163], v[124:127]
	v_mfma_f32_16x16x32_bf16 v[116:119], v[100:103], v[178:181], v[116:119]
	v_mfma_f32_16x16x32_bf16 v[108:111], v[136:139], v[178:181], v[108:111]
	v_mfma_f32_16x16x32_bf16 v[92:95], v[100:103], v[186:189], v[92:95]
	v_mfma_f32_16x16x32_bf16 v[84:87], v[136:139], v[186:189], v[84:87]
	v_mfma_f32_16x16x32_bf16 v[76:79], v[100:103], v[202:205], v[76:79]
	v_mfma_f32_16x16x32_bf16 v[68:71], v[136:139], v[202:205], v[68:71]
	v_mfma_f32_16x16x32_bf16 v[128:131], v[132:135], v[174:177], v[128:131]
	v_mfma_f32_16x16x32_bf16 v[124:127], v[140:143], v[174:177], v[124:127]
	v_mfma_f32_16x16x32_bf16 v[116:119], v[132:135], v[182:185], v[116:119]
	v_mfma_f32_16x16x32_bf16 v[108:111], v[140:143], v[182:185], v[108:111]
	v_mfma_f32_16x16x32_bf16 v[92:95], v[132:135], v[198:201], v[92:95]
	v_mfma_f32_16x16x32_bf16 v[84:87], v[140:143], v[198:201], v[84:87]
	v_mfma_f32_16x16x32_bf16 v[76:79], v[132:135], v[206:209], v[76:79]
	v_mfma_f32_16x16x32_bf16 v[68:71], v[140:143], v[206:209], v[68:71]
	v_mfma_f32_16x16x32_bf16 v[96:99], v[144:147], v[160:163], v[96:99]
	v_mfma_f32_16x16x32_bf16 v[120:123], v[152:155], v[160:163], v[120:123]
	v_mfma_f32_16x16x32_bf16 v[112:115], v[144:147], v[178:181], v[112:115]
	v_mfma_f32_16x16x32_bf16 v[104:107], v[152:155], v[178:181], v[104:107]
	v_mfma_f32_16x16x32_bf16 v[88:91], v[144:147], v[186:189], v[88:91]
	v_mfma_f32_16x16x32_bf16 v[80:83], v[152:155], v[186:189], v[80:83]
	v_mfma_f32_16x16x32_bf16 v[72:75], v[144:147], v[202:205], v[72:75]
	v_mfma_f32_16x16x32_bf16 v[64:67], v[152:155], v[202:205], v[64:67]
	v_mfma_f32_16x16x32_bf16 v[96:99], v[148:151], v[174:177], v[96:99]
	v_mfma_f32_16x16x32_bf16 v[120:123], v[156:159], v[174:177], v[120:123]
	v_mfma_f32_16x16x32_bf16 v[112:115], v[148:151], v[182:185], v[112:115]
	v_mfma_f32_16x16x32_bf16 v[104:107], v[156:159], v[182:185], v[104:107]
	v_mfma_f32_16x16x32_bf16 v[88:91], v[148:151], v[198:201], v[88:91]
	v_mfma_f32_16x16x32_bf16 v[80:83], v[156:159], v[198:201], v[80:83]
	v_mfma_f32_16x16x32_bf16 v[72:75], v[148:151], v[206:209], v[72:75]
	v_mfma_f32_16x16x32_bf16 v[64:67], v[156:159], v[206:209], v[64:67]
	s_barrier
; #define PG_BAR __builtin_amdgcn_s_barrier()
; template <class Epi, class Sched, class Hook = NoHook>
; __device__ __forceinline__ void gemm_phase_w(LAS unsigned char* lds, const Sched& S, const Epi& E, int wave_id, const Hook& HK = Hook()) {
;     ...
;         if constexpr (!SEG2) {
;             for (int tt = 0; tt < nt; tt += 2) {
;                 if constexpr (GATHER) { if (tt == nt - 2) {
;                     if (has_next) { gnxt_00 = S.grow_l(nxt, lds, nbuf, R0) + (unsigned)(C0 * 2); gnxt_01 = S.grow_l(nxt, lds, nbuf, R1) + (unsigned)(C1 * 2); gnxt_10 = S.grow_l(nxt, lds, nbuf, 128 + R0) + (unsigned)(C0 * 2); gnxt_11 = S.grow_l(nxt, lds, nbuf, 128 + R1) + (unsigned)(C1 * 2); }
;                     else { gnxt_00 = gcur_00; gnxt_01 = gcur_01; gnxt_10 = gcur_10; gnxt_11 = gcur_11; } } }
;                 PG_TRIP(tt, false, false, false);
;             }
;         } else {
;             for (int tt = 0; tt < nt - 4; tt += 2) PG_TRIP(tt, false, false, false);
;             PG_TRIP(nt - 4, false, true, false);
;             PG_TRIP(nt - 2, true, false, true);
;         }
;     ...
;         if (wr == 0) PG_BAR;
	s_or_b32 s52, s50, 1
	s_lshl_b32 s53, s52, 7
	s_add_i32 s49, s53, s49
	s_ashr_i32 s51, s49, 31
	s_add_u32 s50, s4, s49
	s_addc_u32 s51, s5, s51
	s_add_i32 s49, s59, s31
	v_lshl_add_u64 v[190:191], s[50:51], 0, v[168:169]
	s_mov_b32 m0, s49
	s_add_i32 s53, s53, s58
	ds_read_b128 v[160:163], v197 offset:49152
	ds_read_b128 v[174:177], v197 offset:50176
	ds_read_b128 v[178:181], v197 offset:51200
	ds_read_b128 v[182:185], v197 offset:52224
	ds_read_b128 v[186:189], v197 offset:53248
	ds_read_b128 v[198:201], v197 offset:54272
	ds_read_b128 v[202:205], v197 offset:55296
	ds_read_b128 v[206:209], v197 offset:56320
	global_load_lds_dwordx4 v[190:191], off
	s_add_i32 m0, s49, 0x2000
	s_ashr_i32 s49, s53, 31
	v_lshl_add_u64 v[190:191], s[50:51], 0, v[170:171]
	s_add_u32 s50, s4, s53
	s_addc_u32 s51, s5, s49
	s_add_i32 s49, s60, s31
	global_load_lds_dwordx4 v[190:191], off
	v_lshl_add_u64 v[190:191], s[50:51], 0, v[168:169]
	s_mov_b32 m0, s49
	s_nop 0
	global_load_lds_dwordx4 v[190:191], off
	s_add_i32 m0, s49, 0x2000
	s_lshl_b32 s49, s52, 12
	s_add_i32 s49, s49, s48
	s_add_u32 s48, s3, s49
	v_lshl_add_u64 v[190:191], s[50:51], 0, v[170:171]
	s_addc_u32 s49, s30, 0
	global_load_lds_dwordx4 v[190:191], off
	v_lshl_add_u64 v[190:191], s[48:49], 0, v[164:165]
	s_mov_b32 m0, s29
	s_nop 0
	global_load_lds_dwordx4 v[190:191], off
	v_lshl_add_u64 v[190:191], s[48:49], 0, v[166:167]
	s_mov_b32 m0, s38
	s_nop 0
	global_load_lds_dwordx4 v[190:191], off
	s_waitcnt vmcnt(8)
	s_waitcnt lgkmcnt(0)
	s_barrier
	s_waitcnt lgkmcnt(0)
	v_mfma_f32_16x16x32_bf16 v[60:63], v[100:103], v[160:163], v[60:63]
	v_mfma_f32_16x16x32_bf16 v[52:55], v[136:139], v[160:163], v[52:55]
	v_mfma_f32_16x16x32_bf16 v[44:47], v[100:103], v[178:181], v[44:47]
	v_mfma_f32_16x16x32_bf16 v[36:39], v[136:139], v[178:181], v[36:39]
	v_mfma_f32_16x16x32_bf16 v[28:31], v[100:103], v[186:189], v[28:31]
	v_mfma_f32_16x16x32_bf16 v[20:23], v[136:139], v[186:189], v[20:23]
	v_mfma_f32_16x16x32_bf16 v[12:15], v[100:103], v[202:205], v[12:15]
	v_mfma_f32_16x16x32_bf16 v[4:7], v[136:139], v[202:205], v[4:7]
	v_mfma_f32_16x16x32_bf16 v[60:63], v[132:135], v[174:177], v[60:63]
	v_mfma_f32_16x16x32_bf16 v[52:55], v[140:143], v[174:177], v[52:55]
	v_mfma_f32_16x16x32_bf16 v[44:47], v[132:135], v[182:185], v[44:47]
	v_mfma_f32_16x16x32_bf16 v[36:39], v[140:143], v[182:185], v[36:39]
	v_mfma_f32_16x16x32_bf16 v[28:31], v[132:135], v[198:201], v[28:31]
	v_mfma_f32_16x16x32_bf16 v[20:23], v[140:143], v[198:201], v[20:23]
	v_mfma_f32_16x16x32_bf16 v[12:15], v[132:135], v[206:209], v[12:15]
	v_mfma_f32_16x16x32_bf16 v[4:7], v[140:143], v[206:209], v[4:7]
	v_mfma_f32_16x16x32_bf16 v[56:59], v[144:147], v[160:163], v[56:59]
	v_mfma_f32_16x16x32_bf16 v[48:51], v[152:155], v[160:163], v[48:51]
	v_mfma_f32_16x16x32_bf16 v[40:43], v[144:147], v[178:181], v[40:43]
	v_mfma_f32_16x16x32_bf16 v[32:35], v[152:155], v[178:181], v[32:35]
	v_mfma_f32_16x16x32_bf16 v[24:27], v[144:147], v[186:189], v[24:27]
	v_mfma_f32_16x16x32_bf16 v[16:19], v[152:155], v[186:189], v[16:19]
	v_mfma_f32_16x16x32_bf16 v[8:11], v[144:147], v[202:205], v[8:11]
	v_mfma_f32_16x16x32_bf16 v[0:3], v[152:155], v[202:205], v[0:3]
	v_mfma_f32_16x16x32_bf16 v[56:59], v[148:151], v[174:177], v[56:59]
	v_mfma_f32_16x16x32_bf16 v[48:51], v[156:159], v[174:177], v[48:51]
	v_mfma_f32_16x16x32_bf16 v[40:43], v[148:151], v[182:185], v[40:43]
	v_mfma_f32_16x16x32_bf16 v[32:35], v[156:159], v[182:185], v[32:35]
	v_mfma_f32_16x16x32_bf16 v[24:27], v[148:151], v[198:201], v[24:27]
	v_mfma_f32_16x16x32_bf16 v[16:19], v[156:159], v[198:201], v[16:19]
	v_mfma_f32_16x16x32_bf16 v[8:11], v[148:151], v[206:209], v[8:11]
	v_mfma_f32_16x16x32_bf16 v[0:3], v[156:159], v[206:209], v[0:3]
	s_barrier
	s_addk_i32 s20, 0x2000
	s_cmp_gt_u32 s21, 29
	s_mov_b32 s21, s45
	s_cbranch_scc0 .LBB0_1983
	s_and_b64 vcc, exec, s[16:17]
	s_cbranch_vccz .LBB0_1986
	s_barrier

; template <class Epi, class Sched, class Hook = NoHook>
; __device__ __forceinline__ void gemm_phase_w(LAS unsigned char* lds, const Sched& S, const Epi& E, int wave_id, const Hook& HK = Hook()) {
;     ...
;         if constexpr (!SEG2) {
;             for (int tt = 0; tt < nt; tt += 2) {
;                 if constexpr (GATHER) { if (tt == nt - 2) {
;                     if (has_next) { gnxt_00 = S.grow_l(nxt, lds, nbuf, R0) + (unsigned)(C0 * 2); gnxt_01 = S.grow_l(nxt, lds, nbuf, R1) + (unsigned)(C1 * 2); gnxt_10 = S.grow_l(nxt, lds, nbuf, 128 + R0) + (unsigned)(C0 * 2); gnxt_11 = S.grow_l(nxt, lds, nbuf, 128 + R1) + (unsigned)(C1 * 2); }
;                     else { gnxt_00 = gcur_00; gnxt_01 = gcur_01; gnxt_10 = gcur_10; gnxt_11 = gcur_11; } } }
;                 PG_TRIP(tt, false, false, false);
.LBB0_2156:
	v_add_u32_e32 v147, s69, v166
	ds_read_b128 v[186:189], v147
	ds_read_b128 v[190:193], v147 offset:1024
	ds_read_b128 v[194:197], v147 offset:2048
	ds_read_b128 v[198:201], v147 offset:3072
	v_add_u32_e32 v147, s70, v166
	ds_read_b128 v[202:205], v147
	ds_read_b128 v[206:209], v147 offset:1024
	ds_read_b128 v[210:213], v147 offset:2048
	ds_read_b128 v[214:217], v147 offset:3072
	v_lshl_add_u64 v[250:251], s[38:39], 0, v[130:131]
	s_add_i32 m0, s58, 0xc000
	ds_read_b128 v[218:221], v182
	ds_read_b128 v[222:225], v182 offset:1024
	ds_read_b128 v[226:229], v182 offset:2048
	ds_read_b128 v[230:233], v182 offset:3072
	ds_read_b128 v[234:237], v182 offset:4096
	ds_read_b128 v[238:241], v182 offset:5120
	ds_read_b128 v[242:245], v182 offset:6144
	ds_read_b128 v[246:249], v182 offset:7168
	global_load_lds_dwordx4 v[250:251], off
	v_lshl_add_u64 v[250:251], s[38:39], 0, v[132:133]
	s_add_i32 m0, s58, 0xe000
	s_nop 0
	global_load_lds_dwordx4 v[250:251], off
	s_waitcnt vmcnt(8)
	s_waitcnt lgkmcnt(0)
	s_barrier
	s_waitcnt lgkmcnt(0)
	v_mfma_f32_16x16x32_bf16 v[124:127], v[186:189], v[218:221], v[124:127]
	v_mfma_f32_16x16x32_bf16 v[120:123], v[194:197], v[218:221], v[120:123]
	v_mfma_f32_16x16x32_bf16 v[108:111], v[186:189], v[226:229], v[108:111]
	v_mfma_f32_16x16x32_bf16 v[104:107], v[194:197], v[226:229], v[104:107]
	v_mfma_f32_16x16x32_bf16 v[92:95], v[186:189], v[234:237], v[92:95]
	v_mfma_f32_16x16x32_bf16 v[88:91], v[194:197], v[234:237], v[88:91]
	v_mfma_f32_16x16x32_bf16 v[76:79], v[186:189], v[242:245], v[76:79]
	v_mfma_f32_16x16x32_bf16 v[72:75], v[194:197], v[242:245], v[72:75]
	v_mfma_f32_16x16x32_bf16 v[124:127], v[190:193], v[222:225], v[124:127]
	v_mfma_f32_16x16x32_bf16 v[120:123], v[198:201], v[222:225], v[120:123]
	v_mfma_f32_16x16x32_bf16 v[108:111], v[190:193], v[230:233], v[108:111]
	v_mfma_f32_16x16x32_bf16 v[104:107], v[198:201], v[230:233], v[104:107]
	v_mfma_f32_16x16x32_bf16 v[92:95], v[190:193], v[238:241], v[92:95]
	v_mfma_f32_16x16x32_bf16 v[88:91], v[198:201], v[238:241], v[88:91]
	v_mfma_f32_16x16x32_bf16 v[76:79], v[190:193], v[246:249], v[76:79]
	v_mfma_f32_16x16x32_bf16 v[72:75], v[198:201], v[246:249], v[72:75]
	v_mfma_f32_16x16x32_bf16 v[116:119], v[202:205], v[218:221], v[116:119]
	v_mfma_f32_16x16x32_bf16 v[112:115], v[210:213], v[218:221], v[112:115]
	v_mfma_f32_16x16x32_bf16 v[100:103], v[202:205], v[226:229], v[100:103]
	v_mfma_f32_16x16x32_bf16 v[96:99], v[210:213], v[226:229], v[96:99]
	v_mfma_f32_16x16x32_bf16 v[84:87], v[202:205], v[234:237], v[84:87]
	v_mfma_f32_16x16x32_bf16 v[80:83], v[210:213], v[234:237], v[80:83]
	v_mfma_f32_16x16x32_bf16 v[68:71], v[202:205], v[242:245], v[68:71]
	v_mfma_f32_16x16x32_bf16 v[64:67], v[210:213], v[242:245], v[64:67]
	v_mfma_f32_16x16x32_bf16 v[116:119], v[206:209], v[222:225], v[116:119]
	v_mfma_f32_16x16x32_bf16 v[112:115], v[214:217], v[222:225], v[112:115]
	v_mfma_f32_16x16x32_bf16 v[100:103], v[206:209], v[230:233], v[100:103]
	v_mfma_f32_16x16x32_bf16 v[96:99], v[214:217], v[230:233], v[96:99]
	v_mfma_f32_16x16x32_bf16 v[84:87], v[206:209], v[238:241], v[84:87]
	v_mfma_f32_16x16x32_bf16 v[80:83], v[214:217], v[238:241], v[80:83]
	v_mfma_f32_16x16x32_bf16 v[68:71], v[206:209], v[246:249], v[68:71]
	v_mfma_f32_16x16x32_bf16 v[64:67], v[214:217], v[246:249], v[64:67]
	s_barrier
	s_and_b64 s[40:41], s[40:41], exec
	s_cselect_b32 s22, 0, s80
	s_add_i32 s84, s81, s22
	s_ashr_i32 s41, s84, 31
	s_add_u32 s40, s16, s84
	s_addc_u32 s41, s17, s41
	s_add_i32 s85, s69, s44
	v_lshl_add_u64 v[250:251], s[40:41], 0, v[136:137]
	s_mov_b32 m0, s85
	s_add_i32 s84, s84, 0x80000
	ds_read_b128 v[218:221], v182 offset:16384
	ds_read_b128 v[222:225], v182 offset:17408
	ds_read_b128 v[226:229], v182 offset:18432
	ds_read_b128 v[230:233], v182 offset:19456
	ds_read_b128 v[234:237], v182 offset:20480
	ds_read_b128 v[238:241], v182 offset:21504
	ds_read_b128 v[242:245], v182 offset:22528
	ds_read_b128 v[246:249], v182 offset:23552
	global_load_lds_dwordx4 v[250:251], off
	v_lshl_add_u64 v[250:251], s[40:41], 0, v[138:139]
	s_add_i32 m0, s85, 0x2000
	s_ashr_i32 s41, s84, 31
	s_add_u32 s40, s16, s84
	s_addc_u32 s41, s17, s41
	s_add_i32 s84, s70, s44
	global_load_lds_dwordx4 v[250:251], off
	v_lshl_add_u64 v[250:251], s[40:41], 0, v[136:137]
	s_mov_b32 m0, s84
	v_mov_b32_e32 v147, v141
	global_load_lds_dwordx4 v[250:251], off
	s_add_i32 m0, s84, 0x2000
	v_lshl_add_u64 v[250:251], s[40:41], 0, v[138:139]
	s_add_u32 s40, s14, s22
	global_load_lds_dwordx4 v[250:251], off
	s_addc_u32 s41, s15, 0
	s_mov_b32 m0, s58
	s_nop 0
	global_load_lds_dwordx4 v140, s[40:41]
	s_mov_b32 m0, s59
	s_nop 0
	global_load_lds_dwordx4 v146, s[40:41]
	s_waitcnt vmcnt(8)
	s_waitcnt lgkmcnt(0)
	s_barrier
	s_waitcnt lgkmcnt(0)
	v_mfma_f32_16x16x32_bf16 v[60:63], v[186:189], v[218:221], v[60:63]
	v_mfma_f32_16x16x32_bf16 v[56:59], v[194:197], v[218:221], v[56:59]
	v_mfma_f32_16x16x32_bf16 v[44:47], v[186:189], v[226:229], v[44:47]
	v_mfma_f32_16x16x32_bf16 v[40:43], v[194:197], v[226:229], v[40:43]
	v_mfma_f32_16x16x32_bf16 v[28:31], v[186:189], v[234:237], v[28:31]
	v_mfma_f32_16x16x32_bf16 v[24:27], v[194:197], v[234:237], v[24:27]
	v_mfma_f32_16x16x32_bf16 v[12:15], v[186:189], v[242:245], v[12:15]
	v_mfma_f32_16x16x32_bf16 v[8:11], v[194:197], v[242:245], v[8:11]
	v_mfma_f32_16x16x32_bf16 v[60:63], v[190:193], v[222:225], v[60:63]
	v_mfma_f32_16x16x32_bf16 v[56:59], v[198:201], v[222:225], v[56:59]
	v_mfma_f32_16x16x32_bf16 v[44:47], v[190:193], v[230:233], v[44:47]
	v_mfma_f32_16x16x32_bf16 v[40:43], v[198:201], v[230:233], v[40:43]
	v_mfma_f32_16x16x32_bf16 v[28:31], v[190:193], v[238:241], v[28:31]
	v_mfma_f32_16x16x32_bf16 v[24:27], v[198:201], v[238:241], v[24:27]
	v_mfma_f32_16x16x32_bf16 v[12:15], v[190:193], v[246:249], v[12:15]
	v_mfma_f32_16x16x32_bf16 v[8:11], v[198:201], v[246:249], v[8:11]
	v_mfma_f32_16x16x32_bf16 v[52:55], v[202:205], v[218:221], v[52:55]
	v_mfma_f32_16x16x32_bf16 v[48:51], v[210:213], v[218:221], v[48:51]
	v_mfma_f32_16x16x32_bf16 v[36:39], v[202:205], v[226:229], v[36:39]
	v_mfma_f32_16x16x32_bf16 v[32:35], v[210:213], v[226:229], v[32:35]
	v_mfma_f32_16x16x32_bf16 v[20:23], v[202:205], v[234:237], v[20:23]
	v_mfma_f32_16x16x32_bf16 v[16:19], v[210:213], v[234:237], v[16:19]
	v_mfma_f32_16x16x32_bf16 v[4:7], v[202:205], v[242:245], v[4:7]
	v_mfma_f32_16x16x32_bf16 v[0:3], v[210:213], v[242:245], v[0:3]
	v_mfma_f32_16x16x32_bf16 v[52:55], v[206:209], v[222:225], v[52:55]
	v_mfma_f32_16x16x32_bf16 v[48:51], v[214:217], v[222:225], v[48:51]
	v_mfma_f32_16x16x32_bf16 v[36:39], v[206:209], v[230:233], v[36:39]
	v_mfma_f32_16x16x32_bf16 v[32:35], v[214:217], v[230:233], v[32:35]
	v_mfma_f32_16x16x32_bf16 v[20:23], v[206:209], v[238:241], v[20:23]
	v_mfma_f32_16x16x32_bf16 v[16:19], v[214:217], v[238:241], v[16:19]
	v_mfma_f32_16x16x32_bf16 v[4:7], v[206:209], v[246:249], v[4:7]
	v_mfma_f32_16x16x32_bf16 v[0:3], v[214:217], v[246:249], v[0:3]
	s_barrier
	s_add_i32 s84, 0, 0x18000
	v_add_u32_e32 v185, s84, v166
	s_add_i32 s85, 0, 0x1c000
	ds_read_b128 v[186:189], v185
	ds_read_b128 v[190:193], v185 offset:1024
	ds_read_b128 v[194:197], v185 offset:2048
	ds_read_b128 v[198:201], v185 offset:3072
	v_add_u32_e32 v185, s85, v166
	ds_read_b128 v[202:205], v185
	ds_read_b128 v[206:209], v185 offset:1024
	ds_read_b128 v[210:213], v185 offset:2048
	ds_read_b128 v[214:217], v185 offset:3072
	s_mov_b32 m0, s60
	v_lshl_add_u64 v[148:149], s[40:41], 0, v[148:149]
	ds_read_b128 v[218:221], v182 offset:32768
	ds_read_b128 v[222:225], v182 offset:33792
	ds_read_b128 v[226:229], v182 offset:34816
	ds_read_b128 v[230:233], v182 offset:35840
	ds_read_b128 v[234:237], v182 offset:36864
	ds_read_b128 v[238:241], v182 offset:37888
	ds_read_b128 v[242:245], v182 offset:38912
	ds_read_b128 v[246:249], v182 offset:39936
	global_load_lds_dwordx4 v[148:149], off
	v_lshl_add_u64 v[148:149], s[40:41], 0, v[150:151]
	s_mov_b32 m0, s61
	s_nop 0
	global_load_lds_dwordx4 v[148:149], off
	s_waitcnt vmcnt(8)
	s_waitcnt lgkmcnt(0)
	s_barrier
	s_waitcnt lgkmcnt(0)
	v_mfma_f32_16x16x32_bf16 v[124:127], v[186:189], v[218:221], v[124:127]
	v_mfma_f32_16x16x32_bf16 v[120:123], v[194:197], v[218:221], v[120:123]
	v_mfma_f32_16x16x32_bf16 v[108:111], v[186:189], v[226:229], v[108:111]
	v_mfma_f32_16x16x32_bf16 v[104:107], v[194:197], v[226:229], v[104:107]
	v_mfma_f32_16x16x32_bf16 v[92:95], v[186:189], v[234:237], v[92:95]
	v_mfma_f32_16x16x32_bf16 v[88:91], v[194:197], v[234:237], v[88:91]
	v_mfma_f32_16x16x32_bf16 v[76:79], v[186:189], v[242:245], v[76:79]
	v_mfma_f32_16x16x32_bf16 v[72:75], v[194:197], v[242:245], v[72:75]
	v_mfma_f32_16x16x32_bf16 v[124:127], v[190:193], v[222:225], v[124:127]
	v_mfma_f32_16x16x32_bf16 v[120:123], v[198:201], v[222:225], v[120:123]
	v_mfma_f32_16x16x32_bf16 v[108:111], v[190:193], v[230:233], v[108:111]
	v_mfma_f32_16x16x32_bf16 v[104:107], v[198:201], v[230:233], v[104:107]
	v_mfma_f32_16x16x32_bf16 v[92:95], v[190:193], v[238:241], v[92:95]
	v_mfma_f32_16x16x32_bf16 v[88:91], v[198:201], v[238:241], v[88:91]
	v_mfma_f32_16x16x32_bf16 v[76:79], v[190:193], v[246:249], v[76:79]
	v_mfma_f32_16x16x32_bf16 v[72:75], v[198:201], v[246:249], v[72:75]
	v_mfma_f32_16x16x32_bf16 v[116:119], v[202:205], v[218:221], v[116:119]
	v_mfma_f32_16x16x32_bf16 v[112:115], v[210:213], v[218:221], v[112:115]
	v_mfma_f32_16x16x32_bf16 v[100:103], v[202:205], v[226:229], v[100:103]
	v_mfma_f32_16x16x32_bf16 v[96:99], v[210:213], v[226:229], v[96:99]
	v_mfma_f32_16x16x32_bf16 v[84:87], v[202:205], v[234:237], v[84:87]
	v_mfma_f32_16x16x32_bf16 v[80:83], v[210:213], v[234:237], v[80:83]
	v_mfma_f32_16x16x32_bf16 v[68:71], v[202:205], v[242:245], v[68:71]
	v_mfma_f32_16x16x32_bf16 v[64:67], v[210:213], v[242:245], v[64:67]
	v_mfma_f32_16x16x32_bf16 v[116:119], v[206:209], v[222:225], v[116:119]
	v_mfma_f32_16x16x32_bf16 v[112:115], v[214:217], v[222:225], v[112:115]
	v_mfma_f32_16x16x32_bf16 v[100:103], v[206:209], v[230:233], v[100:103]
	v_mfma_f32_16x16x32_bf16 v[96:99], v[214:217], v[230:233], v[96:99]
	v_mfma_f32_16x16x32_bf16 v[84:87], v[206:209], v[238:241], v[84:87]
	v_mfma_f32_16x16x32_bf16 v[80:83], v[214:217], v[238:241], v[80:83]
	v_mfma_f32_16x16x32_bf16 v[68:71], v[206:209], v[246:249], v[68:71]
	v_mfma_f32_16x16x32_bf16 v[64:67], v[214:217], v[246:249], v[64:67]
	s_barrier
; template <class Epi, class Sched, class Hook = NoHook>
; __device__ __forceinline__ void gemm_phase_w(LAS unsigned char* lds, const Sched& S, const Epi& E, int wave_id, const Hook& HK = Hook()) {
;     ...
;         if constexpr (!SEG2) {
;             for (int tt = 0; tt < nt; tt += 2) {
;                 if constexpr (GATHER) { if (tt == nt - 2) {
;                     if (has_next) { gnxt_00 = S.grow_l(nxt, lds, nbuf, R0) + (unsigned)(C0 * 2); gnxt_01 = S.grow_l(nxt, lds, nbuf, R1) + (unsigned)(C1 * 2); gnxt_10 = S.grow_l(nxt, lds, nbuf, 128 + R0) + (unsigned)(C0 * 2); gnxt_11 = S.grow_l(nxt, lds, nbuf, 128 + R1) + (unsigned)(C1 * 2); }
;                     else { gnxt_00 = gcur_00; gnxt_01 = gcur_01; gnxt_10 = gcur_10; gnxt_11 = gcur_11; } } }
;                 PG_TRIP(tt, false, false, false);
;             }
	s_bitset1_b32 s22, 7
	s_add_i32 s81, s81, s22
	s_ashr_i32 s41, s81, 31
	s_add_u32 s40, s16, s81
	s_addc_u32 s41, s17, s41
	s_add_i32 s84, s84, s44
	v_lshl_add_u64 v[246:247], s[40:41], 0, v[136:137]
	s_mov_b32 m0, s84
	s_add_i32 s81, s81, 0x80000
	ds_read_b128 v[148:151], v182 offset:49152
	ds_read_b128 v[218:221], v182 offset:50176
	ds_read_b128 v[222:225], v182 offset:51200
	ds_read_b128 v[226:229], v182 offset:52224
	ds_read_b128 v[230:233], v182 offset:53248
	ds_read_b128 v[234:237], v182 offset:54272
	ds_read_b128 v[238:241], v182 offset:55296
	ds_read_b128 v[242:245], v182 offset:56320
	global_load_lds_dwordx4 v[246:247], off
	v_lshl_add_u64 v[246:247], s[40:41], 0, v[138:139]
	s_add_i32 m0, s84, 0x2000
	s_ashr_i32 s41, s81, 31
	s_add_u32 s40, s16, s81
	s_addc_u32 s41, s17, s41
	s_add_i32 s81, s85, s44
	global_load_lds_dwordx4 v[246:247], off
	v_lshl_add_u64 v[246:247], s[40:41], 0, v[136:137]
	s_mov_b32 m0, s81
	v_lshl_add_u64 v[146:147], s[14:15], 0, v[146:147]
	global_load_lds_dwordx4 v[246:247], off
	v_lshl_add_u64 v[246:247], s[40:41], 0, v[138:139]
	s_add_i32 m0, s81, 0x2000
	v_lshl_add_u64 v[146:147], v[146:147], 0, s[22:23]
	global_load_lds_dwordx4 v[246:247], off
	v_lshl_add_u64 v[246:247], s[14:15], 0, v[140:141]
	v_lshl_add_u64 v[246:247], v[246:247], 0, s[22:23]
	s_mov_b32 m0, s62
	s_nop 0
	global_load_lds_dwordx4 v[246:247], off
	s_mov_b32 m0, s63
	s_nop 0
	global_load_lds_dwordx4 v[146:147], off
	s_waitcnt vmcnt(8)
	s_waitcnt lgkmcnt(0)
	s_barrier
	s_waitcnt lgkmcnt(0)
	v_mfma_f32_16x16x32_bf16 v[60:63], v[186:189], v[148:151], v[60:63]
	v_mfma_f32_16x16x32_bf16 v[56:59], v[194:197], v[148:151], v[56:59]
	v_mfma_f32_16x16x32_bf16 v[44:47], v[186:189], v[222:225], v[44:47]
	v_mfma_f32_16x16x32_bf16 v[40:43], v[194:197], v[222:225], v[40:43]
	v_mfma_f32_16x16x32_bf16 v[28:31], v[186:189], v[230:233], v[28:31]
	v_mfma_f32_16x16x32_bf16 v[24:27], v[194:197], v[230:233], v[24:27]
	v_mfma_f32_16x16x32_bf16 v[12:15], v[186:189], v[238:241], v[12:15]
	v_mfma_f32_16x16x32_bf16 v[8:11], v[194:197], v[238:241], v[8:11]
	v_mfma_f32_16x16x32_bf16 v[60:63], v[190:193], v[218:221], v[60:63]
	v_mfma_f32_16x16x32_bf16 v[56:59], v[198:201], v[218:221], v[56:59]
	v_mfma_f32_16x16x32_bf16 v[44:47], v[190:193], v[226:229], v[44:47]
	v_mfma_f32_16x16x32_bf16 v[40:43], v[198:201], v[226:229], v[40:43]
	v_mfma_f32_16x16x32_bf16 v[28:31], v[190:193], v[234:237], v[28:31]
	v_mfma_f32_16x16x32_bf16 v[24:27], v[198:201], v[234:237], v[24:27]
	v_mfma_f32_16x16x32_bf16 v[12:15], v[190:193], v[242:245], v[12:15]
	v_mfma_f32_16x16x32_bf16 v[8:11], v[198:201], v[242:245], v[8:11]
	v_mfma_f32_16x16x32_bf16 v[52:55], v[202:205], v[148:151], v[52:55]
	v_mfma_f32_16x16x32_bf16 v[48:51], v[210:213], v[148:151], v[48:51]
	v_mfma_f32_16x16x32_bf16 v[36:39], v[202:205], v[222:225], v[36:39]
	v_mfma_f32_16x16x32_bf16 v[32:35], v[210:213], v[222:225], v[32:35]
	v_mfma_f32_16x16x32_bf16 v[20:23], v[202:205], v[230:233], v[20:23]
	v_mfma_f32_16x16x32_bf16 v[16:19], v[210:213], v[230:233], v[16:19]
	v_mfma_f32_16x16x32_bf16 v[4:7], v[202:205], v[238:241], v[4:7]
	v_mfma_f32_16x16x32_bf16 v[0:3], v[210:213], v[238:241], v[0:3]
	v_mfma_f32_16x16x32_bf16 v[52:55], v[206:209], v[218:221], v[52:55]
	v_mfma_f32_16x16x32_bf16 v[48:51], v[214:217], v[218:221], v[48:51]
	v_mfma_f32_16x16x32_bf16 v[36:39], v[206:209], v[226:229], v[36:39]
	v_mfma_f32_16x16x32_bf16 v[32:35], v[214:217], v[226:229], v[32:35]
	v_mfma_f32_16x16x32_bf16 v[20:23], v[206:209], v[234:237], v[20:23]
	v_mfma_f32_16x16x32_bf16 v[16:19], v[214:217], v[234:237], v[16:19]
	v_mfma_f32_16x16x32_bf16 v[4:7], v[206:209], v[242:245], v[4:7]
	v_mfma_f32_16x16x32_bf16 v[0:3], v[214:217], v[242:245], v[0:3]
	s_barrier
	s_add_i32 s79, s79, 2
	s_addk_i32 s80, 0x100
	s_add_u32 s38, s38, 0x100
	s_addc_u32 s39, s39, 0
	s_cmp_gt_u32 s79, 29
	s_cbranch_scc1 .LBB0_2160

; template <class Epi, class Sched, class Hook = NoHook>
; __device__ __forceinline__ void gemm_phase_w(LAS unsigned char* lds, const Sched& S, const Epi& E, int wave_id, const Hook& HK = Hook()) {
;     ...
;         if constexpr (!SEG2) {
;             for (int tt = 0; tt < nt; tt += 2) {
;                 if constexpr (GATHER) { if (tt == nt - 2) {
;                     if (has_next) { gnxt_00 = S.grow_l(nxt, lds, nbuf, R0) + (unsigned)(C0 * 2); gnxt_01 = S.grow_l(nxt, lds, nbuf, R1) + (unsigned)(C1 * 2); gnxt_10 = S.grow_l(nxt, lds, nbuf, 128 + R0) + (unsigned)(C0 * 2); gnxt_11 = S.grow_l(nxt, lds, nbuf, 128 + R1) + (unsigned)(C1 * 2); }
;                     else { gnxt_00 = gcur_00; gnxt_01 = gcur_01; gnxt_10 = gcur_10; gnxt_11 = gcur_11; } } }
;                 PG_TRIP(tt, false, false, false);
.LBB0_2410:
	v_add_u32_e32 v147, s49, v163
	ds_read_b128 v[182:185], v147
	ds_read_b128 v[186:189], v147 offset:1024
	ds_read_b128 v[190:193], v147 offset:2048
	ds_read_b128 v[194:197], v147 offset:3072
	v_add_u32_e32 v147, s50, v163
	ds_read_b128 v[198:201], v147
	ds_read_b128 v[202:205], v147 offset:1024
	ds_read_b128 v[206:209], v147 offset:2048
	ds_read_b128 v[210:213], v147 offset:3072
	v_lshl_add_u64 v[246:247], s[38:39], 0, v[130:131]
	s_add_i32 m0, s57, 0xc000
	ds_read_b128 v[214:217], v179
	ds_read_b128 v[218:221], v179 offset:1024
	ds_read_b128 v[222:225], v179 offset:2048
	ds_read_b128 v[226:229], v179 offset:3072
	ds_read_b128 v[230:233], v179 offset:4096
	ds_read_b128 v[234:237], v179 offset:5120
	ds_read_b128 v[238:241], v179 offset:6144
	ds_read_b128 v[242:245], v179 offset:7168
	global_load_lds_dwordx4 v[246:247], off
	v_lshl_add_u64 v[246:247], s[38:39], 0, v[132:133]
	s_add_i32 m0, s57, 0xe000
	s_nop 0
	global_load_lds_dwordx4 v[246:247], off
	s_waitcnt vmcnt(8)
	s_waitcnt lgkmcnt(0)
	s_barrier
	s_waitcnt lgkmcnt(0)
	v_mfma_f32_16x16x32_bf16 v[124:127], v[182:185], v[214:217], v[124:127]
	v_mfma_f32_16x16x32_bf16 v[120:123], v[190:193], v[214:217], v[120:123]
	v_mfma_f32_16x16x32_bf16 v[108:111], v[182:185], v[222:225], v[108:111]
	v_mfma_f32_16x16x32_bf16 v[104:107], v[190:193], v[222:225], v[104:107]
	v_mfma_f32_16x16x32_bf16 v[92:95], v[182:185], v[230:233], v[92:95]
	v_mfma_f32_16x16x32_bf16 v[88:91], v[190:193], v[230:233], v[88:91]
	v_mfma_f32_16x16x32_bf16 v[76:79], v[182:185], v[238:241], v[76:79]
	v_mfma_f32_16x16x32_bf16 v[72:75], v[190:193], v[238:241], v[72:75]
	v_mfma_f32_16x16x32_bf16 v[124:127], v[186:189], v[218:221], v[124:127]
	v_mfma_f32_16x16x32_bf16 v[120:123], v[194:197], v[218:221], v[120:123]
	v_mfma_f32_16x16x32_bf16 v[108:111], v[186:189], v[226:229], v[108:111]
	v_mfma_f32_16x16x32_bf16 v[104:107], v[194:197], v[226:229], v[104:107]
	v_mfma_f32_16x16x32_bf16 v[92:95], v[186:189], v[234:237], v[92:95]
	v_mfma_f32_16x16x32_bf16 v[88:91], v[194:197], v[234:237], v[88:91]
	v_mfma_f32_16x16x32_bf16 v[76:79], v[186:189], v[242:245], v[76:79]
	v_mfma_f32_16x16x32_bf16 v[72:75], v[194:197], v[242:245], v[72:75]
	v_mfma_f32_16x16x32_bf16 v[116:119], v[198:201], v[214:217], v[116:119]
	v_mfma_f32_16x16x32_bf16 v[112:115], v[206:209], v[214:217], v[112:115]
	v_mfma_f32_16x16x32_bf16 v[100:103], v[198:201], v[222:225], v[100:103]
	v_mfma_f32_16x16x32_bf16 v[96:99], v[206:209], v[222:225], v[96:99]
	v_mfma_f32_16x16x32_bf16 v[84:87], v[198:201], v[230:233], v[84:87]
	v_mfma_f32_16x16x32_bf16 v[80:83], v[206:209], v[230:233], v[80:83]
	v_mfma_f32_16x16x32_bf16 v[68:71], v[198:201], v[238:241], v[68:71]
	v_mfma_f32_16x16x32_bf16 v[64:67], v[206:209], v[238:241], v[64:67]
	v_mfma_f32_16x16x32_bf16 v[116:119], v[202:205], v[218:221], v[116:119]
	v_mfma_f32_16x16x32_bf16 v[112:115], v[210:213], v[218:221], v[112:115]
	v_mfma_f32_16x16x32_bf16 v[100:103], v[202:205], v[226:229], v[100:103]
	v_mfma_f32_16x16x32_bf16 v[96:99], v[210:213], v[226:229], v[96:99]
	v_mfma_f32_16x16x32_bf16 v[84:87], v[202:205], v[234:237], v[84:87]
	v_mfma_f32_16x16x32_bf16 v[80:83], v[210:213], v[234:237], v[80:83]
	v_mfma_f32_16x16x32_bf16 v[68:71], v[202:205], v[242:245], v[68:71]
	v_mfma_f32_16x16x32_bf16 v[64:67], v[210:213], v[242:245], v[64:67]
	s_barrier
	s_and_b64 s[40:41], s[40:41], exec
	s_cselect_b32 s22, 0, s70
	s_add_i32 s72, s71, s22
	s_ashr_i32 s41, s72, 31
	s_add_u32 s40, s16, s72
	s_addc_u32 s41, s17, s41
	s_add_i32 s73, s49, s44
	v_lshl_add_u64 v[246:247], s[40:41], 0, v[136:137]
	s_mov_b32 m0, s73
	s_add_i32 s72, s72, 0x80000
	ds_read_b128 v[214:217], v179 offset:16384
	ds_read_b128 v[218:221], v179 offset:17408
	ds_read_b128 v[222:225], v179 offset:18432
	ds_read_b128 v[226:229], v179 offset:19456
	ds_read_b128 v[230:233], v179 offset:20480
	ds_read_b128 v[234:237], v179 offset:21504
	ds_read_b128 v[238:241], v179 offset:22528
	ds_read_b128 v[242:245], v179 offset:23552
	global_load_lds_dwordx4 v[246:247], off
	v_lshl_add_u64 v[246:247], s[40:41], 0, v[138:139]
	s_add_i32 m0, s73, 0x2000
	s_ashr_i32 s41, s72, 31
	s_add_u32 s40, s16, s72
	s_addc_u32 s41, s17, s41
	s_add_i32 s72, s50, s44
	global_load_lds_dwordx4 v[246:247], off
	v_lshl_add_u64 v[246:247], s[40:41], 0, v[136:137]
	s_mov_b32 m0, s72
	v_mov_b32_e32 v147, v141
	global_load_lds_dwordx4 v[246:247], off
	s_add_i32 m0, s72, 0x2000
	v_lshl_add_u64 v[246:247], s[40:41], 0, v[138:139]
	s_add_u32 s40, s14, s22
	global_load_lds_dwordx4 v[246:247], off
	s_addc_u32 s41, s15, 0
	s_mov_b32 m0, s57
	s_nop 0
	global_load_lds_dwordx4 v140, s[40:41]
	s_mov_b32 m0, s58
	s_nop 0
	global_load_lds_dwordx4 v146, s[40:41]
	s_waitcnt vmcnt(8)
	s_waitcnt lgkmcnt(0)
	s_barrier
	s_waitcnt lgkmcnt(0)
	v_mfma_f32_16x16x32_bf16 v[60:63], v[182:185], v[214:217], v[60:63]
	v_mfma_f32_16x16x32_bf16 v[56:59], v[190:193], v[214:217], v[56:59]
	v_mfma_f32_16x16x32_bf16 v[44:47], v[182:185], v[222:225], v[44:47]
	v_mfma_f32_16x16x32_bf16 v[40:43], v[190:193], v[222:225], v[40:43]
	v_mfma_f32_16x16x32_bf16 v[28:31], v[182:185], v[230:233], v[28:31]
	v_mfma_f32_16x16x32_bf16 v[24:27], v[190:193], v[230:233], v[24:27]
	v_mfma_f32_16x16x32_bf16 v[12:15], v[182:185], v[238:241], v[12:15]
	v_mfma_f32_16x16x32_bf16 v[8:11], v[190:193], v[238:241], v[8:11]
	v_mfma_f32_16x16x32_bf16 v[60:63], v[186:189], v[218:221], v[60:63]
	v_mfma_f32_16x16x32_bf16 v[56:59], v[194:197], v[218:221], v[56:59]
	v_mfma_f32_16x16x32_bf16 v[44:47], v[186:189], v[226:229], v[44:47]
	v_mfma_f32_16x16x32_bf16 v[40:43], v[194:197], v[226:229], v[40:43]
	v_mfma_f32_16x16x32_bf16 v[28:31], v[186:189], v[234:237], v[28:31]
	v_mfma_f32_16x16x32_bf16 v[24:27], v[194:197], v[234:237], v[24:27]
	v_mfma_f32_16x16x32_bf16 v[12:15], v[186:189], v[242:245], v[12:15]
	v_mfma_f32_16x16x32_bf16 v[8:11], v[194:197], v[242:245], v[8:11]
	v_mfma_f32_16x16x32_bf16 v[52:55], v[198:201], v[214:217], v[52:55]
	v_mfma_f32_16x16x32_bf16 v[48:51], v[206:209], v[214:217], v[48:51]
	v_mfma_f32_16x16x32_bf16 v[36:39], v[198:201], v[222:225], v[36:39]
	v_mfma_f32_16x16x32_bf16 v[32:35], v[206:209], v[222:225], v[32:35]
	v_mfma_f32_16x16x32_bf16 v[20:23], v[198:201], v[230:233], v[20:23]
	v_mfma_f32_16x16x32_bf16 v[16:19], v[206:209], v[230:233], v[16:19]
	v_mfma_f32_16x16x32_bf16 v[4:7], v[198:201], v[238:241], v[4:7]
	v_mfma_f32_16x16x32_bf16 v[0:3], v[206:209], v[238:241], v[0:3]
	v_mfma_f32_16x16x32_bf16 v[52:55], v[202:205], v[218:221], v[52:55]
	v_mfma_f32_16x16x32_bf16 v[48:51], v[210:213], v[218:221], v[48:51]
	v_mfma_f32_16x16x32_bf16 v[36:39], v[202:205], v[226:229], v[36:39]
	v_mfma_f32_16x16x32_bf16 v[32:35], v[210:213], v[226:229], v[32:35]
	v_mfma_f32_16x16x32_bf16 v[20:23], v[202:205], v[234:237], v[20:23]
	v_mfma_f32_16x16x32_bf16 v[16:19], v[210:213], v[234:237], v[16:19]
	v_mfma_f32_16x16x32_bf16 v[4:7], v[202:205], v[242:245], v[4:7]
	v_mfma_f32_16x16x32_bf16 v[0:3], v[210:213], v[242:245], v[0:3]
	s_barrier
	s_add_i32 s72, 0, 0x18000
	s_add_i32 s73, 0, 0x1c000
	v_add_u32_e32 v194, s72, v163
	v_add_u32_e32 v210, s73, v163
	ds_read_b128 v[182:185], v194
	ds_read_b128 v[186:189], v194 offset:1024
	ds_read_b128 v[190:193], v194 offset:2048
	ds_read_b128 v[194:197], v194 offset:3072
	ds_read_b128 v[198:201], v210
	ds_read_b128 v[202:205], v210 offset:1024
	ds_read_b128 v[206:209], v210 offset:2048
	ds_read_b128 v[210:213], v210 offset:3072
	s_mov_b32 m0, s59
	v_lshl_add_u64 v[148:149], s[40:41], 0, v[148:149]
	ds_read_b128 v[214:217], v179 offset:32768
	ds_read_b128 v[218:221], v179 offset:33792
	ds_read_b128 v[222:225], v179 offset:34816
	ds_read_b128 v[226:229], v179 offset:35840
	ds_read_b128 v[230:233], v179 offset:36864
	ds_read_b128 v[234:237], v179 offset:37888
	ds_read_b128 v[238:241], v179 offset:38912
	ds_read_b128 v[242:245], v179 offset:39936
	global_load_lds_dwordx4 v[148:149], off
	v_lshl_add_u64 v[148:149], s[40:41], 0, v[150:151]
	s_mov_b32 m0, s60
	s_nop 0
	global_load_lds_dwordx4 v[148:149], off
	s_waitcnt vmcnt(8)
	s_waitcnt lgkmcnt(0)
	s_barrier
	s_waitcnt lgkmcnt(0)
	v_mfma_f32_16x16x32_bf16 v[124:127], v[182:185], v[214:217], v[124:127]
	v_mfma_f32_16x16x32_bf16 v[120:123], v[190:193], v[214:217], v[120:123]
	v_mfma_f32_16x16x32_bf16 v[108:111], v[182:185], v[222:225], v[108:111]
	v_mfma_f32_16x16x32_bf16 v[104:107], v[190:193], v[222:225], v[104:107]
	v_mfma_f32_16x16x32_bf16 v[92:95], v[182:185], v[230:233], v[92:95]
	v_mfma_f32_16x16x32_bf16 v[88:91], v[190:193], v[230:233], v[88:91]
	v_mfma_f32_16x16x32_bf16 v[76:79], v[182:185], v[238:241], v[76:79]
	v_mfma_f32_16x16x32_bf16 v[72:75], v[190:193], v[238:241], v[72:75]
	v_mfma_f32_16x16x32_bf16 v[124:127], v[186:189], v[218:221], v[124:127]
	v_mfma_f32_16x16x32_bf16 v[120:123], v[194:197], v[218:221], v[120:123]
	v_mfma_f32_16x16x32_bf16 v[108:111], v[186:189], v[226:229], v[108:111]
	v_mfma_f32_16x16x32_bf16 v[104:107], v[194:197], v[226:229], v[104:107]
	v_mfma_f32_16x16x32_bf16 v[92:95], v[186:189], v[234:237], v[92:95]
	v_mfma_f32_16x16x32_bf16 v[88:91], v[194:197], v[234:237], v[88:91]
	v_mfma_f32_16x16x32_bf16 v[76:79], v[186:189], v[242:245], v[76:79]
	v_mfma_f32_16x16x32_bf16 v[72:75], v[194:197], v[242:245], v[72:75]
	v_mfma_f32_16x16x32_bf16 v[116:119], v[198:201], v[214:217], v[116:119]
	v_mfma_f32_16x16x32_bf16 v[112:115], v[206:209], v[214:217], v[112:115]
	v_mfma_f32_16x16x32_bf16 v[100:103], v[198:201], v[222:225], v[100:103]
	v_mfma_f32_16x16x32_bf16 v[96:99], v[206:209], v[222:225], v[96:99]
	v_mfma_f32_16x16x32_bf16 v[84:87], v[198:201], v[230:233], v[84:87]
	v_mfma_f32_16x16x32_bf16 v[80:83], v[206:209], v[230:233], v[80:83]
	v_mfma_f32_16x16x32_bf16 v[68:71], v[198:201], v[238:241], v[68:71]
	v_mfma_f32_16x16x32_bf16 v[64:67], v[206:209], v[238:241], v[64:67]
	v_mfma_f32_16x16x32_bf16 v[116:119], v[202:205], v[218:221], v[116:119]
	v_mfma_f32_16x16x32_bf16 v[112:115], v[210:213], v[218:221], v[112:115]
	v_mfma_f32_16x16x32_bf16 v[100:103], v[202:205], v[226:229], v[100:103]
	v_mfma_f32_16x16x32_bf16 v[96:99], v[210:213], v[226:229], v[96:99]
	v_mfma_f32_16x16x32_bf16 v[84:87], v[202:205], v[234:237], v[84:87]
	v_mfma_f32_16x16x32_bf16 v[80:83], v[210:213], v[234:237], v[80:83]
	v_mfma_f32_16x16x32_bf16 v[68:71], v[202:205], v[242:245], v[68:71]
	v_mfma_f32_16x16x32_bf16 v[64:67], v[210:213], v[242:245], v[64:67]
	s_barrier
; template <class Epi, class Sched, class Hook = NoHook>
; __device__ __forceinline__ void gemm_phase_w(LAS unsigned char* lds, const Sched& S, const Epi& E, int wave_id, const Hook& HK = Hook()) {
;     ...
;         if constexpr (!SEG2) {
;             for (int tt = 0; tt < nt; tt += 2) {
;                 if constexpr (GATHER) { if (tt == nt - 2) {
;                     if (has_next) { gnxt_00 = S.grow_l(nxt, lds, nbuf, R0) + (unsigned)(C0 * 2); gnxt_01 = S.grow_l(nxt, lds, nbuf, R1) + (unsigned)(C1 * 2); gnxt_10 = S.grow_l(nxt, lds, nbuf, 128 + R0) + (unsigned)(C0 * 2); gnxt_11 = S.grow_l(nxt, lds, nbuf, 128 + R1) + (unsigned)(C1 * 2); }
;                     else { gnxt_00 = gcur_00; gnxt_01 = gcur_01; gnxt_10 = gcur_10; gnxt_11 = gcur_11; } } }
;                 PG_TRIP(tt, false, false, false);
;             }
	s_bitset1_b32 s22, 7
	s_add_i32 s71, s71, s22
	s_ashr_i32 s41, s71, 31
	s_add_u32 s40, s16, s71
	s_addc_u32 s41, s17, s41
	s_add_i32 s72, s72, s44
	v_lshl_add_u64 v[242:243], s[40:41], 0, v[136:137]
	s_mov_b32 m0, s72
	s_add_i32 s71, s71, 0x80000
	ds_read_b128 v[148:151], v179 offset:49152
	ds_read_b128 v[214:217], v179 offset:50176
	ds_read_b128 v[218:221], v179 offset:51200
	ds_read_b128 v[222:225], v179 offset:52224
	ds_read_b128 v[226:229], v179 offset:53248
	ds_read_b128 v[230:233], v179 offset:54272
	ds_read_b128 v[234:237], v179 offset:55296
	ds_read_b128 v[238:241], v179 offset:56320
	global_load_lds_dwordx4 v[242:243], off
	v_lshl_add_u64 v[242:243], s[40:41], 0, v[138:139]
	s_add_i32 m0, s72, 0x2000
	s_ashr_i32 s41, s71, 31
	s_add_u32 s40, s16, s71
	s_addc_u32 s41, s17, s41
	s_add_i32 s71, s73, s44
	global_load_lds_dwordx4 v[242:243], off
	v_lshl_add_u64 v[242:243], s[40:41], 0, v[136:137]
	s_mov_b32 m0, s71
	v_lshl_add_u64 v[146:147], s[14:15], 0, v[146:147]
	global_load_lds_dwordx4 v[242:243], off
	v_lshl_add_u64 v[242:243], s[40:41], 0, v[138:139]
	s_add_i32 m0, s71, 0x2000
	v_lshl_add_u64 v[146:147], v[146:147], 0, s[22:23]
	global_load_lds_dwordx4 v[242:243], off
	v_lshl_add_u64 v[242:243], s[14:15], 0, v[140:141]
	v_lshl_add_u64 v[242:243], v[242:243], 0, s[22:23]
	s_mov_b32 m0, s51
	s_nop 0
	global_load_lds_dwordx4 v[242:243], off
	s_mov_b32 m0, s61
	s_nop 0
	global_load_lds_dwordx4 v[146:147], off
	s_waitcnt vmcnt(8)
	s_waitcnt lgkmcnt(0)
	s_barrier
	s_waitcnt lgkmcnt(0)
	v_mfma_f32_16x16x32_bf16 v[60:63], v[182:185], v[148:151], v[60:63]
	v_mfma_f32_16x16x32_bf16 v[56:59], v[190:193], v[148:151], v[56:59]
	v_mfma_f32_16x16x32_bf16 v[44:47], v[182:185], v[218:221], v[44:47]
	v_mfma_f32_16x16x32_bf16 v[40:43], v[190:193], v[218:221], v[40:43]
	v_mfma_f32_16x16x32_bf16 v[28:31], v[182:185], v[226:229], v[28:31]
	v_mfma_f32_16x16x32_bf16 v[24:27], v[190:193], v[226:229], v[24:27]
	v_mfma_f32_16x16x32_bf16 v[12:15], v[182:185], v[234:237], v[12:15]
	v_mfma_f32_16x16x32_bf16 v[8:11], v[190:193], v[234:237], v[8:11]
	v_mfma_f32_16x16x32_bf16 v[60:63], v[186:189], v[214:217], v[60:63]
	v_mfma_f32_16x16x32_bf16 v[56:59], v[194:197], v[214:217], v[56:59]
	v_mfma_f32_16x16x32_bf16 v[44:47], v[186:189], v[222:225], v[44:47]
	v_mfma_f32_16x16x32_bf16 v[40:43], v[194:197], v[222:225], v[40:43]
	v_mfma_f32_16x16x32_bf16 v[28:31], v[186:189], v[230:233], v[28:31]
	v_mfma_f32_16x16x32_bf16 v[24:27], v[194:197], v[230:233], v[24:27]
	v_mfma_f32_16x16x32_bf16 v[12:15], v[186:189], v[238:241], v[12:15]
	v_mfma_f32_16x16x32_bf16 v[8:11], v[194:197], v[238:241], v[8:11]
	v_mfma_f32_16x16x32_bf16 v[52:55], v[198:201], v[148:151], v[52:55]
	v_mfma_f32_16x16x32_bf16 v[48:51], v[206:209], v[148:151], v[48:51]
	v_mfma_f32_16x16x32_bf16 v[36:39], v[198:201], v[218:221], v[36:39]
	v_mfma_f32_16x16x32_bf16 v[32:35], v[206:209], v[218:221], v[32:35]
	v_mfma_f32_16x16x32_bf16 v[20:23], v[198:201], v[226:229], v[20:23]
	v_mfma_f32_16x16x32_bf16 v[16:19], v[206:209], v[226:229], v[16:19]
	v_mfma_f32_16x16x32_bf16 v[4:7], v[198:201], v[234:237], v[4:7]
	v_mfma_f32_16x16x32_bf16 v[0:3], v[206:209], v[234:237], v[0:3]
	v_mfma_f32_16x16x32_bf16 v[52:55], v[202:205], v[214:217], v[52:55]
	v_mfma_f32_16x16x32_bf16 v[48:51], v[210:213], v[214:217], v[48:51]
	v_mfma_f32_16x16x32_bf16 v[36:39], v[202:205], v[222:225], v[36:39]
	v_mfma_f32_16x16x32_bf16 v[32:35], v[210:213], v[222:225], v[32:35]
	v_mfma_f32_16x16x32_bf16 v[20:23], v[202:205], v[230:233], v[20:23]
	v_mfma_f32_16x16x32_bf16 v[16:19], v[210:213], v[230:233], v[16:19]
	v_mfma_f32_16x16x32_bf16 v[4:7], v[202:205], v[238:241], v[4:7]
	v_mfma_f32_16x16x32_bf16 v[0:3], v[210:213], v[238:241], v[0:3]
	s_barrier
	s_add_i32 s69, s69, 2
	s_addk_i32 s70, 0x100
	s_add_u32 s38, s38, 0x100
	s_addc_u32 s39, s39, 0
	s_cmp_gt_u32 s69, 29
	s_cbranch_scc1 .LBB0_2414

.LBB0_2522:
	ds_read_b128 v[156:159], v153
	ds_read_b128 v[160:163], v153 offset:1024
	ds_read_b128 v[164:167], v153 offset:2048
	ds_read_b128 v[168:171], v153 offset:3072
	ds_read_b128 v[172:175], v154
	ds_read_b128 v[176:179], v154 offset:1024
	ds_read_b128 v[180:183], v154 offset:2048
	ds_read_b128 v[184:187], v154 offset:3072
	s_add_i32 s22, s53, s10
	s_add_u32 s58, s28, s22
	s_addc_u32 s59, s29, 0
	s_add_i32 m0, s31, 0xc000
	s_add_i32 s60, s31, 0xe000
	s_add_i32 s61, s10, 0xfffc0080
	s_cmp_eq_u32 s19, 12
	s_cselect_b32 s22, s50, s53
	s_cselect_b32 s23, s51, s56
	v_lshl_add_u64 v[220:221], s[58:59], 0, v[130:131]
	ds_read_b128 v[188:191], v155
	ds_read_b128 v[192:195], v155 offset:1024
	ds_read_b128 v[196:199], v155 offset:2048
	ds_read_b128 v[200:203], v155 offset:3072
	ds_read_b128 v[204:207], v155 offset:4096
	ds_read_b128 v[208:211], v155 offset:5120
	ds_read_b128 v[212:215], v155 offset:6144
	ds_read_b128 v[216:219], v155 offset:7168
	global_load_lds_dwordx4 v[220:221], off
	v_lshl_add_u64 v[220:221], s[58:59], 0, v[132:133]
	s_mov_b32 m0, s60
	s_nop 0
	global_load_lds_dwordx4 v[220:221], off
	s_waitcnt vmcnt(8)
	s_waitcnt lgkmcnt(0)
	s_barrier
	s_waitcnt lgkmcnt(0)
	v_mfma_f32_16x16x32_bf16 v[124:127], v[156:159], v[188:191], v[124:127]
	v_mfma_f32_16x16x32_bf16 v[120:123], v[164:167], v[188:191], v[120:123]
	v_mfma_f32_16x16x32_bf16 v[108:111], v[156:159], v[196:199], v[108:111]
	v_mfma_f32_16x16x32_bf16 v[104:107], v[164:167], v[196:199], v[104:107]
	v_mfma_f32_16x16x32_bf16 v[92:95], v[156:159], v[204:207], v[92:95]
	v_mfma_f32_16x16x32_bf16 v[88:91], v[164:167], v[204:207], v[88:91]
	v_mfma_f32_16x16x32_bf16 v[76:79], v[156:159], v[212:215], v[76:79]
	v_mfma_f32_16x16x32_bf16 v[72:75], v[164:167], v[212:215], v[72:75]
	v_mfma_f32_16x16x32_bf16 v[124:127], v[160:163], v[192:195], v[124:127]
	v_mfma_f32_16x16x32_bf16 v[120:123], v[168:171], v[192:195], v[120:123]
	v_mfma_f32_16x16x32_bf16 v[108:111], v[160:163], v[200:203], v[108:111]
	v_mfma_f32_16x16x32_bf16 v[104:107], v[168:171], v[200:203], v[104:107]
	v_mfma_f32_16x16x32_bf16 v[92:95], v[160:163], v[208:211], v[92:95]
	v_mfma_f32_16x16x32_bf16 v[88:91], v[168:171], v[208:211], v[88:91]
	v_mfma_f32_16x16x32_bf16 v[76:79], v[160:163], v[216:219], v[76:79]
	v_mfma_f32_16x16x32_bf16 v[72:75], v[168:171], v[216:219], v[72:75]
	v_mfma_f32_16x16x32_bf16 v[116:119], v[172:175], v[188:191], v[116:119]
	v_mfma_f32_16x16x32_bf16 v[112:115], v[180:183], v[188:191], v[112:115]
	v_mfma_f32_16x16x32_bf16 v[100:103], v[172:175], v[196:199], v[100:103]
	v_mfma_f32_16x16x32_bf16 v[96:99], v[180:183], v[196:199], v[96:99]
	v_mfma_f32_16x16x32_bf16 v[84:87], v[172:175], v[204:207], v[84:87]
	v_mfma_f32_16x16x32_bf16 v[80:83], v[180:183], v[204:207], v[80:83]
	v_mfma_f32_16x16x32_bf16 v[68:71], v[172:175], v[212:215], v[68:71]
	v_mfma_f32_16x16x32_bf16 v[64:67], v[180:183], v[212:215], v[64:67]
	v_mfma_f32_16x16x32_bf16 v[116:119], v[176:179], v[192:195], v[116:119]
	v_mfma_f32_16x16x32_bf16 v[112:115], v[184:187], v[192:195], v[112:115]
	v_mfma_f32_16x16x32_bf16 v[100:103], v[176:179], v[200:203], v[100:103]
	v_mfma_f32_16x16x32_bf16 v[96:99], v[184:187], v[200:203], v[96:99]
	v_mfma_f32_16x16x32_bf16 v[84:87], v[176:179], v[208:211], v[84:87]
	v_mfma_f32_16x16x32_bf16 v[80:83], v[184:187], v[208:211], v[80:83]
	v_mfma_f32_16x16x32_bf16 v[68:71], v[176:179], v[216:219], v[68:71]
	v_mfma_f32_16x16x32_bf16 v[64:67], v[184:187], v[216:219], v[64:67]
	s_barrier
	s_cselect_b32 s60, 0, s61
	s_add_i32 s58, s60, s23
	s_ashr_i32 s59, s58, 31
	s_add_u32 s58, s8, s58
	s_addc_u32 s59, s9, s59
	s_add_i32 s61, s42, s26
	v_lshl_add_u64 v[220:221], s[58:59], 0, v[130:131]
	s_mov_b32 m0, s61
	ds_read_b128 v[188:191], v155 offset:16384
	ds_read_b128 v[192:195], v155 offset:17408
	ds_read_b128 v[196:199], v155 offset:18432
	ds_read_b128 v[200:203], v155 offset:19456
	ds_read_b128 v[204:207], v155 offset:20480
	ds_read_b128 v[208:211], v155 offset:21504
	ds_read_b128 v[212:215], v155 offset:22528
	ds_read_b128 v[216:219], v155 offset:23552
	global_load_lds_dwordx4 v[220:221], off
	s_add_i32 m0, s61, 0x2000
	s_add_i32 s61, s23, 0x40000
	v_lshl_add_u64 v[220:221], s[58:59], 0, v[132:133]
	s_add_i32 s58, s61, s60
	s_ashr_i32 s59, s58, 31
	s_add_u32 s58, s8, s58
	s_addc_u32 s59, s9, s59
	s_add_i32 s62, s43, s26
	global_load_lds_dwordx4 v[220:221], off
	v_lshl_add_u64 v[220:221], s[58:59], 0, v[130:131]
	s_mov_b32 m0, s62
	s_nop 0
	global_load_lds_dwordx4 v[220:221], off
	s_add_i32 m0, s62, 0x2000
	s_add_i32 s62, s60, s22
	v_lshl_add_u64 v[220:221], s[58:59], 0, v[132:133]
	s_add_u32 s58, s28, s62
	s_addc_u32 s59, s29, 0
	global_load_lds_dwordx4 v[220:221], off
	v_lshl_add_u64 v[220:221], s[58:59], 0, v[130:131]
	s_mov_b32 m0, s31
	s_nop 0
	global_load_lds_dwordx4 v[220:221], off
	v_lshl_add_u64 v[220:221], s[58:59], 0, v[132:133]
	s_mov_b32 m0, s33
	s_nop 0
	global_load_lds_dwordx4 v[220:221], off
	s_waitcnt vmcnt(8)
	s_waitcnt lgkmcnt(0)
	s_barrier
	s_waitcnt lgkmcnt(0)
	v_mfma_f32_16x16x32_bf16 v[60:63], v[156:159], v[188:191], v[60:63]
	v_mfma_f32_16x16x32_bf16 v[56:59], v[164:167], v[188:191], v[56:59]
	v_mfma_f32_16x16x32_bf16 v[44:47], v[156:159], v[196:199], v[44:47]
	v_mfma_f32_16x16x32_bf16 v[40:43], v[164:167], v[196:199], v[40:43]
	v_mfma_f32_16x16x32_bf16 v[28:31], v[156:159], v[204:207], v[28:31]
	v_mfma_f32_16x16x32_bf16 v[24:27], v[164:167], v[204:207], v[24:27]
	v_mfma_f32_16x16x32_bf16 v[12:15], v[156:159], v[212:215], v[12:15]
	v_mfma_f32_16x16x32_bf16 v[8:11], v[164:167], v[212:215], v[8:11]
	v_mfma_f32_16x16x32_bf16 v[60:63], v[160:163], v[192:195], v[60:63]
	v_mfma_f32_16x16x32_bf16 v[56:59], v[168:171], v[192:195], v[56:59]
	v_mfma_f32_16x16x32_bf16 v[44:47], v[160:163], v[200:203], v[44:47]
	v_mfma_f32_16x16x32_bf16 v[40:43], v[168:171], v[200:203], v[40:43]
	v_mfma_f32_16x16x32_bf16 v[28:31], v[160:163], v[208:211], v[28:31]
	v_mfma_f32_16x16x32_bf16 v[24:27], v[168:171], v[208:211], v[24:27]
	v_mfma_f32_16x16x32_bf16 v[12:15], v[160:163], v[216:219], v[12:15]
	v_mfma_f32_16x16x32_bf16 v[8:11], v[168:171], v[216:219], v[8:11]
	v_mfma_f32_16x16x32_bf16 v[52:55], v[172:175], v[188:191], v[52:55]
	v_mfma_f32_16x16x32_bf16 v[48:51], v[180:183], v[188:191], v[48:51]
	v_mfma_f32_16x16x32_bf16 v[36:39], v[172:175], v[196:199], v[36:39]
	v_mfma_f32_16x16x32_bf16 v[32:35], v[180:183], v[196:199], v[32:35]
	v_mfma_f32_16x16x32_bf16 v[20:23], v[172:175], v[204:207], v[20:23]
	v_mfma_f32_16x16x32_bf16 v[16:19], v[180:183], v[204:207], v[16:19]
	v_mfma_f32_16x16x32_bf16 v[4:7], v[172:175], v[212:215], v[4:7]
	v_mfma_f32_16x16x32_bf16 v[0:3], v[180:183], v[212:215], v[0:3]
	v_mfma_f32_16x16x32_bf16 v[52:55], v[176:179], v[192:195], v[52:55]
	v_mfma_f32_16x16x32_bf16 v[48:51], v[184:187], v[192:195], v[48:51]
	v_mfma_f32_16x16x32_bf16 v[36:39], v[176:179], v[200:203], v[36:39]
	v_mfma_f32_16x16x32_bf16 v[32:35], v[184:187], v[200:203], v[32:35]
	v_mfma_f32_16x16x32_bf16 v[20:23], v[176:179], v[208:211], v[20:23]
	v_mfma_f32_16x16x32_bf16 v[16:19], v[184:187], v[208:211], v[16:19]
	v_mfma_f32_16x16x32_bf16 v[4:7], v[176:179], v[216:219], v[4:7]
	v_mfma_f32_16x16x32_bf16 v[0:3], v[184:187], v[216:219], v[0:3]
	s_barrier
	s_add_i32 s63, 0, 0x18000
	s_add_i32 s64, 0, 0x1c000
	v_add_u32_e32 v168, s63, v137
	v_add_u32_e32 v184, s64, v137
	ds_read_b128 v[156:159], v168
	ds_read_b128 v[160:163], v168 offset:1024
	ds_read_b128 v[164:167], v168 offset:2048
	ds_read_b128 v[168:171], v168 offset:3072
	ds_read_b128 v[172:175], v184
	ds_read_b128 v[176:179], v184 offset:1024
	ds_read_b128 v[180:183], v184 offset:2048
	ds_read_b128 v[184:187], v184 offset:3072
	s_add_i32 s62, s62, 0x40000
	s_add_u32 s58, s28, s62
	s_addc_u32 s59, s29, 0
	s_mov_b32 m0, s34
	v_lshl_add_u64 v[220:221], s[58:59], 0, v[130:131]
	ds_read_b128 v[188:191], v155 offset:32768
	ds_read_b128 v[192:195], v155 offset:33792
	ds_read_b128 v[196:199], v155 offset:34816
	ds_read_b128 v[200:203], v155 offset:35840
	ds_read_b128 v[204:207], v155 offset:36864
	ds_read_b128 v[208:211], v155 offset:37888
	ds_read_b128 v[212:215], v155 offset:38912
	ds_read_b128 v[216:219], v155 offset:39936
	global_load_lds_dwordx4 v[220:221], off
	v_lshl_add_u64 v[220:221], s[58:59], 0, v[132:133]
	s_mov_b32 m0, s35
	s_nop 0
	global_load_lds_dwordx4 v[220:221], off
	s_waitcnt vmcnt(8)
	s_waitcnt lgkmcnt(0)
	s_barrier
	s_waitcnt lgkmcnt(0)
	v_mfma_f32_16x16x32_bf16 v[124:127], v[156:159], v[188:191], v[124:127]
	v_mfma_f32_16x16x32_bf16 v[120:123], v[164:167], v[188:191], v[120:123]
	v_mfma_f32_16x16x32_bf16 v[108:111], v[156:159], v[196:199], v[108:111]
	v_mfma_f32_16x16x32_bf16 v[104:107], v[164:167], v[196:199], v[104:107]
	v_mfma_f32_16x16x32_bf16 v[92:95], v[156:159], v[204:207], v[92:95]
	v_mfma_f32_16x16x32_bf16 v[88:91], v[164:167], v[204:207], v[88:91]
	v_mfma_f32_16x16x32_bf16 v[76:79], v[156:159], v[212:215], v[76:79]
	v_mfma_f32_16x16x32_bf16 v[72:75], v[164:167], v[212:215], v[72:75]
	v_mfma_f32_16x16x32_bf16 v[124:127], v[160:163], v[192:195], v[124:127]
	v_mfma_f32_16x16x32_bf16 v[120:123], v[168:171], v[192:195], v[120:123]
	v_mfma_f32_16x16x32_bf16 v[108:111], v[160:163], v[200:203], v[108:111]
	v_mfma_f32_16x16x32_bf16 v[104:107], v[168:171], v[200:203], v[104:107]
	v_mfma_f32_16x16x32_bf16 v[92:95], v[160:163], v[208:211], v[92:95]
	v_mfma_f32_16x16x32_bf16 v[88:91], v[168:171], v[208:211], v[88:91]
	v_mfma_f32_16x16x32_bf16 v[76:79], v[160:163], v[216:219], v[76:79]
	v_mfma_f32_16x16x32_bf16 v[72:75], v[168:171], v[216:219], v[72:75]
	v_mfma_f32_16x16x32_bf16 v[116:119], v[172:175], v[188:191], v[116:119]
	v_mfma_f32_16x16x32_bf16 v[112:115], v[180:183], v[188:191], v[112:115]
	v_mfma_f32_16x16x32_bf16 v[100:103], v[172:175], v[196:199], v[100:103]
	v_mfma_f32_16x16x32_bf16 v[96:99], v[180:183], v[196:199], v[96:99]
	v_mfma_f32_16x16x32_bf16 v[84:87], v[172:175], v[204:207], v[84:87]
	v_mfma_f32_16x16x32_bf16 v[80:83], v[180:183], v[204:207], v[80:83]
	v_mfma_f32_16x16x32_bf16 v[68:71], v[172:175], v[212:215], v[68:71]
	v_mfma_f32_16x16x32_bf16 v[64:67], v[180:183], v[212:215], v[64:67]
	v_mfma_f32_16x16x32_bf16 v[116:119], v[176:179], v[192:195], v[116:119]
	v_mfma_f32_16x16x32_bf16 v[112:115], v[184:187], v[192:195], v[112:115]
	v_mfma_f32_16x16x32_bf16 v[100:103], v[176:179], v[200:203], v[100:103]
	v_mfma_f32_16x16x32_bf16 v[96:99], v[184:187], v[200:203], v[96:99]
	v_mfma_f32_16x16x32_bf16 v[84:87], v[176:179], v[208:211], v[84:87]
	v_mfma_f32_16x16x32_bf16 v[80:83], v[184:187], v[208:211], v[80:83]
	v_mfma_f32_16x16x32_bf16 v[68:71], v[176:179], v[216:219], v[68:71]
	v_mfma_f32_16x16x32_bf16 v[64:67], v[184:187], v[216:219], v[64:67]
	s_barrier
; #define PG_BAR __builtin_amdgcn_s_barrier()
; template <class Epi, class Sched, class Hook = NoHook>
; __device__ __forceinline__ void gemm_phase_w(LAS unsigned char* lds, const Sched& S, const Epi& E, int wave_id, const Hook& HK = Hook()) {
;     ...
;         if constexpr (!SEG2) {
;             for (int tt = 0; tt < nt; tt += 2) {
;                 if constexpr (GATHER) { if (tt == nt - 2) {
;                     if (has_next) { gnxt_00 = S.grow_l(nxt, lds, nbuf, R0) + (unsigned)(C0 * 2); gnxt_01 = S.grow_l(nxt, lds, nbuf, R1) + (unsigned)(C1 * 2); gnxt_10 = S.grow_l(nxt, lds, nbuf, 128 + R0) + (unsigned)(C0 * 2); gnxt_11 = S.grow_l(nxt, lds, nbuf, 128 + R1) + (unsigned)(C1 * 2); }
;                     else { gnxt_00 = gcur_00; gnxt_01 = gcur_01; gnxt_10 = gcur_10; gnxt_11 = gcur_11; } } }
;                 PG_TRIP(tt, false, false, false);
;             }
;         } else {
;             for (int tt = 0; tt < nt - 4; tt += 2) PG_TRIP(tt, false, false, false);
;             PG_TRIP(nt - 4, false, true, false);
;             PG_TRIP(nt - 2, true, false, true);
;         }
;     ...
;         if (wr == 0) PG_BAR;
	s_bitset1_b32 s60, 7
	s_add_i32 s23, s60, s23
	s_ashr_i32 s59, s23, 31
	s_add_u32 s58, s8, s23
	s_addc_u32 s59, s9, s59
	s_add_i32 s23, s63, s26
	v_lshl_add_u64 v[220:221], s[58:59], 0, v[130:131]
	s_mov_b32 m0, s23
	ds_read_b128 v[188:191], v155 offset:49152
	ds_read_b128 v[192:195], v155 offset:50176
	ds_read_b128 v[196:199], v155 offset:51200
	ds_read_b128 v[200:203], v155 offset:52224
	ds_read_b128 v[204:207], v155 offset:53248
	ds_read_b128 v[208:211], v155 offset:54272
	ds_read_b128 v[212:215], v155 offset:55296
	ds_read_b128 v[216:219], v155 offset:56320
	global_load_lds_dwordx4 v[220:221], off
	s_add_i32 m0, s23, 0x2000
	s_add_i32 s23, s60, s61
	v_lshl_add_u64 v[220:221], s[58:59], 0, v[132:133]
	s_ashr_i32 s59, s23, 31
	s_add_u32 s58, s8, s23
	s_addc_u32 s59, s9, s59
	s_add_i32 s23, s64, s26
	global_load_lds_dwordx4 v[220:221], off
	v_lshl_add_u64 v[220:221], s[58:59], 0, v[130:131]
	s_mov_b32 m0, s23
	s_add_i32 s60, s60, s22
	global_load_lds_dwordx4 v[220:221], off
	s_add_i32 m0, s23, 0x2000
	s_add_u32 s22, s28, s60
	v_lshl_add_u64 v[220:221], s[58:59], 0, v[132:133]
	s_addc_u32 s23, s29, 0
	global_load_lds_dwordx4 v[220:221], off
	v_lshl_add_u64 v[220:221], s[22:23], 0, v[130:131]
	s_mov_b32 m0, s37
	s_nop 0
	global_load_lds_dwordx4 v[220:221], off
	v_lshl_add_u64 v[220:221], s[22:23], 0, v[132:133]
	s_mov_b32 m0, s38
	s_nop 0
	global_load_lds_dwordx4 v[220:221], off
	s_waitcnt vmcnt(8)
	s_waitcnt lgkmcnt(0)
	s_barrier
	s_waitcnt lgkmcnt(0)
	v_mfma_f32_16x16x32_bf16 v[60:63], v[156:159], v[188:191], v[60:63]
	v_mfma_f32_16x16x32_bf16 v[56:59], v[164:167], v[188:191], v[56:59]
	v_mfma_f32_16x16x32_bf16 v[44:47], v[156:159], v[196:199], v[44:47]
	v_mfma_f32_16x16x32_bf16 v[40:43], v[164:167], v[196:199], v[40:43]
	v_mfma_f32_16x16x32_bf16 v[28:31], v[156:159], v[204:207], v[28:31]
	v_mfma_f32_16x16x32_bf16 v[24:27], v[164:167], v[204:207], v[24:27]
	v_mfma_f32_16x16x32_bf16 v[12:15], v[156:159], v[212:215], v[12:15]
	v_mfma_f32_16x16x32_bf16 v[8:11], v[164:167], v[212:215], v[8:11]
	v_mfma_f32_16x16x32_bf16 v[60:63], v[160:163], v[192:195], v[60:63]
	v_mfma_f32_16x16x32_bf16 v[56:59], v[168:171], v[192:195], v[56:59]
	v_mfma_f32_16x16x32_bf16 v[44:47], v[160:163], v[200:203], v[44:47]
	v_mfma_f32_16x16x32_bf16 v[40:43], v[168:171], v[200:203], v[40:43]
	v_mfma_f32_16x16x32_bf16 v[28:31], v[160:163], v[208:211], v[28:31]
	v_mfma_f32_16x16x32_bf16 v[24:27], v[168:171], v[208:211], v[24:27]
	v_mfma_f32_16x16x32_bf16 v[12:15], v[160:163], v[216:219], v[12:15]
	v_mfma_f32_16x16x32_bf16 v[8:11], v[168:171], v[216:219], v[8:11]
	v_mfma_f32_16x16x32_bf16 v[52:55], v[172:175], v[188:191], v[52:55]
	v_mfma_f32_16x16x32_bf16 v[48:51], v[180:183], v[188:191], v[48:51]
	v_mfma_f32_16x16x32_bf16 v[36:39], v[172:175], v[196:199], v[36:39]
	v_mfma_f32_16x16x32_bf16 v[32:35], v[180:183], v[196:199], v[32:35]
	v_mfma_f32_16x16x32_bf16 v[20:23], v[172:175], v[204:207], v[20:23]
	v_mfma_f32_16x16x32_bf16 v[16:19], v[180:183], v[204:207], v[16:19]
	v_mfma_f32_16x16x32_bf16 v[4:7], v[172:175], v[212:215], v[4:7]
	v_mfma_f32_16x16x32_bf16 v[0:3], v[180:183], v[212:215], v[0:3]
	v_mfma_f32_16x16x32_bf16 v[52:55], v[176:179], v[192:195], v[52:55]
	v_mfma_f32_16x16x32_bf16 v[48:51], v[184:187], v[192:195], v[48:51]
	v_mfma_f32_16x16x32_bf16 v[36:39], v[176:179], v[200:203], v[36:39]
	v_mfma_f32_16x16x32_bf16 v[32:35], v[184:187], v[200:203], v[32:35]
	v_mfma_f32_16x16x32_bf16 v[20:23], v[176:179], v[208:211], v[20:23]
	v_mfma_f32_16x16x32_bf16 v[16:19], v[184:187], v[208:211], v[16:19]
	v_mfma_f32_16x16x32_bf16 v[4:7], v[176:179], v[216:219], v[4:7]
	v_mfma_f32_16x16x32_bf16 v[0:3], v[184:187], v[216:219], v[0:3]
	s_barrier
	s_addk_i32 s10, 0x100
	s_add_i32 s19, s19, 2
	s_cmp_gt_u32 s19, 13
	s_cbranch_scc0 .LBB0_2522
	s_and_b64 vcc, exec, s[6:7]
	s_cbranch_vccz .LBB0_2525
	s_barrier
